# back-edge rotation extended to the in-projection, GLU, out-projection (both halves) and the two split-K MoE K-loops
# baseline (speedup 1.0000x reference)
.Lrot_ip:
	ds_read_b64_tr_b16 v[174:175], v204
	ds_read_b64_tr_b16 v[176:177], v204 offset:2048
	ds_read_b64_tr_b16 v[178:179], v208
	ds_read_b64_tr_b16 v[180:181], v208 offset:2048
	ds_read_b128 v[182:185], v206
	ds_read_b128 v[186:189], v206 offset:2048
	ds_read_b64_tr_b16 v[190:191], v212
	ds_read_b64_tr_b16 v[192:193], v212 offset:2048
	v_add_u32_e32 v214, s9, v146
	ds_read_b64_tr_b16 v[194:195], v214
	ds_read_b64_tr_b16 v[196:197], v214 offset:2048
	ds_read_b128 v[198:201], v206 offset:4096
	s_waitcnt lgkmcnt(6)
	v_mfma_f32_16x16x32_bf16 v[62:65], v[174:177], v[182:185], v[62:65]
	v_add_u32_e32 v202, 0xfff40000, v173
	s_add_i32 s9, s2, s7
	s_mov_b32 s14, m0
	s_mov_b32 m0, s9
	s_nop 0
	global_load_lds_dwordx4 v202, s[16:17]
	s_mov_b32 m0, s14
	v_mfma_f32_16x16x32_bf16 v[46:49], v[178:181], v[182:185], v[46:49]
	s_waitcnt lgkmcnt(3)
	v_mfma_f32_16x16x32_bf16 v[38:41], v[190:193], v[182:185], v[38:41]
	s_waitcnt lgkmcnt(1)
	v_mfma_f32_16x16x32_bf16 v[34:37], v[194:197], v[182:185], v[34:37]
	v_mfma_f32_16x16x32_bf16 v[30:33], v[174:177], v[186:189], v[30:33]
	ds_read_b128 v[182:185], v206 offset:6144
	v_add_u32_e32 v202, 0xfff80000, v173
	s_add_i32 s14, s9, 0x2000
	v_mfma_f32_16x16x32_bf16 v[26:29], v[178:181], v[186:189], v[26:29]
	s_mov_b32 s30, m0
	s_mov_b32 m0, s14
	s_nop 0
	global_load_lds_dwordx4 v202, s[16:17]
	s_mov_b32 m0, s30
	v_mfma_f32_16x16x32_bf16 v[22:25], v[190:193], v[186:189], v[22:25]
	v_mfma_f32_16x16x32_bf16 v[18:21], v[194:197], v[186:189], v[18:21]
	s_waitcnt lgkmcnt(1)
	v_mfma_f32_16x16x32_bf16 v[66:69], v[174:177], v[198:201], v[66:69]
	ds_read_b128 v[186:189], v206 offset:8192
	v_add_u32_e32 v202, 0xfffc0000, v173
	s_add_i32 s14, s9, 0x4000
	v_mfma_f32_16x16x32_bf16 v[78:81], v[178:181], v[198:201], v[78:81]
	s_mov_b32 s30, m0
	s_mov_b32 m0, s14
	s_nop 0
	global_load_lds_dwordx4 v202, s[16:17]
	s_mov_b32 m0, s30
	v_mfma_f32_16x16x32_bf16 v[90:93], v[190:193], v[198:201], v[90:93]
	v_mfma_f32_16x16x32_bf16 v[94:97], v[194:197], v[198:201], v[94:97]
	s_waitcnt lgkmcnt(1)
	v_mfma_f32_16x16x32_bf16 v[114:117], v[174:177], v[182:185], v[114:117]
	ds_read_b128 v[198:201], v206 offset:10240
	s_addk_i32 s9, 0x6000
	s_mov_b32 s14, m0
	s_mov_b32 m0, s9
	s_nop 0
	global_load_lds_dwordx4 v173, s[16:17]
	s_mov_b32 m0, s14
	v_mfma_f32_16x16x32_bf16 v[122:125], v[178:181], v[182:185], v[122:125]
	v_mfma_f32_16x16x32_bf16 v[138:141], v[190:193], v[182:185], v[138:141]
	v_mfma_f32_16x16x32_bf16 v[142:145], v[194:197], v[182:185], v[142:145]
	ds_read_b128 v[182:185], v206 offset:12288
	ds_read_b64_tr_b16 v[202:203], v204 offset:16384
	ds_read_b64_tr_b16 v[204:205], v204 offset:18432
	s_waitcnt lgkmcnt(4)
	v_mfma_f32_16x16x32_bf16 v[118:121], v[174:177], v[186:189], v[118:121]
	v_mfma_f32_16x16x32_bf16 v[126:129], v[178:181], v[186:189], v[126:129]
	v_mfma_f32_16x16x32_bf16 v[134:137], v[190:193], v[186:189], v[134:137]
	v_mfma_f32_16x16x32_bf16 v[130:133], v[194:197], v[186:189], v[130:133]
	ds_read_b128 v[186:189], v206 offset:14336
	ds_read_b64_tr_b16 v[206:207], v208 offset:16384
	ds_read_b64_tr_b16 v[208:209], v208 offset:18432
	s_waitcnt lgkmcnt(6)
	v_mfma_f32_16x16x32_bf16 v[98:101], v[174:177], v[198:201], v[98:101]
	v_mfma_f32_16x16x32_bf16 v[102:105], v[178:181], v[198:201], v[102:105]
	v_mfma_f32_16x16x32_bf16 v[110:113], v[190:193], v[198:201], v[110:113]
	v_mfma_f32_16x16x32_bf16 v[106:109], v[194:197], v[198:201], v[106:109]
	v_add_u32_e32 v215, s8, v171
	ds_read_b128 v[198:201], v215
	ds_read_b64_tr_b16 v[210:211], v212 offset:16384
	ds_read_b64_tr_b16 v[212:213], v212 offset:18432
	s_waitcnt lgkmcnt(8)
	v_mfma_f32_16x16x32_bf16 v[70:73], v[174:177], v[182:185], v[70:73]
	v_mfma_f32_16x16x32_bf16 v[82:85], v[178:181], v[182:185], v[82:85]
	v_mfma_f32_16x16x32_bf16 v[86:89], v[190:193], v[182:185], v[86:89]
	v_mfma_f32_16x16x32_bf16 v[74:77], v[194:197], v[182:185], v[74:77]
	s_waitcnt lgkmcnt(5)
	v_mfma_f32_16x16x32_bf16 v[42:45], v[174:177], v[186:189], v[42:45]
	ds_read_b128 v[174:177], v215 offset:2048
	s_and_b32 s8, s6, 0x8000
	v_mfma_f32_16x16x32_bf16 v[54:57], v[178:181], v[186:189], v[54:57]
	ds_read_b64_tr_b16 v[178:179], v214 offset:16384
	ds_read_b64_tr_b16 v[180:181], v214 offset:18432
	v_mfma_f32_16x16x32_bf16 v[58:61], v[190:193], v[186:189], v[58:61]
	v_mfma_f32_16x16x32_bf16 v[50:53], v[194:197], v[186:189], v[50:53]
	s_waitcnt lgkmcnt(5)
	v_mfma_f32_16x16x32_bf16 v[62:65], v[202:205], v[198:201], v[62:65]
	ds_read_b128 v[182:185], v215 offset:4096
	s_add_u32 s14, s3, s0
	s_addc_u32 s30, s4, s1
	v_mfma_f32_16x16x32_bf16 v[46:49], v[206:209], v[198:201], v[46:49]
	s_waitcnt vmcnt(7)
	v_add_u32_e32 v190, s8, v172
	s_add_u32 s8, s14, 0x100000
	s_waitcnt lgkmcnt(4)
	v_mfma_f32_16x16x32_bf16 v[38:41], v[210:213], v[198:201], v[38:41]
	ds_write_b128 v190, v[14:17]
	s_addc_u32 s9, s30, 0
	global_load_dwordx4 v[14:17], v162, s[8:9]
	s_waitcnt lgkmcnt(2)
	v_mfma_f32_16x16x32_bf16 v[34:37], v[178:181], v[198:201], v[34:37]
	v_mfma_f32_16x16x32_bf16 v[30:33], v[202:205], v[174:177], v[30:33]
	ds_read_b128 v[186:189], v215 offset:6144
	s_waitcnt vmcnt(7)
	s_add_u32 s8, s14, 0x120000
	v_mfma_f32_16x16x32_bf16 v[26:29], v[206:209], v[174:177], v[26:29]
	ds_write_b128 v190, v[10:13] offset:8192
	s_addc_u32 s9, s30, 0
	global_load_dwordx4 v[10:13], v162, s[8:9]
	v_mfma_f32_16x16x32_bf16 v[22:25], v[210:213], v[174:177], v[22:25]
	v_mfma_f32_16x16x32_bf16 v[18:21], v[178:181], v[174:177], v[18:21]
	s_waitcnt lgkmcnt(3)
	v_mfma_f32_16x16x32_bf16 v[66:69], v[202:205], v[182:185], v[66:69]
	ds_read_b128 v[174:177], v215 offset:8192
	s_waitcnt vmcnt(7)
	s_add_u32 s8, s14, 0x140000
	v_mfma_f32_16x16x32_bf16 v[78:81], v[206:209], v[182:185], v[78:81]
	ds_write_b128 v190, v[6:9] offset:16384
	s_addc_u32 s9, s30, 0
	global_load_dwordx4 v[6:9], v162, s[8:9]
	v_mfma_f32_16x16x32_bf16 v[90:93], v[210:213], v[182:185], v[90:93]
	v_mfma_f32_16x16x32_bf16 v[94:97], v[178:181], v[182:185], v[94:97]
	s_waitcnt lgkmcnt(3)
	v_mfma_f32_16x16x32_bf16 v[114:117], v[202:205], v[186:189], v[114:117]
	ds_read_b128 v[182:185], v215 offset:10240
	s_waitcnt vmcnt(7)
	s_add_u32 s8, s14, 0x160000
	v_mfma_f32_16x16x32_bf16 v[122:125], v[206:209], v[186:189], v[122:125]
	ds_write_b128 v190, v[2:5] offset:24576
	s_addc_u32 s9, s30, 0
	global_load_dwordx4 v[2:5], v162, s[8:9]
	v_mfma_f32_16x16x32_bf16 v[138:141], v[210:213], v[186:189], v[138:141]
	v_mfma_f32_16x16x32_bf16 v[142:145], v[178:181], v[186:189], v[142:145]
	s_waitcnt lgkmcnt(3)
	v_mfma_f32_16x16x32_bf16 v[118:121], v[202:205], v[174:177], v[118:121]
	ds_read_b128 v[186:189], v215 offset:12288
	v_mfma_f32_16x16x32_bf16 v[126:129], v[206:209], v[174:177], v[126:129]
	v_mfma_f32_16x16x32_bf16 v[134:137], v[210:213], v[174:177], v[134:137]
	v_mfma_f32_16x16x32_bf16 v[130:133], v[178:181], v[174:177], v[130:133]
	s_waitcnt lgkmcnt(2)
	v_mfma_f32_16x16x32_bf16 v[98:101], v[202:205], v[182:185], v[98:101]
	ds_read_b128 v[174:177], v215 offset:14336
	v_mfma_f32_16x16x32_bf16 v[102:105], v[206:209], v[182:185], v[102:105]
	v_mfma_f32_16x16x32_bf16 v[110:113], v[210:213], v[182:185], v[110:113]
	v_mfma_f32_16x16x32_bf16 v[106:109], v[178:181], v[182:185], v[106:109]
	s_waitcnt lgkmcnt(1)
	v_mfma_f32_16x16x32_bf16 v[70:73], v[202:205], v[186:189], v[70:73]
	v_mfma_f32_16x16x32_bf16 v[82:85], v[206:209], v[186:189], v[82:85]
	v_mfma_f32_16x16x32_bf16 v[86:89], v[210:213], v[186:189], v[86:89]
	v_mfma_f32_16x16x32_bf16 v[74:77], v[178:181], v[186:189], v[74:77]
	s_waitcnt lgkmcnt(0)
	v_mfma_f32_16x16x32_bf16 v[42:45], v[202:205], v[174:177], v[42:45]
	v_mfma_f32_16x16x32_bf16 v[54:57], v[206:209], v[174:177], v[54:57]
	v_mfma_f32_16x16x32_bf16 v[58:61], v[210:213], v[174:177], v[58:61]
	v_mfma_f32_16x16x32_bf16 v[50:53], v[178:181], v[174:177], v[50:53]
	s_add_i32 s8, s5, 0x8000
	s_cmp_lg_u32 s5, 0x10000
	s_cselect_b32 s5, s8, 0
	s_add_i32 s8, s7, 0x8000
	s_cmp_lg_u32 s7, 0x10000
	s_cselect_b32 s7, s8, 0
	s_add_u32 s0, s0, 0x80000
	s_addc_u32 s1, s1, 0
	s_add_i32 s6, s6, 0x8000
	v_add_u32_e32 v173, 0x80, v173
	s_add_i32 s9, s6, 0xffff8000
	s_and_b32 s9, s9, 0x8000
	s_add_i32 s9, s9, 0
	s_add_i32 s8, s5, 0
	s_add_i32 s9, s9, 0x18000
	v_add_u32_e32 v204, s9, v153
	v_add_u32_e32 v206, s8, v169
	v_add_u32_e32 v212, s9, v151
	v_add_u32_e32 v208, s9, v152
	s_waitcnt lgkmcnt(0)
	s_barrier
	s_cmp_lg_u32 s0, 0xf00000
	s_cbranch_scc1 .Lrot_ip
	s_add_i32 s0, 0, 0x18000
	v_add_u32_e32 v202, s0, v153
	v_add_u32_e32 v169, 0, v169
	v_add_u32_e32 v210, s0, v151
	v_add_u32_e32 v212, s0, v146
	ds_read_b64_tr_b16 v[172:173], v202
	ds_read_b64_tr_b16 v[174:175], v202 offset:2048
	v_add_u32_e32 v206, s0, v152
	ds_read_b128 v[176:179], v169
	ds_read_b64_tr_b16 v[180:181], v206
	ds_read_b64_tr_b16 v[182:183], v206 offset:2048
	ds_read_b128 v[184:187], v169 offset:2048
	ds_read_b64_tr_b16 v[188:189], v210
	ds_read_b64_tr_b16 v[190:191], v210 offset:2048
	ds_read_b64_tr_b16 v[192:193], v212
	ds_read_b64_tr_b16 v[194:195], v212 offset:2048
	s_waitcnt lgkmcnt(7)
	v_mfma_f32_16x16x32_bf16 v[62:65], v[172:175], v[176:179], v[62:65]
	ds_read_b128 v[196:199], v169 offset:4096
	s_waitcnt lgkmcnt(6)
	v_mfma_f32_16x16x32_bf16 v[46:49], v[180:183], v[176:179], v[46:49]
	s_waitcnt lgkmcnt(3)
	v_mfma_f32_16x16x32_bf16 v[38:41], v[188:191], v[176:179], v[38:41]
	s_waitcnt lgkmcnt(1)
	v_mfma_f32_16x16x32_bf16 v[34:37], v[192:195], v[176:179], v[34:37]
	v_mfma_f32_16x16x32_bf16 v[30:33], v[172:175], v[184:187], v[30:33]
	ds_read_b128 v[176:179], v169 offset:6144
	v_mfma_f32_16x16x32_bf16 v[26:29], v[180:183], v[184:187], v[26:29]
	v_mfma_f32_16x16x32_bf16 v[22:25], v[188:191], v[184:187], v[22:25]
	v_mfma_f32_16x16x32_bf16 v[18:21], v[192:195], v[184:187], v[18:21]
	s_waitcnt lgkmcnt(1)
	v_mfma_f32_16x16x32_bf16 v[66:69], v[172:175], v[196:199], v[66:69]
	ds_read_b128 v[184:187], v169 offset:8192
	v_mfma_f32_16x16x32_bf16 v[78:81], v[180:183], v[196:199], v[78:81]
	v_mfma_f32_16x16x32_bf16 v[90:93], v[188:191], v[196:199], v[90:93]
	v_mfma_f32_16x16x32_bf16 v[94:97], v[192:195], v[196:199], v[94:97]
	s_waitcnt lgkmcnt(1)
	v_mfma_f32_16x16x32_bf16 v[114:117], v[172:175], v[176:179], v[114:117]
	ds_read_b128 v[196:199], v169 offset:10240
	v_mfma_f32_16x16x32_bf16 v[122:125], v[180:183], v[176:179], v[122:125]
	v_mfma_f32_16x16x32_bf16 v[138:141], v[188:191], v[176:179], v[138:141]
	v_mfma_f32_16x16x32_bf16 v[142:145], v[192:195], v[176:179], v[142:145]
	ds_read_b128 v[176:179], v169 offset:12288
	ds_read_b64_tr_b16 v[200:201], v202 offset:16384
	ds_read_b64_tr_b16 v[202:203], v202 offset:18432
	s_waitcnt lgkmcnt(4)
	v_mfma_f32_16x16x32_bf16 v[118:121], v[172:175], v[184:187], v[118:121]
	v_mfma_f32_16x16x32_bf16 v[126:129], v[180:183], v[184:187], v[126:129]
	v_mfma_f32_16x16x32_bf16 v[134:137], v[188:191], v[184:187], v[134:137]
	v_mfma_f32_16x16x32_bf16 v[130:133], v[192:195], v[184:187], v[130:133]
	ds_read_b128 v[184:187], v169 offset:14336
	ds_read_b64_tr_b16 v[204:205], v206 offset:16384
	ds_read_b64_tr_b16 v[206:207], v206 offset:18432
	s_waitcnt lgkmcnt(6)
	v_mfma_f32_16x16x32_bf16 v[98:101], v[172:175], v[196:199], v[98:101]
	v_mfma_f32_16x16x32_bf16 v[102:105], v[180:183], v[196:199], v[102:105]
	v_mfma_f32_16x16x32_bf16 v[110:113], v[188:191], v[196:199], v[110:113]
	v_mfma_f32_16x16x32_bf16 v[106:109], v[192:195], v[196:199], v[106:109]
	v_add_u32_e32 v171, 0, v171
	ds_read_b128 v[196:199], v171
	ds_read_b64_tr_b16 v[208:209], v210 offset:16384
	ds_read_b64_tr_b16 v[210:211], v210 offset:18432
	s_waitcnt lgkmcnt(8)
	v_mfma_f32_16x16x32_bf16 v[70:73], v[172:175], v[176:179], v[70:73]
	v_mfma_f32_16x16x32_bf16 v[82:85], v[180:183], v[176:179], v[82:85]
	v_mfma_f32_16x16x32_bf16 v[86:89], v[188:191], v[176:179], v[86:89]
	v_mfma_f32_16x16x32_bf16 v[74:77], v[192:195], v[176:179], v[74:77]
	s_waitcnt lgkmcnt(5)
	v_mfma_f32_16x16x32_bf16 v[42:45], v[172:175], v[184:187], v[42:45]
	ds_read_b128 v[172:175], v171 offset:2048
	ds_read_b64_tr_b16 v[176:177], v212 offset:16384
	ds_read_b64_tr_b16 v[178:179], v212 offset:18432
	v_mfma_f32_16x16x32_bf16 v[54:57], v[180:183], v[184:187], v[54:57]
	v_mfma_f32_16x16x32_bf16 v[58:61], v[188:191], v[184:187], v[58:61]
	v_mfma_f32_16x16x32_bf16 v[50:53], v[192:195], v[184:187], v[50:53]
	ds_read_b128 v[180:183], v171 offset:4096
	s_waitcnt vmcnt(3)
	v_add_u32_e32 v168, s38, v168
	s_waitcnt lgkmcnt(6)
	v_mfma_f32_16x16x32_bf16 v[62:65], v[200:203], v[196:199], v[62:65]
	ds_write_b128 v168, v[14:17]
	v_mfma_f32_16x16x32_bf16 v[46:49], v[204:207], v[196:199], v[46:49]
	s_waitcnt lgkmcnt(5)
	v_mfma_f32_16x16x32_bf16 v[38:41], v[208:211], v[196:199], v[38:41]
	s_waitcnt lgkmcnt(2)
	v_mfma_f32_16x16x32_bf16 v[14:17], v[176:179], v[196:199], v[34:37]
	s_nop 2
	ds_read_b128 v[34:37], v171 offset:6144
	s_waitcnt vmcnt(2)
	v_mfma_f32_16x16x32_bf16 v[30:33], v[200:203], v[172:175], v[30:33]
	ds_write_b128 v168, v[10:13] offset:8192
	v_mfma_f32_16x16x32_bf16 v[26:29], v[204:207], v[172:175], v[26:29]
	v_mfma_f32_16x16x32_bf16 v[22:25], v[208:211], v[172:175], v[22:25]
	v_mfma_f32_16x16x32_bf16 v[10:13], v[176:179], v[172:175], v[18:21]
	s_waitcnt lgkmcnt(3)
	v_mfma_f32_16x16x32_bf16 v[18:21], v[200:203], v[180:183], v[66:69]
	v_mfma_f32_16x16x32_bf16 v[66:69], v[204:207], v[180:183], v[78:81]
	v_mfma_f32_16x16x32_bf16 v[78:81], v[208:211], v[180:183], v[90:93]
	s_nop 2
	ds_read_b128 v[90:93], v171 offset:8192
	s_waitcnt vmcnt(1)
	ds_write_b128 v168, v[6:9] offset:16384
	v_mfma_f32_16x16x32_bf16 v[6:9], v[176:179], v[180:183], v[94:97]
	s_waitcnt lgkmcnt(3)
	v_mfma_f32_16x16x32_bf16 v[94:97], v[200:203], v[34:37], v[114:117]
	v_mfma_f32_16x16x32_bf16 v[114:117], v[204:207], v[34:37], v[122:125]
	v_mfma_f32_16x16x32_bf16 v[122:125], v[208:211], v[34:37], v[138:141]
	s_nop 2
	ds_read_b128 v[138:141], v171 offset:10240
	s_waitcnt vmcnt(0)
	ds_write_b128 v168, v[2:5] offset:24576
	v_mfma_f32_16x16x32_bf16 v[2:5], v[176:179], v[34:37], v[142:145]
	s_waitcnt lgkmcnt(3)
	v_mfma_f32_16x16x32_bf16 v[34:37], v[200:203], v[90:93], v[118:121]
	v_mfma_f32_16x16x32_bf16 v[118:121], v[204:207], v[90:93], v[126:129]
	v_mfma_f32_16x16x32_bf16 v[126:129], v[208:211], v[90:93], v[134:137]
	s_nop 2
	ds_read_b128 v[134:137], v171 offset:12288
	v_mfma_f32_16x16x32_bf16 v[90:93], v[176:179], v[90:93], v[130:133]
	s_waitcnt lgkmcnt(2)
	v_mfma_f32_16x16x32_bf16 v[98:101], v[200:203], v[138:141], v[98:101]
	s_nop 0
	ds_read_b128 v[130:133], v171 offset:14336
	v_mfma_f32_16x16x32_bf16 v[102:105], v[204:207], v[138:141], v[102:105]
	v_mfma_f32_16x16x32_bf16 v[110:113], v[208:211], v[138:141], v[110:113]
	v_mfma_f32_16x16x32_bf16 v[106:109], v[176:179], v[138:141], v[106:109]
	s_waitcnt lgkmcnt(1)
	v_mfma_f32_16x16x32_bf16 v[70:73], v[200:203], v[134:137], v[70:73]
	v_mfma_f32_16x16x32_bf16 v[82:85], v[204:207], v[134:137], v[82:85]
	v_mfma_f32_16x16x32_bf16 v[86:89], v[208:211], v[134:137], v[86:89]
	v_mfma_f32_16x16x32_bf16 v[74:77], v[176:179], v[134:137], v[74:77]
	s_waitcnt lgkmcnt(0)
	v_mfma_f32_16x16x32_bf16 v[42:45], v[200:203], v[130:133], v[42:45]
	v_mfma_f32_16x16x32_bf16 v[54:57], v[204:207], v[130:133], v[54:57]
	v_mfma_f32_16x16x32_bf16 v[58:61], v[208:211], v[130:133], v[58:61]
	v_mfma_f32_16x16x32_bf16 v[50:53], v[176:179], v[130:133], v[50:53]
	s_waitcnt lgkmcnt(0)
	s_barrier
	v_add_u32_e32 v153, s38, v153
	v_add_u32_e32 v152, s38, v152
	v_add_u32_e32 v151, s38, v151
	ds_read_b64_tr_b16 v[130:131], v153
	ds_read_b64_tr_b16 v[132:133], v153 offset:2048
	ds_read_b64_tr_b16 v[134:135], v152
	ds_read_b64_tr_b16 v[136:137], v152 offset:2048
	ds_read_b128 v[138:141], v169 offset:32768
	ds_read_b64_tr_b16 v[142:143], v151
	ds_read_b128 v[172:175], v169 offset:34816
	ds_read_b128 v[176:179], v169 offset:36864
	ds_read_b64_tr_b16 v[144:145], v151 offset:2048
	v_add_u32_e32 v146, s38, v146
	ds_read_b64_tr_b16 v[180:181], v146
	ds_read_b64_tr_b16 v[182:183], v146 offset:2048
	s_waitcnt lgkmcnt(6)
	v_mfma_f32_16x16x32_bf16 v[62:65], v[130:133], v[138:141], v[62:65]
	v_mfma_f32_16x16x32_bf16 v[46:49], v[134:137], v[138:141], v[46:49]
	s_waitcnt lgkmcnt(2)
	v_mfma_f32_16x16x32_bf16 v[38:41], v[142:145], v[138:141], v[38:41]
	s_waitcnt lgkmcnt(0)
	v_mfma_f32_16x16x32_bf16 v[14:17], v[180:183], v[138:141], v[14:17]
	v_mfma_f32_16x16x32_bf16 v[30:33], v[130:133], v[172:175], v[30:33]
	ds_read_b128 v[138:141], v169 offset:38912
	v_mfma_f32_16x16x32_bf16 v[26:29], v[134:137], v[172:175], v[26:29]
	v_mfma_f32_16x16x32_bf16 v[22:25], v[142:145], v[172:175], v[22:25]
	v_mfma_f32_16x16x32_bf16 v[10:13], v[180:183], v[172:175], v[10:13]
	v_mfma_f32_16x16x32_bf16 v[18:21], v[130:133], v[176:179], v[18:21]
	ds_read_b128 v[172:175], v169 offset:40960
	v_mfma_f32_16x16x32_bf16 v[66:69], v[134:137], v[176:179], v[66:69]
	v_mfma_f32_16x16x32_bf16 v[78:81], v[142:145], v[176:179], v[78:81]
	v_mfma_f32_16x16x32_bf16 v[6:9], v[180:183], v[176:179], v[6:9]
	s_waitcnt lgkmcnt(1)
	v_mfma_f32_16x16x32_bf16 v[176:179], v[130:133], v[138:141], v[94:97]
	s_nop 2
	ds_read_b128 v[94:97], v169 offset:43008
	v_mfma_f32_16x16x32_bf16 v[2:5], v[180:183], v[138:141], v[2:5]
	v_mfma_f32_16x16x32_bf16 v[184:187], v[134:137], v[138:141], v[114:117]
	v_mfma_f32_16x16x32_bf16 v[188:191], v[142:145], v[138:141], v[122:125]
	s_nop 1
	ds_read_b128 v[114:117], v169 offset:45056
	ds_read_b64_tr_b16 v[196:197], v153 offset:16384
	ds_read_b64_tr_b16 v[198:199], v153 offset:18432
	s_waitcnt lgkmcnt(4)
	v_mfma_f32_16x16x32_bf16 v[34:37], v[130:133], v[172:175], v[34:37]
	v_mfma_f32_16x16x32_bf16 v[138:141], v[134:137], v[172:175], v[118:121]
	v_mfma_f32_16x16x32_bf16 v[192:195], v[142:145], v[172:175], v[126:129]
	v_mfma_f32_16x16x32_bf16 v[172:175], v[180:183], v[172:175], v[90:93]
	s_nop 2
	ds_read_b128 v[90:93], v169 offset:47104
	ds_read_b64_tr_b16 v[212:213], v152 offset:16384
	ds_read_b64_tr_b16 v[214:215], v152 offset:18432
	s_waitcnt lgkmcnt(6)
	v_mfma_f32_16x16x32_bf16 v[200:203], v[130:133], v[94:97], v[98:101]
	v_mfma_f32_16x16x32_bf16 v[204:207], v[134:137], v[94:97], v[102:105]
	v_mfma_f32_16x16x32_bf16 v[208:211], v[142:145], v[94:97], v[110:113]
	v_mfma_f32_16x16x32_bf16 v[216:219], v[180:183], v[94:97], v[106:109]
	s_waitcnt lgkmcnt(5)
	v_mfma_f32_16x16x32_bf16 v[220:223], v[130:133], v[114:117], v[70:73]
	s_nop 2
	ds_read_b128 v[70:73], v171 offset:32768
	ds_read_b64_tr_b16 v[232:233], v151 offset:16384
	ds_read_b64_tr_b16 v[234:235], v151 offset:18432
	v_mfma_f32_16x16x32_bf16 v[224:227], v[134:137], v[114:117], v[82:85]
	v_mfma_f32_16x16x32_bf16 v[228:231], v[142:145], v[114:117], v[86:89]
	v_mfma_f32_16x16x32_bf16 v[236:239], v[180:183], v[114:117], v[74:77]
	s_waitcnt lgkmcnt(5)
	v_mfma_f32_16x16x32_bf16 v[130:133], v[130:133], v[90:93], v[42:45]
	s_nop 2
	ds_read_b128 v[42:45], v171 offset:34816
	ds_read_b64_tr_b16 v[240:241], v146 offset:16384
	ds_read_b64_tr_b16 v[242:243], v146 offset:18432
	v_mfma_f32_16x16x32_bf16 v[134:137], v[134:137], v[90:93], v[54:57]
	v_mfma_f32_16x16x32_bf16 v[142:145], v[142:145], v[90:93], v[58:61]
	v_mfma_f32_16x16x32_bf16 v[180:183], v[180:183], v[90:93], v[50:53]
	s_waitcnt lgkmcnt(3)
	v_mfma_f32_16x16x32_bf16 v[118:121], v[232:235], v[70:73], v[38:41]
	s_nop 2
	ds_read_b128 v[38:41], v171 offset:36864
	v_mfma_f32_16x16x32_bf16 v[126:129], v[196:199], v[70:73], v[62:65]
	v_mfma_f32_16x16x32_bf16 v[122:125], v[212:215], v[70:73], v[46:49]
	s_waitcnt lgkmcnt(1)
	v_mfma_f32_16x16x32_bf16 v[114:117], v[240:243], v[70:73], v[14:17]
	s_nop 2
	ds_read_b128 v[14:17], v171 offset:38912
	v_mfma_f32_16x16x32_bf16 v[110:113], v[196:199], v[42:45], v[30:33]
	v_mfma_f32_16x16x32_bf16 v[106:109], v[212:215], v[42:45], v[26:29]
	v_mfma_f32_16x16x32_bf16 v[102:105], v[232:235], v[42:45], v[22:25]
	v_mfma_f32_16x16x32_bf16 v[98:101], v[240:243], v[42:45], v[10:13]
	s_nop 2
	ds_read_b128 v[10:13], v171 offset:40960
	s_waitcnt lgkmcnt(2)
	v_mfma_f32_16x16x32_bf16 v[94:97], v[196:199], v[38:41], v[18:21]
	v_mfma_f32_16x16x32_bf16 v[90:93], v[212:215], v[38:41], v[66:69]
	v_mfma_f32_16x16x32_bf16 v[86:89], v[232:235], v[38:41], v[78:81]
	v_mfma_f32_16x16x32_bf16 v[82:85], v[240:243], v[38:41], v[6:9]
	s_nop 2
	ds_read_b128 v[6:9], v171 offset:43008
	s_waitcnt lgkmcnt(2)
	v_mfma_f32_16x16x32_bf16 v[78:81], v[196:199], v[14:17], v[176:179]
	v_mfma_f32_16x16x32_bf16 v[74:77], v[212:215], v[14:17], v[184:187]
	v_mfma_f32_16x16x32_bf16 v[70:73], v[232:235], v[14:17], v[188:191]
	v_mfma_f32_16x16x32_bf16 v[66:69], v[240:243], v[14:17], v[2:5]
	s_nop 2
	ds_read_b128 v[2:5], v171 offset:45056
	s_waitcnt lgkmcnt(2)
	v_mfma_f32_16x16x32_bf16 v[62:65], v[196:199], v[10:13], v[34:37]
	v_mfma_f32_16x16x32_bf16 v[58:61], v[212:215], v[10:13], v[138:141]
	v_mfma_f32_16x16x32_bf16 v[54:57], v[232:235], v[10:13], v[192:195]
	v_mfma_f32_16x16x32_bf16 v[50:53], v[240:243], v[10:13], v[172:175]
	s_waitcnt lgkmcnt(1)
	v_mfma_f32_16x16x32_bf16 v[46:49], v[196:199], v[6:9], v[200:203]
	ds_read_b128 v[138:141], v171 offset:47104
	v_mfma_f32_16x16x32_bf16 v[42:45], v[212:215], v[6:9], v[204:207]
	v_mfma_f32_16x16x32_bf16 v[38:41], v[232:235], v[6:9], v[208:211]
	v_mfma_f32_16x16x32_bf16 v[34:37], v[240:243], v[6:9], v[216:219]
	s_waitcnt lgkmcnt(1)
	v_mfma_f32_16x16x32_bf16 v[30:33], v[196:199], v[2:5], v[220:223]
	v_mfma_f32_16x16x32_bf16 v[26:29], v[212:215], v[2:5], v[224:227]
	v_mfma_f32_16x16x32_bf16 v[22:25], v[232:235], v[2:5], v[228:231]
	v_mfma_f32_16x16x32_bf16 v[18:21], v[240:243], v[2:5], v[236:239]
	s_waitcnt lgkmcnt(0)
	v_mfma_f32_16x16x32_bf16 v[14:17], v[196:199], v[138:141], v[130:133]
	v_mfma_f32_16x16x32_bf16 v[10:13], v[212:215], v[138:141], v[134:137]
	v_mfma_f32_16x16x32_bf16 v[6:9], v[232:235], v[138:141], v[142:145]
	v_mfma_f32_16x16x32_bf16 v[2:5], v[240:243], v[138:141], v[180:183]
	s_waitcnt lgkmcnt(0)
	s_barrier
	v_mov_b32_e32 v151, v155
	v_mov_b32_e32 v168, v1
	s_cmpk_gt_i32 s28, 0x3ff
	s_mov_b64 s[0:1], -1
	s_cbranch_scc1 .LBB0_607
	s_add_i32 s0, s52, s50
	v_add_u32_e32 v140, s0, v168
	s_lshl_b32 s0, s51, 6
	s_or_b32 s0, s0, s28
	v_lshlrev_b32_e32 v132, 2, v151
	v_add_u32_e32 v146, s0, v132
	v_ashrrev_i32_e32 v141, 31, v140
	v_lshlrev_b64 v[142:143], 11, v[140:141]
	v_cmp_lt_i32_e64 s[4:5], s39, v146
	s_and_saveexec_b64 s[0:1], s[4:5]
	s_xor_b64 s[0:1], exec, s[0:1]
	s_cbranch_execz .LBB0_442
	v_cmp_lt_u32_e32 vcc, s41, v146
	s_and_saveexec_b64 s[2:3], vcc
	s_xor_b64 s[2:3], exec, s[2:3]
	s_cbranch_execz .LBB0_439
	v_cmp_lt_u32_e32 vcc, s42, v146
	v_cvt_pk_bf16_f32 v130, v126, v127
	v_cvt_pk_bf16_f32 v131, v128, v129
	s_and_saveexec_b64 s[6:7], vcc
	s_xor_b64 s[6:7], exec, s[6:7]
	s_cbranch_execz .LBB0_436
	v_lshl_add_u64 v[134:135], s[24:25], 0, v[142:143]
	v_lshl_add_u64 v[134:135], v[146:147], 1, v[134:135]
	v_add_co_u32_e32 v134, vcc, 0xfffff000, v134
	s_nop 1
	v_addc_co_u32_e32 v135, vcc, -1, v135, vcc
	global_store_dwordx2 v[134:135], v[130:131], off offset:-2048

.Lrot_gl:
	ds_read_b64_tr_b16 v[160:161], v157
	ds_read_b64_tr_b16 v[162:163], v157 offset:2048
	ds_read_b64_tr_b16 v[164:165], v168
	ds_read_b64_tr_b16 v[166:167], v168 offset:2048
	ds_read_b128 v[172:175], v169
	ds_read_b128 v[176:179], v169 offset:2048
	ds_read_b64_tr_b16 v[180:181], v200
	ds_read_b64_tr_b16 v[182:183], v200 offset:2048
	v_add_u32_e32 v201, s34, v148
	ds_read_b64_tr_b16 v[184:185], v201
	ds_read_b64_tr_b16 v[186:187], v201 offset:2048
	ds_read_b128 v[188:191], v169 offset:4096
	s_waitcnt lgkmcnt(6)
	v_mfma_f32_16x16x32_bf16 v[18:21], v[160:163], v[172:175], v[18:21]
	v_add_u32_e32 v192, 0xfffa0000, v156
	s_add_i32 s34, s27, s31
	s_mov_b32 s35, m0
	s_mov_b32 m0, s34
	s_nop 0
	global_load_lds_dwordx4 v192, s[6:7]
	s_mov_b32 m0, s35
	v_mfma_f32_16x16x32_bf16 v[22:25], v[164:167], v[172:175], v[22:25]
	s_waitcnt lgkmcnt(3)
	v_mfma_f32_16x16x32_bf16 v[26:29], v[180:183], v[172:175], v[26:29]
	s_waitcnt lgkmcnt(1)
	v_mfma_f32_16x16x32_bf16 v[30:33], v[184:187], v[172:175], v[30:33]
	v_mfma_f32_16x16x32_bf16 v[34:37], v[160:163], v[176:179], v[34:37]
	ds_read_b128 v[172:175], v169 offset:6144
	v_add_u32_e32 v192, 0xfffc0000, v156
	s_add_i32 s35, s34, 0x2000
	v_mfma_f32_16x16x32_bf16 v[38:41], v[164:167], v[176:179], v[38:41]
	s_mov_b32 s36, m0
	s_mov_b32 m0, s35
	s_nop 0
	global_load_lds_dwordx4 v192, s[6:7]
	s_mov_b32 m0, s36
	v_mfma_f32_16x16x32_bf16 v[42:45], v[180:183], v[176:179], v[42:45]
	v_mfma_f32_16x16x32_bf16 v[54:57], v[184:187], v[176:179], v[54:57]
	s_waitcnt lgkmcnt(1)
	v_mfma_f32_16x16x32_bf16 v[66:69], v[160:163], v[188:191], v[66:69]
	ds_read_b128 v[176:179], v169 offset:8192
	v_add_u32_e32 v192, 0xfffe0000, v156
	s_add_i32 s35, s34, 0x4000
	v_mfma_f32_16x16x32_bf16 v[78:81], v[164:167], v[188:191], v[78:81]
	s_mov_b32 s36, m0
	s_mov_b32 m0, s35
	s_nop 0
	global_load_lds_dwordx4 v192, s[6:7]
	s_mov_b32 m0, s36
	v_mfma_f32_16x16x32_bf16 v[90:93], v[180:183], v[188:191], v[90:93]
	v_mfma_f32_16x16x32_bf16 v[94:97], v[184:187], v[188:191], v[94:97]
	s_waitcnt lgkmcnt(1)
	v_mfma_f32_16x16x32_bf16 v[114:117], v[160:163], v[172:175], v[114:117]
	ds_read_b128 v[188:191], v169 offset:10240
	s_addk_i32 s34, 0x6000
	s_mov_b32 s35, m0
	s_mov_b32 m0, s34
	s_nop 0
	global_load_lds_dwordx4 v156, s[6:7]
	s_mov_b32 m0, s35
	v_mfma_f32_16x16x32_bf16 v[122:125], v[164:167], v[172:175], v[122:125]
	v_mfma_f32_16x16x32_bf16 v[138:141], v[180:183], v[172:175], v[138:141]
	v_mfma_f32_16x16x32_bf16 v[142:145], v[184:187], v[172:175], v[142:145]
	ds_read_b128 v[172:175], v169 offset:12288
	ds_read_b64_tr_b16 v[192:193], v157 offset:16384
	ds_read_b64_tr_b16 v[194:195], v157 offset:18432
	s_waitcnt lgkmcnt(4)
	v_mfma_f32_16x16x32_bf16 v[118:121], v[160:163], v[176:179], v[118:121]
	v_mfma_f32_16x16x32_bf16 v[126:129], v[164:167], v[176:179], v[126:129]
	v_mfma_f32_16x16x32_bf16 v[134:137], v[180:183], v[176:179], v[134:137]
	v_mfma_f32_16x16x32_bf16 v[130:133], v[184:187], v[176:179], v[130:133]
	ds_read_b128 v[176:179], v169 offset:14336
	ds_read_b64_tr_b16 v[196:197], v168 offset:16384
	ds_read_b64_tr_b16 v[198:199], v168 offset:18432
	s_waitcnt lgkmcnt(6)
	v_mfma_f32_16x16x32_bf16 v[98:101], v[160:163], v[188:191], v[98:101]
	v_mfma_f32_16x16x32_bf16 v[102:105], v[164:167], v[188:191], v[102:105]
	v_mfma_f32_16x16x32_bf16 v[110:113], v[180:183], v[188:191], v[110:113]
	v_mfma_f32_16x16x32_bf16 v[106:109], v[184:187], v[188:191], v[106:109]
	v_add_u32_e32 v157, s33, v153
	ds_read_b128 v[188:191], v157
	ds_read_b64_tr_b16 v[216:217], v200 offset:16384
	ds_read_b64_tr_b16 v[218:219], v200 offset:18432
	s_waitcnt lgkmcnt(8)
	v_mfma_f32_16x16x32_bf16 v[70:73], v[160:163], v[172:175], v[70:73]
	v_mfma_f32_16x16x32_bf16 v[82:85], v[164:167], v[172:175], v[82:85]
	v_mfma_f32_16x16x32_bf16 v[86:89], v[180:183], v[172:175], v[86:89]
	v_mfma_f32_16x16x32_bf16 v[74:77], v[184:187], v[172:175], v[74:77]
	s_waitcnt lgkmcnt(5)
	v_mfma_f32_16x16x32_bf16 v[46:49], v[160:163], v[176:179], v[46:49]
	ds_read_b128 v[160:163], v157 offset:2048
	s_and_b32 s33, s29, 0x8000
	v_mfma_f32_16x16x32_bf16 v[58:61], v[164:167], v[176:179], v[58:61]
	ds_read_b64_tr_b16 v[164:165], v201 offset:16384
	ds_read_b64_tr_b16 v[166:167], v201 offset:18432
	v_mfma_f32_16x16x32_bf16 v[62:65], v[180:183], v[176:179], v[62:65]
	v_mfma_f32_16x16x32_bf16 v[50:53], v[184:187], v[176:179], v[50:53]
	s_waitcnt lgkmcnt(5)
	v_mfma_f32_16x16x32_bf16 v[18:21], v[192:195], v[188:191], v[18:21]
	ds_read_b128 v[172:175], v157 offset:4096
	v_add_u32_e32 v168, s33, v155
	s_add_u32 s33, s2, s0
	v_mfma_f32_16x16x32_bf16 v[22:25], v[196:199], v[188:191], v[22:25]
	s_addc_u32 s36, s28, s1
	s_waitcnt vmcnt(7)
	s_add_u32 s34, s33, 0x40000
	s_waitcnt lgkmcnt(4)
	v_mfma_f32_16x16x32_bf16 v[26:29], v[216:219], v[188:191], v[26:29]
	ds_write_b128 v168, v[14:17]
	s_addc_u32 s35, s36, 0
	global_load_dwordx4 v[14:17], v208, s[34:35]
	s_waitcnt lgkmcnt(2)
	v_mfma_f32_16x16x32_bf16 v[30:33], v[164:167], v[188:191], v[30:33]
	v_mfma_f32_16x16x32_bf16 v[34:37], v[192:195], v[160:163], v[34:37]
	ds_read_b128 v[176:179], v157 offset:6144
	s_waitcnt vmcnt(7)
	s_add_u32 s34, s33, 0x48000
	v_mfma_f32_16x16x32_bf16 v[38:41], v[196:199], v[160:163], v[38:41]
	ds_write_b128 v168, v[10:13] offset:8192
	s_addc_u32 s35, s36, 0
	global_load_dwordx4 v[10:13], v208, s[34:35]
	v_mfma_f32_16x16x32_bf16 v[42:45], v[216:219], v[160:163], v[42:45]
	v_mfma_f32_16x16x32_bf16 v[54:57], v[164:167], v[160:163], v[54:57]
	s_waitcnt lgkmcnt(3)
	v_mfma_f32_16x16x32_bf16 v[66:69], v[192:195], v[172:175], v[66:69]
	ds_read_b128 v[160:163], v157 offset:8192
	s_waitcnt vmcnt(7)
	s_add_u32 s34, s33, 0x50000
	v_mfma_f32_16x16x32_bf16 v[78:81], v[196:199], v[172:175], v[78:81]
	ds_write_b128 v168, v[6:9] offset:16384
	s_addc_u32 s35, s36, 0
	global_load_dwordx4 v[6:9], v208, s[34:35]
	v_mfma_f32_16x16x32_bf16 v[90:93], v[216:219], v[172:175], v[90:93]
	v_mfma_f32_16x16x32_bf16 v[94:97], v[164:167], v[172:175], v[94:97]
	s_waitcnt lgkmcnt(3)
	v_mfma_f32_16x16x32_bf16 v[114:117], v[192:195], v[176:179], v[114:117]
	ds_read_b128 v[172:175], v157 offset:10240
	s_waitcnt vmcnt(7)
	s_add_u32 s34, s33, 0x58000
	v_mfma_f32_16x16x32_bf16 v[122:125], v[196:199], v[176:179], v[122:125]
	ds_write_b128 v168, v[2:5] offset:24576
	s_addc_u32 s35, s36, 0
	global_load_dwordx4 v[2:5], v208, s[34:35]
	v_mfma_f32_16x16x32_bf16 v[138:141], v[216:219], v[176:179], v[138:141]
	v_mfma_f32_16x16x32_bf16 v[142:145], v[164:167], v[176:179], v[142:145]
	s_waitcnt lgkmcnt(3)
	v_mfma_f32_16x16x32_bf16 v[118:121], v[192:195], v[160:163], v[118:121]
	ds_read_b128 v[176:179], v157 offset:12288
	v_mfma_f32_16x16x32_bf16 v[126:129], v[196:199], v[160:163], v[126:129]
	v_mfma_f32_16x16x32_bf16 v[134:137], v[216:219], v[160:163], v[134:137]
	v_mfma_f32_16x16x32_bf16 v[130:133], v[164:167], v[160:163], v[130:133]
	s_waitcnt lgkmcnt(2)
	v_mfma_f32_16x16x32_bf16 v[98:101], v[192:195], v[172:175], v[98:101]
	ds_read_b128 v[160:163], v157 offset:14336
	v_mfma_f32_16x16x32_bf16 v[102:105], v[196:199], v[172:175], v[102:105]
	v_mfma_f32_16x16x32_bf16 v[110:113], v[216:219], v[172:175], v[110:113]
	v_mfma_f32_16x16x32_bf16 v[106:109], v[164:167], v[172:175], v[106:109]
	s_waitcnt lgkmcnt(1)
	v_mfma_f32_16x16x32_bf16 v[70:73], v[192:195], v[176:179], v[70:73]
	v_mfma_f32_16x16x32_bf16 v[82:85], v[196:199], v[176:179], v[82:85]
	v_mfma_f32_16x16x32_bf16 v[86:89], v[216:219], v[176:179], v[86:89]
	v_mfma_f32_16x16x32_bf16 v[74:77], v[164:167], v[176:179], v[74:77]
	s_waitcnt lgkmcnt(0)
	v_mfma_f32_16x16x32_bf16 v[46:49], v[192:195], v[160:163], v[46:49]
	v_mfma_f32_16x16x32_bf16 v[58:61], v[196:199], v[160:163], v[58:61]
	v_mfma_f32_16x16x32_bf16 v[62:65], v[216:219], v[160:163], v[62:65]
	v_mfma_f32_16x16x32_bf16 v[50:53], v[164:167], v[160:163], v[50:53]
	s_add_i32 s33, s30, 0x8000
	s_cmp_lg_u32 s30, 0x10000
	s_cselect_b32 s30, s33, 0
	s_add_i32 s33, s31, 0x8000
	s_cmp_lg_u32 s31, 0x10000
	s_cselect_b32 s31, s33, 0
	s_add_u32 s0, s0, 0x20000
	s_addc_u32 s1, s1, 0
	s_add_i32 s29, s29, 0x8000
	v_add_u32_e32 v156, 0x80, v156
	s_add_i32 s34, s29, 0xffff8000
	s_and_b32 s34, s34, 0x8000
	s_add_i32 s34, s34, 0
	s_add_i32 s33, s30, 0
	s_add_i32 s34, s34, 0x18000
	v_add_u32_e32 v157, s34, v152
	v_add_u32_e32 v169, s33, v150
	v_add_u32_e32 v200, s34, v149
	v_add_u32_e32 v168, s34, v151
	s_waitcnt lgkmcnt(0)
	s_barrier
	s_cmp_lg_u32 s0, 0x1c0000
	s_cbranch_scc1 .Lrot_gl
	s_add_i32 s0, 0, 0x18000
	s_add_i32 s1, 0, 0x10000
	v_add_u32_e32 v155, s0, v152
	v_add_u32_e32 v157, s1, v150
	v_add_u32_e32 v168, s0, v149
	v_add_u32_e32 v169, s0, v148
	v_add_u32_e32 v156, s0, v151
	ds_read_b64_tr_b16 v[160:161], v155
	ds_read_b64_tr_b16 v[162:163], v155 offset:2048
	ds_read_b64_tr_b16 v[164:165], v156
	ds_read_b64_tr_b16 v[166:167], v156 offset:2048
	ds_read_b128 v[172:175], v157
	ds_read_b128 v[176:179], v157 offset:2048
	ds_read_b64_tr_b16 v[180:181], v168
	ds_read_b64_tr_b16 v[182:183], v168 offset:2048
	ds_read_b64_tr_b16 v[184:185], v169
	ds_read_b64_tr_b16 v[186:187], v169 offset:2048
	ds_read_b128 v[188:191], v157 offset:4096
	s_waitcnt lgkmcnt(6)
	v_mfma_f32_16x16x32_bf16 v[18:21], v[160:163], v[172:175], v[18:21]
	v_mfma_f32_16x16x32_bf16 v[22:25], v[164:167], v[172:175], v[22:25]
	s_waitcnt lgkmcnt(3)
	v_mfma_f32_16x16x32_bf16 v[26:29], v[180:183], v[172:175], v[26:29]
	s_waitcnt lgkmcnt(1)
	v_mfma_f32_16x16x32_bf16 v[30:33], v[184:187], v[172:175], v[30:33]
	ds_read_b128 v[172:175], v157 offset:6144
	v_mfma_f32_16x16x32_bf16 v[34:37], v[160:163], v[176:179], v[34:37]
	v_mfma_f32_16x16x32_bf16 v[38:41], v[164:167], v[176:179], v[38:41]
	v_mfma_f32_16x16x32_bf16 v[42:45], v[180:183], v[176:179], v[42:45]
	v_mfma_f32_16x16x32_bf16 v[54:57], v[184:187], v[176:179], v[54:57]
	ds_read_b128 v[176:179], v157 offset:8192
	s_waitcnt lgkmcnt(2)
	v_mfma_f32_16x16x32_bf16 v[66:69], v[160:163], v[188:191], v[66:69]
	v_mfma_f32_16x16x32_bf16 v[78:81], v[164:167], v[188:191], v[78:81]
	v_mfma_f32_16x16x32_bf16 v[90:93], v[180:183], v[188:191], v[90:93]
	v_mfma_f32_16x16x32_bf16 v[94:97], v[184:187], v[188:191], v[94:97]
	ds_read_b128 v[188:191], v157 offset:10240
	s_waitcnt lgkmcnt(2)
	v_mfma_f32_16x16x32_bf16 v[114:117], v[160:163], v[172:175], v[114:117]
	v_mfma_f32_16x16x32_bf16 v[122:125], v[164:167], v[172:175], v[122:125]
	v_mfma_f32_16x16x32_bf16 v[138:141], v[180:183], v[172:175], v[138:141]
	v_mfma_f32_16x16x32_bf16 v[142:145], v[184:187], v[172:175], v[142:145]
	ds_read_b128 v[172:175], v157 offset:12288
	ds_read_b64_tr_b16 v[192:193], v155 offset:16384
	ds_read_b64_tr_b16 v[194:195], v155 offset:18432
	s_waitcnt lgkmcnt(4)
	v_mfma_f32_16x16x32_bf16 v[118:121], v[160:163], v[176:179], v[118:121]
	v_mfma_f32_16x16x32_bf16 v[126:129], v[164:167], v[176:179], v[126:129]
	v_mfma_f32_16x16x32_bf16 v[134:137], v[180:183], v[176:179], v[134:137]
	v_mfma_f32_16x16x32_bf16 v[130:133], v[184:187], v[176:179], v[130:133]
	ds_read_b128 v[176:179], v157 offset:14336
	ds_read_b64_tr_b16 v[196:197], v156 offset:16384
	ds_read_b64_tr_b16 v[198:199], v156 offset:18432
	s_waitcnt lgkmcnt(6)
	v_mfma_f32_16x16x32_bf16 v[98:101], v[160:163], v[188:191], v[98:101]
	v_mfma_f32_16x16x32_bf16 v[102:105], v[164:167], v[188:191], v[102:105]
	v_mfma_f32_16x16x32_bf16 v[110:113], v[180:183], v[188:191], v[110:113]
	v_mfma_f32_16x16x32_bf16 v[106:109], v[184:187], v[188:191], v[106:109]
	v_add_u32_e32 v155, s1, v153
	ds_read_b128 v[188:191], v155
	ds_read_b64_tr_b16 v[216:217], v168 offset:16384
	ds_read_b64_tr_b16 v[218:219], v168 offset:18432
	s_waitcnt lgkmcnt(8)
	v_mfma_f32_16x16x32_bf16 v[70:73], v[160:163], v[172:175], v[70:73]
	v_mfma_f32_16x16x32_bf16 v[82:85], v[164:167], v[172:175], v[82:85]
	v_mfma_f32_16x16x32_bf16 v[86:89], v[180:183], v[172:175], v[86:89]
	v_mfma_f32_16x16x32_bf16 v[74:77], v[184:187], v[172:175], v[74:77]
	s_waitcnt lgkmcnt(5)
	v_mfma_f32_16x16x32_bf16 v[46:49], v[160:163], v[176:179], v[46:49]
	v_mfma_f32_16x16x32_bf16 v[58:61], v[164:167], v[176:179], v[58:61]
	ds_read_b128 v[160:163], v155 offset:2048
	ds_read_b64_tr_b16 v[164:165], v169 offset:16384
	ds_read_b64_tr_b16 v[166:167], v169 offset:18432
	v_mfma_f32_16x16x32_bf16 v[62:65], v[180:183], v[176:179], v[62:65]
	v_mfma_f32_16x16x32_bf16 v[50:53], v[184:187], v[176:179], v[50:53]
	ds_read_b128 v[172:175], v155 offset:4096
	s_add_i32 s0, 0, 0x20000
	s_waitcnt vmcnt(3)
	v_add_u32_e32 v154, s0, v154
	s_waitcnt lgkmcnt(6)
	v_mfma_f32_16x16x32_bf16 v[18:21], v[192:195], v[188:191], v[18:21]
	ds_write_b128 v154, v[14:17]
	v_mfma_f32_16x16x32_bf16 v[22:25], v[196:199], v[188:191], v[22:25]
	s_waitcnt lgkmcnt(5)
	v_mfma_f32_16x16x32_bf16 v[26:29], v[216:219], v[188:191], v[26:29]
	s_waitcnt lgkmcnt(2)
	v_mfma_f32_16x16x32_bf16 v[14:17], v[164:167], v[188:191], v[30:33]
	v_mfma_f32_16x16x32_bf16 v[30:33], v[192:195], v[160:163], v[34:37]
	v_mfma_f32_16x16x32_bf16 v[34:37], v[196:199], v[160:163], v[38:41]
	v_mfma_f32_16x16x32_bf16 v[38:41], v[216:219], v[160:163], v[42:45]
	s_nop 2
	ds_read_b128 v[42:45], v155 offset:6144
	s_waitcnt vmcnt(2)
	ds_write_b128 v154, v[10:13] offset:8192
	v_mfma_f32_16x16x32_bf16 v[10:13], v[164:167], v[160:163], v[54:57]
	s_waitcnt lgkmcnt(3)
	v_mfma_f32_16x16x32_bf16 v[54:57], v[192:195], v[172:175], v[66:69]
	v_mfma_f32_16x16x32_bf16 v[66:69], v[196:199], v[172:175], v[78:81]
	v_mfma_f32_16x16x32_bf16 v[78:81], v[216:219], v[172:175], v[90:93]
	s_nop 2
	ds_read_b128 v[90:93], v155 offset:8192
	s_waitcnt vmcnt(1)
	ds_write_b128 v154, v[6:9] offset:16384
	v_mfma_f32_16x16x32_bf16 v[6:9], v[164:167], v[172:175], v[94:97]
	s_waitcnt lgkmcnt(3)
	v_mfma_f32_16x16x32_bf16 v[94:97], v[192:195], v[42:45], v[114:117]
	v_mfma_f32_16x16x32_bf16 v[114:117], v[196:199], v[42:45], v[122:125]
	v_mfma_f32_16x16x32_bf16 v[122:125], v[216:219], v[42:45], v[138:141]
	s_nop 2
	ds_read_b128 v[138:141], v155 offset:10240
	s_waitcnt vmcnt(0)
	ds_write_b128 v154, v[2:5] offset:24576
	v_mfma_f32_16x16x32_bf16 v[2:5], v[164:167], v[42:45], v[142:145]
	s_waitcnt lgkmcnt(3)
	v_mfma_f32_16x16x32_bf16 v[42:45], v[192:195], v[90:93], v[118:121]
	v_mfma_f32_16x16x32_bf16 v[118:121], v[196:199], v[90:93], v[126:129]
	v_mfma_f32_16x16x32_bf16 v[126:129], v[216:219], v[90:93], v[134:137]
	s_nop 2
	ds_read_b128 v[134:137], v155 offset:12288
	v_mfma_f32_16x16x32_bf16 v[90:93], v[164:167], v[90:93], v[130:133]
	s_nop 2
	ds_read_b128 v[130:133], v155 offset:14336
	s_waitcnt lgkmcnt(3)
	v_mfma_f32_16x16x32_bf16 v[98:101], v[192:195], v[138:141], v[98:101]
	v_mfma_f32_16x16x32_bf16 v[102:105], v[196:199], v[138:141], v[102:105]
	v_mfma_f32_16x16x32_bf16 v[110:113], v[216:219], v[138:141], v[110:113]
	v_mfma_f32_16x16x32_bf16 v[106:109], v[164:167], v[138:141], v[106:109]
	s_waitcnt lgkmcnt(1)
	v_mfma_f32_16x16x32_bf16 v[70:73], v[192:195], v[134:137], v[70:73]
	v_mfma_f32_16x16x32_bf16 v[82:85], v[196:199], v[134:137], v[82:85]
	v_mfma_f32_16x16x32_bf16 v[86:89], v[216:219], v[134:137], v[86:89]
	v_mfma_f32_16x16x32_bf16 v[74:77], v[164:167], v[134:137], v[74:77]
	s_waitcnt lgkmcnt(0)
	v_mfma_f32_16x16x32_bf16 v[46:49], v[192:195], v[130:133], v[46:49]
	v_mfma_f32_16x16x32_bf16 v[58:61], v[196:199], v[130:133], v[58:61]
	v_mfma_f32_16x16x32_bf16 v[62:65], v[216:219], v[130:133], v[62:65]
	v_mfma_f32_16x16x32_bf16 v[50:53], v[164:167], v[130:133], v[50:53]
	s_waitcnt lgkmcnt(0)
	s_barrier
	v_add_u32_e32 v152, s0, v152
	v_add_u32_e32 v169, 0, v150
	v_add_u32_e32 v200, s0, v149
	v_add_u32_e32 v201, s0, v148
	v_add_u32_e32 v168, s0, v151
	ds_read_b64_tr_b16 v[130:131], v152
	ds_read_b64_tr_b16 v[132:133], v152 offset:2048
	ds_read_b64_tr_b16 v[134:135], v168
	ds_read_b64_tr_b16 v[136:137], v168 offset:2048
	ds_read_b128 v[138:141], v169
	ds_read_b128 v[142:145], v169 offset:2048
	ds_read_b64_tr_b16 v[154:155], v200
	ds_read_b64_tr_b16 v[156:157], v200 offset:2048
	ds_read_b64_tr_b16 v[148:149], v201
	ds_read_b64_tr_b16 v[150:151], v201 offset:2048
	ds_read_b128 v[160:163], v169 offset:4096
	s_waitcnt lgkmcnt(6)
	v_mfma_f32_16x16x32_bf16 v[18:21], v[130:133], v[138:141], v[18:21]
	v_mfma_f32_16x16x32_bf16 v[22:25], v[134:137], v[138:141], v[22:25]
	s_waitcnt lgkmcnt(3)
	v_mfma_f32_16x16x32_bf16 v[26:29], v[154:157], v[138:141], v[26:29]
	s_waitcnt lgkmcnt(1)
	v_mfma_f32_16x16x32_bf16 v[14:17], v[148:151], v[138:141], v[14:17]
	ds_read_b128 v[138:141], v169 offset:6144
	v_mfma_f32_16x16x32_bf16 v[10:13], v[148:151], v[142:145], v[10:13]
	v_mfma_f32_16x16x32_bf16 v[30:33], v[130:133], v[142:145], v[30:33]
	v_mfma_f32_16x16x32_bf16 v[34:37], v[134:137], v[142:145], v[34:37]
	v_mfma_f32_16x16x32_bf16 v[38:41], v[154:157], v[142:145], v[38:41]
	ds_read_b128 v[142:145], v169 offset:8192
	s_waitcnt lgkmcnt(2)
	v_mfma_f32_16x16x32_bf16 v[6:9], v[148:151], v[160:163], v[6:9]
	v_mfma_f32_16x16x32_bf16 v[54:57], v[130:133], v[160:163], v[54:57]
	v_mfma_f32_16x16x32_bf16 v[66:69], v[134:137], v[160:163], v[66:69]
	v_mfma_f32_16x16x32_bf16 v[78:81], v[154:157], v[160:163], v[78:81]
	s_waitcnt lgkmcnt(1)
	v_mfma_f32_16x16x32_bf16 v[160:163], v[134:137], v[138:141], v[114:117]
	s_nop 2
	ds_read_b128 v[114:117], v169 offset:10240
	v_mfma_f32_16x16x32_bf16 v[2:5], v[148:151], v[138:141], v[2:5]
	v_mfma_f32_16x16x32_bf16 v[94:97], v[130:133], v[138:141], v[94:97]
	v_mfma_f32_16x16x32_bf16 v[164:167], v[154:157], v[138:141], v[122:125]
	s_waitcnt lgkmcnt(1)
	v_mfma_f32_16x16x32_bf16 v[138:141], v[134:137], v[142:145], v[118:121]
	s_nop 2
	ds_read_b128 v[118:121], v169 offset:12288
	ds_read_b64_tr_b16 v[176:177], v152 offset:16384
	ds_read_b64_tr_b16 v[178:179], v152 offset:18432
	v_mfma_f32_16x16x32_bf16 v[42:45], v[130:133], v[142:145], v[42:45]
	v_mfma_f32_16x16x32_bf16 v[172:175], v[154:157], v[142:145], v[126:129]
	v_mfma_f32_16x16x32_bf16 v[142:145], v[148:151], v[142:145], v[90:93]
	s_nop 2
	ds_read_b128 v[90:93], v169 offset:14336
	ds_read_b64_tr_b16 v[192:193], v168 offset:16384
	ds_read_b64_tr_b16 v[194:195], v168 offset:18432
	s_waitcnt lgkmcnt(6)
	v_mfma_f32_16x16x32_bf16 v[180:183], v[130:133], v[114:117], v[98:101]
	v_mfma_f32_16x16x32_bf16 v[184:187], v[134:137], v[114:117], v[102:105]
	v_mfma_f32_16x16x32_bf16 v[188:191], v[154:157], v[114:117], v[110:113]
	v_mfma_f32_16x16x32_bf16 v[196:199], v[148:151], v[114:117], v[106:109]
	v_add_u32_e32 v168, 0, v153
	s_waitcnt lgkmcnt(5)
	v_mfma_f32_16x16x32_bf16 v[216:219], v[130:133], v[118:121], v[70:73]
	s_nop 2
	ds_read_b128 v[70:73], v168
	ds_read_b64_tr_b16 v[228:229], v200 offset:16384
	ds_read_b64_tr_b16 v[230:231], v200 offset:18432
	v_mfma_f32_16x16x32_bf16 v[220:223], v[134:137], v[118:121], v[82:85]
	v_mfma_f32_16x16x32_bf16 v[224:227], v[154:157], v[118:121], v[86:89]
	v_mfma_f32_16x16x32_bf16 v[232:235], v[148:151], v[118:121], v[74:77]
	s_waitcnt lgkmcnt(5)
	v_mfma_f32_16x16x32_bf16 v[236:239], v[130:133], v[90:93], v[46:49]
	s_nop 2
	ds_read_b128 v[46:49], v168 offset:2048
	ds_read_b64_tr_b16 v[244:245], v201 offset:16384
	ds_read_b64_tr_b16 v[246:247], v201 offset:18432
	v_mfma_f32_16x16x32_bf16 v[240:243], v[134:137], v[90:93], v[58:61]
	v_mfma_f32_16x16x32_bf16 v[152:155], v[154:157], v[90:93], v[62:65]
	v_mfma_f32_16x16x32_bf16 v[148:151], v[148:151], v[90:93], v[50:53]
	s_waitcnt lgkmcnt(5)
	v_mfma_f32_16x16x32_bf16 v[248:251], v[176:179], v[70:73], v[18:21]
	s_nop 2
	ds_read_b128 v[18:21], v168 offset:4096
	v_mfma_f32_16x16x32_bf16 v[202:205], v[192:195], v[70:73], v[22:25]
	s_waitcnt lgkmcnt(4)
	v_mfma_f32_16x16x32_bf16 v[134:137], v[228:231], v[70:73], v[26:29]
	s_waitcnt lgkmcnt(1)
	v_mfma_f32_16x16x32_bf16 v[130:133], v[244:247], v[70:73], v[14:17]
	s_nop 2
	ds_read_b128 v[14:17], v168 offset:6144
	v_mfma_f32_16x16x32_bf16 v[126:129], v[176:179], v[46:49], v[30:33]
	v_mfma_f32_16x16x32_bf16 v[122:125], v[192:195], v[46:49], v[34:37]
	v_mfma_f32_16x16x32_bf16 v[118:121], v[228:231], v[46:49], v[38:41]
	v_mfma_f32_16x16x32_bf16 v[114:117], v[244:247], v[46:49], v[10:13]
	s_nop 2
	ds_read_b128 v[10:13], v168 offset:8192
	s_waitcnt lgkmcnt(2)
	v_mfma_f32_16x16x32_bf16 v[110:113], v[176:179], v[18:21], v[54:57]
	v_mfma_f32_16x16x32_bf16 v[106:109], v[192:195], v[18:21], v[66:69]
	v_mfma_f32_16x16x32_bf16 v[102:105], v[228:231], v[18:21], v[78:81]
	v_mfma_f32_16x16x32_bf16 v[98:101], v[244:247], v[18:21], v[6:9]
	s_nop 2
	ds_read_b128 v[6:9], v168 offset:10240
	s_waitcnt lgkmcnt(2)
	v_mfma_f32_16x16x32_bf16 v[94:97], v[176:179], v[14:17], v[94:97]
	v_mfma_f32_16x16x32_bf16 v[90:93], v[192:195], v[14:17], v[160:163]
	v_mfma_f32_16x16x32_bf16 v[86:89], v[228:231], v[14:17], v[164:167]
	v_mfma_f32_16x16x32_bf16 v[82:85], v[244:247], v[14:17], v[2:5]
	s_nop 2
	ds_read_b128 v[2:5], v168 offset:12288
	s_waitcnt lgkmcnt(2)
	v_mfma_f32_16x16x32_bf16 v[78:81], v[176:179], v[10:13], v[42:45]
	v_mfma_f32_16x16x32_bf16 v[74:77], v[192:195], v[10:13], v[138:141]
	v_mfma_f32_16x16x32_bf16 v[70:73], v[228:231], v[10:13], v[172:175]
	v_mfma_f32_16x16x32_bf16 v[66:69], v[244:247], v[10:13], v[142:145]
	ds_read_b128 v[14:17], v168 offset:14336
	s_waitcnt lgkmcnt(2)
	v_mfma_f32_16x16x32_bf16 v[62:65], v[176:179], v[6:9], v[180:183]
	v_mfma_f32_16x16x32_bf16 v[58:61], v[192:195], v[6:9], v[184:187]
	v_mfma_f32_16x16x32_bf16 v[54:57], v[228:231], v[6:9], v[188:191]
	v_mfma_f32_16x16x32_bf16 v[50:53], v[244:247], v[6:9], v[196:199]
	s_waitcnt lgkmcnt(1)
	v_mfma_f32_16x16x32_bf16 v[46:49], v[176:179], v[2:5], v[216:219]
	v_mfma_f32_16x16x32_bf16 v[42:45], v[192:195], v[2:5], v[220:223]
	v_mfma_f32_16x16x32_bf16 v[38:41], v[228:231], v[2:5], v[224:227]
	v_mfma_f32_16x16x32_bf16 v[34:37], v[244:247], v[2:5], v[232:235]
	s_waitcnt lgkmcnt(0)
	v_mfma_f32_16x16x32_bf16 v[10:13], v[228:231], v[14:17], v[152:155]
	v_mfma_f32_16x16x32_bf16 v[2:5], v[244:247], v[14:17], v[148:151]
	v_mfma_f32_16x16x32_bf16 v[26:29], v[176:179], v[14:17], v[236:239]
	v_mfma_f32_16x16x32_bf16 v[18:21], v[192:195], v[14:17], v[240:243]
	s_lshl_b32 s0, s26, 6
	v_mov_b32_e32 v144, v1
	v_mov_b32_e32 v145, v252
	s_or_b32 s0, s0, s22
	s_waitcnt lgkmcnt(0)
	s_barrier
	s_add_i32 s24, s24, 0
	v_lshl_add_u32 v6, v145, 2, s0
	s_add_i32 s0, s25, s21
	v_add_u32_e32 v138, s0, v144
	v_ashrrev_i32_e32 v139, 31, v138
	v_ashrrev_i32_e32 v7, 31, v6
	v_lshlrev_b64 v[8:9], 11, v[138:139]
	v_lshl_add_u64 v[8:9], s[6:7], 0, v[8:9]
	v_lshlrev_b64 v[140:141], 1, v[6:7]
	v_lshl_add_u64 v[142:143], v[8:9], 0, v[140:141]
	v_lshl_add_u64 v[6:7], v[6:7], 2, s[94:95]
	global_load_dwordx2 v[216:217], v[142:143], off
	global_load_dwordx4 v[30:33], v[6:7], off
	global_load_dwordx4 v[22:25], v[6:7], off offset:64
	global_load_dwordx4 v[14:17], v[6:7], off offset:128
	s_nop 0
	global_load_dwordx4 v[6:9], v[6:7], off offset:192
	s_nop 0
	global_load_dwordx2 v[218:219], v[142:143], off offset:32
	global_load_dwordx2 v[220:221], v[142:143], off offset:64
	global_load_dwordx2 v[200:201], v[142:143], off offset:96
	v_add_u32_e32 v142, 16, v138
	v_ashrrev_i32_e32 v143, 31, v142
	v_lshlrev_b64 v[142:143], 11, v[142:143]
	v_lshl_add_u64 v[142:143], s[6:7], 0, v[142:143]
	v_lshl_add_u64 v[142:143], v[142:143], 0, v[140:141]
	global_load_dwordx2 v[198:199], v[142:143], off
	global_load_dwordx2 v[196:197], v[142:143], off offset:32
	global_load_dwordx2 v[194:195], v[142:143], off offset:64
	global_load_dwordx2 v[192:193], v[142:143], off offset:96
	v_add_u32_e32 v142, 32, v138
	v_ashrrev_i32_e32 v143, 31, v142
	v_lshlrev_b64 v[142:143], 11, v[142:143]
	v_lshl_add_u64 v[142:143], s[6:7], 0, v[142:143]
	v_lshl_add_u64 v[142:143], v[142:143], 0, v[140:141]
	global_load_dwordx2 v[190:191], v[142:143], off
	global_load_dwordx2 v[188:189], v[142:143], off offset:32
	global_load_dwordx2 v[186:187], v[142:143], off offset:64
	global_load_dwordx2 v[184:185], v[142:143], off offset:96
	v_add_u32_e32 v142, 48, v138
	v_ashrrev_i32_e32 v143, 31, v142
	v_lshlrev_b64 v[142:143], 11, v[142:143]
	v_lshl_add_u64 v[142:143], s[6:7], 0, v[142:143]
	v_lshl_add_u64 v[142:143], v[142:143], 0, v[140:141]
	global_load_dwordx2 v[182:183], v[142:143], off
	global_load_dwordx2 v[180:181], v[142:143], off offset:32
	global_load_dwordx2 v[178:179], v[142:143], off offset:64
	global_load_dwordx2 v[176:177], v[142:143], off offset:96
	v_add_u32_e32 v142, 64, v138
	v_ashrrev_i32_e32 v143, 31, v142
	v_lshlrev_b64 v[142:143], 11, v[142:143]
	v_lshl_add_u64 v[142:143], s[6:7], 0, v[142:143]
	v_lshl_add_u64 v[142:143], v[142:143], 0, v[140:141]
	global_load_dwordx2 v[174:175], v[142:143], off
	global_load_dwordx2 v[172:173], v[142:143], off offset:32
	global_load_dwordx2 v[168:169], v[142:143], off offset:64
	global_load_dwordx2 v[166:167], v[142:143], off offset:96
	v_add_u32_e32 v142, 0x50, v138
	v_ashrrev_i32_e32 v143, 31, v142
	v_lshlrev_b64 v[142:143], 11, v[142:143]
	v_lshl_add_u64 v[142:143], s[6:7], 0, v[142:143]
	v_lshl_add_u64 v[142:143], v[142:143], 0, v[140:141]
	global_load_dwordx2 v[164:165], v[142:143], off
	global_load_dwordx2 v[162:163], v[142:143], off offset:32
	global_load_dwordx2 v[160:161], v[142:143], off offset:64
	global_load_dwordx2 v[156:157], v[142:143], off offset:96
	v_add_u32_e32 v215, s25, v144
	v_lshlrev_b32_e32 v222, 3, v145
	v_mul_lo_u32 v215, v215, s18
	v_add3_u32 v215, s24, v222, v215
	v_add_u32_e32 v142, 0x60, v138
	v_add_u32_e32 v138, 0x70, v138
	v_ashrrev_i32_e32 v143, 31, v142
	v_ashrrev_i32_e32 v139, 31, v138
	v_lshlrev_b64 v[142:143], 11, v[142:143]
	v_lshlrev_b64 v[138:139], 11, v[138:139]
	v_lshl_add_u64 v[142:143], s[6:7], 0, v[142:143]
	v_lshl_add_u64 v[138:139], s[6:7], 0, v[138:139]
	v_lshl_add_u64 v[142:143], v[142:143], 0, v[140:141]
	v_lshl_add_u64 v[138:139], v[138:139], 0, v[140:141]
	global_load_dwordx2 v[154:155], v[142:143], off
	global_load_dwordx2 v[152:153], v[142:143], off offset:32
	global_load_dwordx2 v[150:151], v[142:143], off offset:64
	global_load_dwordx2 v[148:149], v[142:143], off offset:96
	global_load_dwordx2 v[144:145], v[138:139], off
	s_nop 0
	global_load_dwordx2 v[142:143], v[138:139], off offset:32
	global_load_dwordx2 v[140:141], v[138:139], off offset:64
	s_nop 0
	global_load_dwordx2 v[138:139], v[138:139], off offset:96
	s_lshl_b32 s2, s22, 1
	s_waitcnt vmcnt(34)
	v_pk_add_f32 v[224:225], v[250:251], v[32:33]
	v_pk_add_f32 v[226:227], v[248:249], v[30:31]
	v_pk_mul_f32 v[224:225], v[224:225], s[14:15] op_sel_hi:[1,0]
	v_pk_mul_f32 v[226:227], v[226:227], s[14:15] op_sel_hi:[1,0]
	v_exp_f32_e32 v224, v224
	v_exp_f32_e32 v226, v226
	v_exp_f32_e32 v227, v227
	v_exp_f32_e32 v225, v225
	s_waitcnt vmcnt(33)
	v_pk_add_f32 v[202:203], v[202:203], v[22:23]
	v_pk_add_f32 v[204:205], v[204:205], v[24:25]
	v_pk_mul_f32 v[202:203], v[202:203], s[14:15] op_sel_hi:[1,0]
	v_pk_mul_f32 v[204:205], v[204:205], s[14:15] op_sel_hi:[1,0]
	v_exp_f32_e32 v202, v202
	v_exp_f32_e32 v203, v203
	v_exp_f32_e32 v204, v204
	v_exp_f32_e32 v205, v205
	v_pk_add_f32 v[226:227], v[226:227], 1.0 op_sel_hi:[1,0]
	v_pk_add_f32 v[224:225], v[224:225], 1.0 op_sel_hi:[1,0]
	s_waitcnt vmcnt(32)
	v_pk_add_f32 v[134:135], v[134:135], v[14:15]
	v_rcp_f32_e32 v226, v226
	v_rcp_f32_e32 v227, v227
	v_rcp_f32_e32 v224, v224
	v_rcp_f32_e32 v225, v225
	v_pk_add_f32 v[136:137], v[136:137], v[16:17]
	v_pk_mul_f32 v[134:135], v[134:135], s[14:15] op_sel_hi:[1,0]
	v_pk_add_f32 v[202:203], v[202:203], 1.0 op_sel_hi:[1,0]
	v_exp_f32_e32 v134, v134
	v_exp_f32_e32 v135, v135
	v_pk_mul_f32 v[136:137], v[136:137], s[14:15] op_sel_hi:[1,0]
	v_rcp_f32_e32 v202, v202
	v_rcp_f32_e32 v203, v203
	v_pk_add_f32 v[204:205], v[204:205], 1.0 op_sel_hi:[1,0]
	v_exp_f32_e32 v136, v136
	v_exp_f32_e32 v137, v137
	s_waitcnt vmcnt(31)
	v_pk_add_f32 v[130:131], v[130:131], v[6:7]
	v_lshlrev_b32_e32 v222, 16, v216
	v_and_b32_e32 v223, 0xffff0000, v216
	v_lshlrev_b32_e32 v216, 16, v217
	v_and_b32_e32 v217, 0xffff0000, v217
	v_rcp_f32_e32 v204, v204
	v_rcp_f32_e32 v205, v205
	v_pk_add_f32 v[132:133], v[132:133], v[8:9]
	v_pk_mul_f32 v[130:131], v[130:131], s[14:15] op_sel_hi:[1,0]
	v_pk_mul_f32 v[222:223], v[226:227], v[222:223]
	v_pk_mul_f32 v[216:217], v[224:225], v[216:217]
	v_exp_f32_e32 v130, v130
	v_exp_f32_e32 v131, v131
	v_pk_mul_f32 v[132:133], v[132:133], s[14:15] op_sel_hi:[1,0]
	v_cvt_pk_bf16_f32 v222, v222, v223
	v_cvt_pk_bf16_f32 v223, v216, v217
	s_waitcnt vmcnt(30)
	v_lshlrev_b32_e32 v216, 16, v218
	v_and_b32_e32 v217, 0xffff0000, v218
	v_pk_add_f32 v[134:135], v[134:135], 1.0 op_sel_hi:[1,0]
	v_exp_f32_e32 v132, v132
	v_exp_f32_e32 v133, v133
	v_pk_mul_f32 v[202:203], v[202:203], v[216:217]
	v_lshlrev_b32_e32 v216, 16, v219
	v_and_b32_e32 v217, 0xffff0000, v219
	v_rcp_f32_e32 v134, v134
	v_rcp_f32_e32 v135, v135
	v_pk_add_f32 v[136:137], v[136:137], 1.0 op_sel_hi:[1,0]
	v_pk_add_f32 v[126:127], v[126:127], v[30:31]
	v_pk_mul_f32 v[204:205], v[204:205], v[216:217]
	v_rcp_f32_e32 v136, v136
	v_rcp_f32_e32 v137, v137
	v_pk_add_f32 v[128:129], v[128:129], v[32:33]
	v_pk_mul_f32 v[126:127], v[126:127], s[14:15] op_sel_hi:[1,0]
	v_cvt_pk_bf16_f32 v202, v202, v203
	v_cvt_pk_bf16_f32 v203, v204, v205
	v_pk_add_f32 v[130:131], v[130:131], 1.0 op_sel_hi:[1,0]
	v_exp_f32_e32 v126, v126
	v_exp_f32_e32 v127, v127
	v_pk_mul_f32 v[128:129], v[128:129], s[14:15] op_sel_hi:[1,0]
	ds_write2_b64 v215, v[222:223], v[202:203] offset1:4
	s_waitcnt vmcnt(29)
	v_lshlrev_b32_e32 v202, 16, v220
	v_and_b32_e32 v203, 0xffff0000, v220
	v_rcp_f32_e32 v130, v130
	v_rcp_f32_e32 v131, v131
	v_pk_add_f32 v[132:133], v[132:133], 1.0 op_sel_hi:[1,0]
	v_exp_f32_e32 v128, v128
	v_exp_f32_e32 v129, v129
	v_pk_add_f32 v[122:123], v[122:123], v[22:23]
	v_pk_mul_f32 v[134:135], v[134:135], v[202:203]
	v_lshlrev_b32_e32 v202, 16, v221
	v_and_b32_e32 v203, 0xffff0000, v221
	v_rcp_f32_e32 v132, v132
	v_rcp_f32_e32 v133, v133
	v_pk_add_f32 v[124:125], v[124:125], v[24:25]
	v_pk_mul_f32 v[122:123], v[122:123], s[14:15] op_sel_hi:[1,0]
	v_pk_mul_f32 v[136:137], v[136:137], v[202:203]
	v_exp_f32_e32 v122, v122
	v_exp_f32_e32 v123, v123
	v_pk_mul_f32 v[124:125], v[124:125], s[14:15] op_sel_hi:[1,0]
	v_cvt_pk_bf16_f32 v134, v134, v135
	v_cvt_pk_bf16_f32 v135, v136, v137
	s_waitcnt vmcnt(28)
	v_lshlrev_b32_e32 v136, 16, v200
	v_and_b32_e32 v137, 0xffff0000, v200
	v_pk_add_f32 v[126:127], v[126:127], 1.0 op_sel_hi:[1,0]
	v_exp_f32_e32 v124, v124
	v_exp_f32_e32 v125, v125
	v_pk_mul_f32 v[130:131], v[130:131], v[136:137]
	v_lshlrev_b32_e32 v136, 16, v201
	v_and_b32_e32 v137, 0xffff0000, v201
	v_rcp_f32_e32 v126, v126
	v_rcp_f32_e32 v127, v127
	v_pk_add_f32 v[128:129], v[128:129], 1.0 op_sel_hi:[1,0]
	v_pk_add_f32 v[118:119], v[118:119], v[14:15]
	v_pk_mul_f32 v[132:133], v[132:133], v[136:137]
	v_rcp_f32_e32 v128, v128
	v_rcp_f32_e32 v129, v129
	v_pk_add_f32 v[120:121], v[120:121], v[16:17]
	v_pk_mul_f32 v[118:119], v[118:119], s[14:15] op_sel_hi:[1,0]
	v_cvt_pk_bf16_f32 v130, v130, v131
	v_cvt_pk_bf16_f32 v131, v132, v133
	v_pk_add_f32 v[122:123], v[122:123], 1.0 op_sel_hi:[1,0]
	v_exp_f32_e32 v118, v118
	v_exp_f32_e32 v119, v119
	v_pk_mul_f32 v[120:121], v[120:121], s[14:15] op_sel_hi:[1,0]
	ds_write2_b64 v215, v[134:135], v[130:131] offset0:8 offset1:12
	s_waitcnt vmcnt(27)
	v_lshlrev_b32_e32 v130, 16, v198
	v_and_b32_e32 v131, 0xffff0000, v198
	v_rcp_f32_e32 v122, v122
	v_rcp_f32_e32 v123, v123
	v_pk_add_f32 v[124:125], v[124:125], 1.0 op_sel_hi:[1,0]
	v_exp_f32_e32 v120, v120
	v_exp_f32_e32 v121, v121
	v_pk_add_f32 v[114:115], v[114:115], v[6:7]
	v_pk_mul_f32 v[126:127], v[126:127], v[130:131]
	v_lshlrev_b32_e32 v130, 16, v199
	v_and_b32_e32 v131, 0xffff0000, v199
	v_rcp_f32_e32 v124, v124
	v_rcp_f32_e32 v125, v125
	v_pk_add_f32 v[116:117], v[116:117], v[8:9]
	v_pk_mul_f32 v[114:115], v[114:115], s[14:15] op_sel_hi:[1,0]
	v_pk_mul_f32 v[128:129], v[128:129], v[130:131]
	v_exp_f32_e32 v114, v114
	v_exp_f32_e32 v115, v115
	v_pk_mul_f32 v[116:117], v[116:117], s[14:15] op_sel_hi:[1,0]
	v_cvt_pk_bf16_f32 v126, v126, v127
	v_cvt_pk_bf16_f32 v127, v128, v129
	s_waitcnt vmcnt(26)
	v_lshlrev_b32_e32 v128, 16, v196
	v_and_b32_e32 v129, 0xffff0000, v196
	v_pk_add_f32 v[118:119], v[118:119], 1.0 op_sel_hi:[1,0]
	v_exp_f32_e32 v116, v116
	v_exp_f32_e32 v117, v117
	v_pk_mul_f32 v[122:123], v[122:123], v[128:129]
	v_lshlrev_b32_e32 v128, 16, v197
	v_and_b32_e32 v129, 0xffff0000, v197
	v_rcp_f32_e32 v118, v118
	v_rcp_f32_e32 v119, v119
	v_pk_add_f32 v[120:121], v[120:121], 1.0 op_sel_hi:[1,0]
	v_pk_add_f32 v[110:111], v[110:111], v[30:31]
	v_pk_mul_f32 v[124:125], v[124:125], v[128:129]
	v_rcp_f32_e32 v120, v120
	v_rcp_f32_e32 v121, v121
	v_pk_add_f32 v[112:113], v[112:113], v[32:33]
	v_pk_mul_f32 v[110:111], v[110:111], s[14:15] op_sel_hi:[1,0]
	v_cvt_pk_bf16_f32 v122, v122, v123
	v_cvt_pk_bf16_f32 v123, v124, v125
	v_add_u32_e32 v124, 0x2000, v215
	v_pk_add_f32 v[114:115], v[114:115], 1.0 op_sel_hi:[1,0]
	v_exp_f32_e32 v110, v110
	v_exp_f32_e32 v111, v111
	v_pk_mul_f32 v[112:113], v[112:113], s[14:15] op_sel_hi:[1,0]
	ds_write2_b64 v124, v[126:127], v[122:123] offset0:32 offset1:36
	s_waitcnt vmcnt(25)
	v_lshlrev_b32_e32 v122, 16, v194
	v_and_b32_e32 v123, 0xffff0000, v194
	v_rcp_f32_e32 v114, v114
	v_rcp_f32_e32 v115, v115
	v_pk_add_f32 v[116:117], v[116:117], 1.0 op_sel_hi:[1,0]
	v_exp_f32_e32 v112, v112
	v_exp_f32_e32 v113, v113
	v_pk_add_f32 v[106:107], v[106:107], v[22:23]
	v_pk_mul_f32 v[118:119], v[118:119], v[122:123]
	v_lshlrev_b32_e32 v122, 16, v195
	v_and_b32_e32 v123, 0xffff0000, v195
	v_rcp_f32_e32 v116, v116
	v_rcp_f32_e32 v117, v117
	v_pk_add_f32 v[108:109], v[108:109], v[24:25]
	v_pk_mul_f32 v[106:107], v[106:107], s[14:15] op_sel_hi:[1,0]
	v_pk_mul_f32 v[120:121], v[120:121], v[122:123]
	v_exp_f32_e32 v106, v106
	v_exp_f32_e32 v107, v107
	v_pk_mul_f32 v[108:109], v[108:109], s[14:15] op_sel_hi:[1,0]
	v_cvt_pk_bf16_f32 v118, v118, v119
	v_cvt_pk_bf16_f32 v119, v120, v121
	s_waitcnt vmcnt(24)
	v_lshlrev_b32_e32 v120, 16, v192
	v_and_b32_e32 v121, 0xffff0000, v192
	v_pk_add_f32 v[110:111], v[110:111], 1.0 op_sel_hi:[1,0]
	v_exp_f32_e32 v108, v108
	v_exp_f32_e32 v109, v109
	v_pk_mul_f32 v[114:115], v[114:115], v[120:121]
	v_lshlrev_b32_e32 v120, 16, v193
	v_and_b32_e32 v121, 0xffff0000, v193
	v_rcp_f32_e32 v110, v110
	v_rcp_f32_e32 v111, v111
	v_pk_add_f32 v[112:113], v[112:113], 1.0 op_sel_hi:[1,0]
	v_pk_add_f32 v[102:103], v[102:103], v[14:15]
	v_pk_mul_f32 v[116:117], v[116:117], v[120:121]
	v_rcp_f32_e32 v112, v112
	v_rcp_f32_e32 v113, v113
	v_pk_add_f32 v[104:105], v[104:105], v[16:17]
	v_pk_mul_f32 v[102:103], v[102:103], s[14:15] op_sel_hi:[1,0]
	v_cvt_pk_bf16_f32 v114, v114, v115
	v_cvt_pk_bf16_f32 v115, v116, v117
	v_pk_add_f32 v[106:107], v[106:107], 1.0 op_sel_hi:[1,0]
	v_exp_f32_e32 v102, v102
	v_exp_f32_e32 v103, v103
	v_pk_mul_f32 v[104:105], v[104:105], s[14:15] op_sel_hi:[1,0]
	ds_write2_b64 v124, v[118:119], v[114:115] offset0:40 offset1:44
	s_waitcnt vmcnt(23)
	v_lshlrev_b32_e32 v114, 16, v190
	v_and_b32_e32 v115, 0xffff0000, v190
	v_rcp_f32_e32 v106, v106
	v_rcp_f32_e32 v107, v107
	v_pk_add_f32 v[108:109], v[108:109], 1.0 op_sel_hi:[1,0]
	v_exp_f32_e32 v104, v104
	v_exp_f32_e32 v105, v105
	v_pk_add_f32 v[98:99], v[98:99], v[6:7]
	v_pk_mul_f32 v[110:111], v[110:111], v[114:115]
	v_lshlrev_b32_e32 v114, 16, v191
	v_and_b32_e32 v115, 0xffff0000, v191
	v_rcp_f32_e32 v108, v108
	v_rcp_f32_e32 v109, v109
	v_pk_add_f32 v[100:101], v[100:101], v[8:9]
	v_pk_mul_f32 v[98:99], v[98:99], s[14:15] op_sel_hi:[1,0]
	v_pk_mul_f32 v[112:113], v[112:113], v[114:115]
	v_exp_f32_e32 v98, v98
	v_exp_f32_e32 v99, v99
	v_pk_mul_f32 v[100:101], v[100:101], s[14:15] op_sel_hi:[1,0]
	v_cvt_pk_bf16_f32 v110, v110, v111
	v_cvt_pk_bf16_f32 v111, v112, v113
	s_waitcnt vmcnt(22)
	v_lshlrev_b32_e32 v112, 16, v188
	v_and_b32_e32 v113, 0xffff0000, v188
	v_pk_add_f32 v[102:103], v[102:103], 1.0 op_sel_hi:[1,0]
	v_exp_f32_e32 v100, v100
	v_exp_f32_e32 v101, v101
	v_pk_mul_f32 v[106:107], v[106:107], v[112:113]
	v_lshlrev_b32_e32 v112, 16, v189
	v_and_b32_e32 v113, 0xffff0000, v189
	v_rcp_f32_e32 v102, v102
	v_rcp_f32_e32 v103, v103
	v_pk_add_f32 v[104:105], v[104:105], 1.0 op_sel_hi:[1,0]
	v_pk_add_f32 v[94:95], v[94:95], v[30:31]
	v_pk_mul_f32 v[108:109], v[108:109], v[112:113]
	v_rcp_f32_e32 v104, v104
	v_rcp_f32_e32 v105, v105
	v_pk_add_f32 v[96:97], v[96:97], v[32:33]
	v_pk_mul_f32 v[94:95], v[94:95], s[14:15] op_sel_hi:[1,0]
	v_cvt_pk_bf16_f32 v106, v106, v107
	v_cvt_pk_bf16_f32 v107, v108, v109
	v_add_u32_e32 v108, 0x4000, v215
	v_pk_add_f32 v[98:99], v[98:99], 1.0 op_sel_hi:[1,0]
	v_exp_f32_e32 v94, v94
	v_exp_f32_e32 v95, v95
	v_pk_mul_f32 v[96:97], v[96:97], s[14:15] op_sel_hi:[1,0]
	ds_write2_b64 v108, v[110:111], v[106:107] offset0:64 offset1:68
	s_waitcnt vmcnt(21)
	v_lshlrev_b32_e32 v106, 16, v186
	v_and_b32_e32 v107, 0xffff0000, v186
	v_rcp_f32_e32 v98, v98
	v_rcp_f32_e32 v99, v99
	v_pk_add_f32 v[100:101], v[100:101], 1.0 op_sel_hi:[1,0]
	v_exp_f32_e32 v96, v96
	v_exp_f32_e32 v97, v97
	v_pk_add_f32 v[90:91], v[90:91], v[22:23]
	v_pk_mul_f32 v[102:103], v[102:103], v[106:107]
	v_lshlrev_b32_e32 v106, 16, v187
	v_and_b32_e32 v107, 0xffff0000, v187
	v_rcp_f32_e32 v100, v100
	v_rcp_f32_e32 v101, v101
	v_pk_add_f32 v[92:93], v[92:93], v[24:25]
	v_pk_mul_f32 v[90:91], v[90:91], s[14:15] op_sel_hi:[1,0]
	v_pk_mul_f32 v[104:105], v[104:105], v[106:107]
	v_exp_f32_e32 v90, v90
	v_exp_f32_e32 v91, v91
	v_pk_mul_f32 v[92:93], v[92:93], s[14:15] op_sel_hi:[1,0]
	v_cvt_pk_bf16_f32 v102, v102, v103
	v_cvt_pk_bf16_f32 v103, v104, v105
	s_waitcnt vmcnt(20)
	v_lshlrev_b32_e32 v104, 16, v184
	v_and_b32_e32 v105, 0xffff0000, v184
	v_pk_add_f32 v[94:95], v[94:95], 1.0 op_sel_hi:[1,0]
	v_exp_f32_e32 v92, v92
	v_exp_f32_e32 v93, v93
	v_pk_mul_f32 v[98:99], v[98:99], v[104:105]
	v_lshlrev_b32_e32 v104, 16, v185
	v_and_b32_e32 v105, 0xffff0000, v185
	v_rcp_f32_e32 v94, v94
	v_rcp_f32_e32 v95, v95
	v_pk_add_f32 v[96:97], v[96:97], 1.0 op_sel_hi:[1,0]
	v_pk_add_f32 v[86:87], v[86:87], v[14:15]
	v_pk_mul_f32 v[100:101], v[100:101], v[104:105]
	v_rcp_f32_e32 v96, v96
	v_rcp_f32_e32 v97, v97
	v_pk_add_f32 v[88:89], v[88:89], v[16:17]
	v_pk_mul_f32 v[86:87], v[86:87], s[14:15] op_sel_hi:[1,0]
	v_cvt_pk_bf16_f32 v98, v98, v99
	v_cvt_pk_bf16_f32 v99, v100, v101
	v_pk_add_f32 v[90:91], v[90:91], 1.0 op_sel_hi:[1,0]
	v_exp_f32_e32 v86, v86
	v_exp_f32_e32 v87, v87
	v_pk_mul_f32 v[88:89], v[88:89], s[14:15] op_sel_hi:[1,0]
	ds_write2_b64 v108, v[102:103], v[98:99] offset0:72 offset1:76
	s_waitcnt vmcnt(19)
	v_lshlrev_b32_e32 v98, 16, v182
	v_and_b32_e32 v99, 0xffff0000, v182
	v_rcp_f32_e32 v90, v90
	v_rcp_f32_e32 v91, v91
	v_pk_add_f32 v[92:93], v[92:93], 1.0 op_sel_hi:[1,0]
	v_exp_f32_e32 v88, v88
	v_exp_f32_e32 v89, v89
	v_pk_add_f32 v[82:83], v[82:83], v[6:7]
	v_pk_mul_f32 v[94:95], v[94:95], v[98:99]
	v_lshlrev_b32_e32 v98, 16, v183
	v_and_b32_e32 v99, 0xffff0000, v183
	v_rcp_f32_e32 v92, v92
	v_rcp_f32_e32 v93, v93
	v_pk_add_f32 v[84:85], v[84:85], v[8:9]
	v_pk_mul_f32 v[82:83], v[82:83], s[14:15] op_sel_hi:[1,0]
	v_pk_mul_f32 v[96:97], v[96:97], v[98:99]
	v_exp_f32_e32 v82, v82
	v_exp_f32_e32 v83, v83
	v_pk_mul_f32 v[84:85], v[84:85], s[14:15] op_sel_hi:[1,0]
	v_cvt_pk_bf16_f32 v94, v94, v95
	v_cvt_pk_bf16_f32 v95, v96, v97
	s_waitcnt vmcnt(18)
	v_lshlrev_b32_e32 v96, 16, v180
	v_and_b32_e32 v97, 0xffff0000, v180
	v_pk_add_f32 v[86:87], v[86:87], 1.0 op_sel_hi:[1,0]
	v_exp_f32_e32 v84, v84
	v_exp_f32_e32 v85, v85
	v_pk_mul_f32 v[90:91], v[90:91], v[96:97]
	v_lshlrev_b32_e32 v96, 16, v181
	v_and_b32_e32 v97, 0xffff0000, v181
	v_rcp_f32_e32 v86, v86
	v_rcp_f32_e32 v87, v87
	v_pk_add_f32 v[88:89], v[88:89], 1.0 op_sel_hi:[1,0]
	v_pk_add_f32 v[78:79], v[78:79], v[30:31]
	v_pk_mul_f32 v[92:93], v[92:93], v[96:97]
	v_rcp_f32_e32 v88, v88
	v_rcp_f32_e32 v89, v89
	v_pk_add_f32 v[80:81], v[80:81], v[32:33]
	v_pk_mul_f32 v[78:79], v[78:79], s[14:15] op_sel_hi:[1,0]
	v_cvt_pk_bf16_f32 v90, v90, v91
	v_cvt_pk_bf16_f32 v91, v92, v93
	v_add_u32_e32 v92, 0x6000, v215
	v_pk_add_f32 v[82:83], v[82:83], 1.0 op_sel_hi:[1,0]
	v_exp_f32_e32 v78, v78
	v_exp_f32_e32 v79, v79
	v_pk_mul_f32 v[80:81], v[80:81], s[14:15] op_sel_hi:[1,0]
	ds_write2_b64 v92, v[94:95], v[90:91] offset0:96 offset1:100
	s_waitcnt vmcnt(17)
	v_lshlrev_b32_e32 v90, 16, v178
	v_and_b32_e32 v91, 0xffff0000, v178
	v_rcp_f32_e32 v82, v82
	v_rcp_f32_e32 v83, v83
	v_pk_add_f32 v[84:85], v[84:85], 1.0 op_sel_hi:[1,0]
	v_exp_f32_e32 v80, v80
	v_exp_f32_e32 v81, v81
	v_pk_add_f32 v[74:75], v[74:75], v[22:23]
	v_pk_mul_f32 v[86:87], v[86:87], v[90:91]
	v_lshlrev_b32_e32 v90, 16, v179
	v_and_b32_e32 v91, 0xffff0000, v179
	v_rcp_f32_e32 v84, v84
	v_rcp_f32_e32 v85, v85
	v_pk_add_f32 v[76:77], v[76:77], v[24:25]
	v_pk_mul_f32 v[74:75], v[74:75], s[14:15] op_sel_hi:[1,0]
	v_pk_mul_f32 v[88:89], v[88:89], v[90:91]
	v_exp_f32_e32 v74, v74
	v_exp_f32_e32 v75, v75
	v_pk_mul_f32 v[76:77], v[76:77], s[14:15] op_sel_hi:[1,0]
	v_cvt_pk_bf16_f32 v86, v86, v87
	v_cvt_pk_bf16_f32 v87, v88, v89
	s_waitcnt vmcnt(16)
	v_lshlrev_b32_e32 v88, 16, v176
	v_and_b32_e32 v89, 0xffff0000, v176
	v_pk_add_f32 v[78:79], v[78:79], 1.0 op_sel_hi:[1,0]
	v_exp_f32_e32 v76, v76
	v_exp_f32_e32 v77, v77
	v_pk_mul_f32 v[82:83], v[82:83], v[88:89]
	v_lshlrev_b32_e32 v88, 16, v177
	v_and_b32_e32 v89, 0xffff0000, v177
	v_rcp_f32_e32 v78, v78
	v_rcp_f32_e32 v79, v79
	v_pk_add_f32 v[80:81], v[80:81], 1.0 op_sel_hi:[1,0]
	v_pk_add_f32 v[70:71], v[70:71], v[14:15]
	v_pk_mul_f32 v[84:85], v[84:85], v[88:89]
	v_rcp_f32_e32 v80, v80
	v_rcp_f32_e32 v81, v81
	v_pk_add_f32 v[72:73], v[72:73], v[16:17]
	v_pk_mul_f32 v[70:71], v[70:71], s[14:15] op_sel_hi:[1,0]
	v_cvt_pk_bf16_f32 v82, v82, v83
	v_cvt_pk_bf16_f32 v83, v84, v85
	v_pk_add_f32 v[74:75], v[74:75], 1.0 op_sel_hi:[1,0]
	v_exp_f32_e32 v70, v70
	v_exp_f32_e32 v71, v71
	v_pk_mul_f32 v[72:73], v[72:73], s[14:15] op_sel_hi:[1,0]
	ds_write2_b64 v92, v[86:87], v[82:83] offset0:104 offset1:108
	s_waitcnt vmcnt(15)
	v_lshlrev_b32_e32 v82, 16, v174
	v_and_b32_e32 v83, 0xffff0000, v174
	v_rcp_f32_e32 v74, v74
	v_rcp_f32_e32 v75, v75
	v_pk_add_f32 v[76:77], v[76:77], 1.0 op_sel_hi:[1,0]
	v_exp_f32_e32 v72, v72
	v_exp_f32_e32 v73, v73
	v_pk_add_f32 v[66:67], v[66:67], v[6:7]
	v_pk_mul_f32 v[78:79], v[78:79], v[82:83]
	v_lshlrev_b32_e32 v82, 16, v175
	v_and_b32_e32 v83, 0xffff0000, v175
	v_rcp_f32_e32 v76, v76
	v_rcp_f32_e32 v77, v77
	v_pk_add_f32 v[68:69], v[68:69], v[8:9]
	v_pk_mul_f32 v[66:67], v[66:67], s[14:15] op_sel_hi:[1,0]
	v_pk_mul_f32 v[80:81], v[80:81], v[82:83]
	v_exp_f32_e32 v66, v66
	v_exp_f32_e32 v67, v67
	v_pk_mul_f32 v[68:69], v[68:69], s[14:15] op_sel_hi:[1,0]
	v_cvt_pk_bf16_f32 v78, v78, v79
	v_cvt_pk_bf16_f32 v79, v80, v81
	s_waitcnt vmcnt(14)
	v_lshlrev_b32_e32 v80, 16, v172
	v_and_b32_e32 v81, 0xffff0000, v172
	v_pk_add_f32 v[70:71], v[70:71], 1.0 op_sel_hi:[1,0]
	v_exp_f32_e32 v68, v68
	v_exp_f32_e32 v69, v69
	v_pk_mul_f32 v[74:75], v[74:75], v[80:81]
	v_lshlrev_b32_e32 v80, 16, v173
	v_and_b32_e32 v81, 0xffff0000, v173
	v_rcp_f32_e32 v70, v70
	v_rcp_f32_e32 v71, v71
	v_pk_add_f32 v[72:73], v[72:73], 1.0 op_sel_hi:[1,0]
	v_pk_add_f32 v[62:63], v[62:63], v[30:31]
	v_pk_mul_f32 v[76:77], v[76:77], v[80:81]
	v_rcp_f32_e32 v72, v72
	v_rcp_f32_e32 v73, v73
	v_pk_add_f32 v[64:65], v[64:65], v[32:33]
	v_pk_mul_f32 v[62:63], v[62:63], s[14:15] op_sel_hi:[1,0]
	v_cvt_pk_bf16_f32 v74, v74, v75
	v_cvt_pk_bf16_f32 v75, v76, v77
	v_add_u32_e32 v76, 0x8000, v215
	v_pk_add_f32 v[66:67], v[66:67], 1.0 op_sel_hi:[1,0]
	v_exp_f32_e32 v62, v62
	v_exp_f32_e32 v63, v63
	v_pk_mul_f32 v[64:65], v[64:65], s[14:15] op_sel_hi:[1,0]
	ds_write2_b64 v76, v[78:79], v[74:75] offset0:128 offset1:132
	s_waitcnt vmcnt(13)
	v_lshlrev_b32_e32 v74, 16, v168
	v_and_b32_e32 v75, 0xffff0000, v168
	v_rcp_f32_e32 v66, v66
	v_rcp_f32_e32 v67, v67
	v_pk_add_f32 v[68:69], v[68:69], 1.0 op_sel_hi:[1,0]
	v_exp_f32_e32 v64, v64
	v_exp_f32_e32 v65, v65
	v_pk_add_f32 v[58:59], v[58:59], v[22:23]
	v_pk_mul_f32 v[70:71], v[70:71], v[74:75]
	v_lshlrev_b32_e32 v74, 16, v169
	v_and_b32_e32 v75, 0xffff0000, v169
	v_rcp_f32_e32 v68, v68
	v_rcp_f32_e32 v69, v69
	v_pk_add_f32 v[60:61], v[60:61], v[24:25]
	v_pk_mul_f32 v[58:59], v[58:59], s[14:15] op_sel_hi:[1,0]
	v_pk_mul_f32 v[72:73], v[72:73], v[74:75]
	v_exp_f32_e32 v58, v58
	v_exp_f32_e32 v59, v59
	v_pk_mul_f32 v[60:61], v[60:61], s[14:15] op_sel_hi:[1,0]
	v_cvt_pk_bf16_f32 v70, v70, v71
	v_cvt_pk_bf16_f32 v71, v72, v73
	s_waitcnt vmcnt(12)
	v_lshlrev_b32_e32 v72, 16, v166
	v_and_b32_e32 v73, 0xffff0000, v166
	v_pk_add_f32 v[62:63], v[62:63], 1.0 op_sel_hi:[1,0]
	v_exp_f32_e32 v60, v60
	v_exp_f32_e32 v61, v61
	v_pk_mul_f32 v[66:67], v[66:67], v[72:73]
	v_lshlrev_b32_e32 v72, 16, v167
	v_and_b32_e32 v73, 0xffff0000, v167
	v_rcp_f32_e32 v62, v62
	v_rcp_f32_e32 v63, v63
	v_pk_add_f32 v[64:65], v[64:65], 1.0 op_sel_hi:[1,0]
	v_pk_add_f32 v[54:55], v[54:55], v[14:15]
	v_pk_mul_f32 v[68:69], v[68:69], v[72:73]
	v_rcp_f32_e32 v64, v64
	v_rcp_f32_e32 v65, v65
	v_pk_add_f32 v[56:57], v[56:57], v[16:17]
	v_pk_mul_f32 v[54:55], v[54:55], s[14:15] op_sel_hi:[1,0]
	v_cvt_pk_bf16_f32 v66, v66, v67
	v_cvt_pk_bf16_f32 v67, v68, v69
	v_pk_add_f32 v[58:59], v[58:59], 1.0 op_sel_hi:[1,0]
	v_exp_f32_e32 v54, v54
	v_exp_f32_e32 v55, v55
	v_pk_mul_f32 v[56:57], v[56:57], s[14:15] op_sel_hi:[1,0]
	ds_write2_b64 v76, v[70:71], v[66:67] offset0:136 offset1:140
	s_waitcnt vmcnt(11)
	v_lshlrev_b32_e32 v66, 16, v164
	v_and_b32_e32 v67, 0xffff0000, v164
	v_rcp_f32_e32 v58, v58
	v_rcp_f32_e32 v59, v59
	v_pk_add_f32 v[60:61], v[60:61], 1.0 op_sel_hi:[1,0]
	v_exp_f32_e32 v56, v56
	v_exp_f32_e32 v57, v57
	v_pk_add_f32 v[50:51], v[50:51], v[6:7]
	v_pk_mul_f32 v[62:63], v[62:63], v[66:67]
	v_lshlrev_b32_e32 v66, 16, v165
	v_and_b32_e32 v67, 0xffff0000, v165
	v_rcp_f32_e32 v60, v60
	v_rcp_f32_e32 v61, v61
	v_pk_add_f32 v[52:53], v[52:53], v[8:9]
	v_pk_mul_f32 v[50:51], v[50:51], s[14:15] op_sel_hi:[1,0]
	v_pk_mul_f32 v[64:65], v[64:65], v[66:67]
	v_exp_f32_e32 v50, v50
	v_exp_f32_e32 v51, v51
	v_pk_mul_f32 v[52:53], v[52:53], s[14:15] op_sel_hi:[1,0]
	v_cvt_pk_bf16_f32 v62, v62, v63
	v_cvt_pk_bf16_f32 v63, v64, v65
	s_waitcnt vmcnt(10)
	v_lshlrev_b32_e32 v64, 16, v162
	v_and_b32_e32 v65, 0xffff0000, v162
	v_pk_add_f32 v[54:55], v[54:55], 1.0 op_sel_hi:[1,0]
	v_exp_f32_e32 v52, v52
	v_exp_f32_e32 v53, v53
	v_pk_mul_f32 v[58:59], v[58:59], v[64:65]
	v_lshlrev_b32_e32 v64, 16, v163
	v_and_b32_e32 v65, 0xffff0000, v163
	v_rcp_f32_e32 v54, v54
	v_rcp_f32_e32 v55, v55
	v_pk_add_f32 v[56:57], v[56:57], 1.0 op_sel_hi:[1,0]
	v_pk_add_f32 v[46:47], v[46:47], v[30:31]
	v_pk_mul_f32 v[60:61], v[60:61], v[64:65]
	v_rcp_f32_e32 v56, v56
	v_rcp_f32_e32 v57, v57
	v_pk_add_f32 v[48:49], v[48:49], v[32:33]
	v_pk_mul_f32 v[46:47], v[46:47], s[14:15] op_sel_hi:[1,0]
	v_cvt_pk_bf16_f32 v58, v58, v59
	v_cvt_pk_bf16_f32 v59, v60, v61
	v_add_u32_e32 v60, 0xa000, v215
	v_pk_add_f32 v[50:51], v[50:51], 1.0 op_sel_hi:[1,0]
	v_exp_f32_e32 v46, v46
	v_exp_f32_e32 v47, v47
	v_pk_mul_f32 v[48:49], v[48:49], s[14:15] op_sel_hi:[1,0]
	ds_write2_b64 v60, v[62:63], v[58:59] offset0:160 offset1:164
	s_waitcnt vmcnt(9)
	v_lshlrev_b32_e32 v58, 16, v160
	v_and_b32_e32 v59, 0xffff0000, v160
	v_rcp_f32_e32 v50, v50
	v_rcp_f32_e32 v51, v51
	v_pk_add_f32 v[52:53], v[52:53], 1.0 op_sel_hi:[1,0]
	v_exp_f32_e32 v48, v48
	v_exp_f32_e32 v49, v49
	v_pk_add_f32 v[42:43], v[42:43], v[22:23]
	v_pk_mul_f32 v[54:55], v[54:55], v[58:59]
	v_lshlrev_b32_e32 v58, 16, v161
	v_and_b32_e32 v59, 0xffff0000, v161
	v_rcp_f32_e32 v52, v52
	v_rcp_f32_e32 v53, v53
	v_pk_add_f32 v[44:45], v[44:45], v[24:25]
	v_pk_mul_f32 v[42:43], v[42:43], s[14:15] op_sel_hi:[1,0]
	v_pk_mul_f32 v[56:57], v[56:57], v[58:59]
	v_exp_f32_e32 v42, v42
	v_exp_f32_e32 v43, v43
	v_pk_mul_f32 v[44:45], v[44:45], s[14:15] op_sel_hi:[1,0]
	v_cvt_pk_bf16_f32 v54, v54, v55
	v_cvt_pk_bf16_f32 v55, v56, v57
	s_waitcnt vmcnt(8)
	v_lshlrev_b32_e32 v56, 16, v156
	v_and_b32_e32 v57, 0xffff0000, v156
	v_pk_add_f32 v[46:47], v[46:47], 1.0 op_sel_hi:[1,0]
	v_exp_f32_e32 v44, v44
	v_exp_f32_e32 v45, v45
	v_pk_mul_f32 v[50:51], v[50:51], v[56:57]
	v_lshlrev_b32_e32 v56, 16, v157
	v_and_b32_e32 v57, 0xffff0000, v157
	v_rcp_f32_e32 v46, v46
	v_rcp_f32_e32 v47, v47
	v_pk_add_f32 v[48:49], v[48:49], 1.0 op_sel_hi:[1,0]
	v_pk_add_f32 v[38:39], v[38:39], v[14:15]
	v_pk_mul_f32 v[52:53], v[52:53], v[56:57]
	v_rcp_f32_e32 v48, v48
	v_rcp_f32_e32 v49, v49
	v_pk_add_f32 v[40:41], v[40:41], v[16:17]
	v_pk_mul_f32 v[38:39], v[38:39], s[14:15] op_sel_hi:[1,0]
	v_cvt_pk_bf16_f32 v50, v50, v51
	v_cvt_pk_bf16_f32 v51, v52, v53
	v_pk_add_f32 v[42:43], v[42:43], 1.0 op_sel_hi:[1,0]
	v_exp_f32_e32 v38, v38
	v_exp_f32_e32 v39, v39
	v_pk_mul_f32 v[40:41], v[40:41], s[14:15] op_sel_hi:[1,0]
	ds_write2_b64 v60, v[54:55], v[50:51] offset0:168 offset1:172
	s_waitcnt vmcnt(7)
	v_lshlrev_b32_e32 v50, 16, v154
	v_and_b32_e32 v51, 0xffff0000, v154
	v_rcp_f32_e32 v42, v42
	v_rcp_f32_e32 v43, v43
	v_pk_add_f32 v[44:45], v[44:45], 1.0 op_sel_hi:[1,0]
	v_exp_f32_e32 v40, v40
	v_exp_f32_e32 v41, v41
	v_pk_add_f32 v[34:35], v[34:35], v[6:7]
	v_pk_mul_f32 v[46:47], v[46:47], v[50:51]
	v_lshlrev_b32_e32 v50, 16, v155
	v_and_b32_e32 v51, 0xffff0000, v155
	v_rcp_f32_e32 v44, v44
	v_rcp_f32_e32 v45, v45
	v_pk_add_f32 v[36:37], v[36:37], v[8:9]
	v_pk_mul_f32 v[34:35], v[34:35], s[14:15] op_sel_hi:[1,0]
	v_pk_mul_f32 v[48:49], v[48:49], v[50:51]
	v_exp_f32_e32 v34, v34
	v_exp_f32_e32 v35, v35
	v_pk_mul_f32 v[36:37], v[36:37], s[14:15] op_sel_hi:[1,0]
	v_cvt_pk_bf16_f32 v46, v46, v47
	v_cvt_pk_bf16_f32 v47, v48, v49
	s_waitcnt vmcnt(6)
	v_lshlrev_b32_e32 v48, 16, v152
	v_and_b32_e32 v49, 0xffff0000, v152
	v_pk_add_f32 v[38:39], v[38:39], 1.0 op_sel_hi:[1,0]
	v_exp_f32_e32 v36, v36
	v_exp_f32_e32 v37, v37
	v_pk_mul_f32 v[42:43], v[42:43], v[48:49]
	v_lshlrev_b32_e32 v48, 16, v153
	v_and_b32_e32 v49, 0xffff0000, v153
	v_rcp_f32_e32 v38, v38
	v_rcp_f32_e32 v39, v39
	v_pk_add_f32 v[40:41], v[40:41], 1.0 op_sel_hi:[1,0]
	v_pk_add_f32 v[28:29], v[28:29], v[32:33]
	v_pk_add_f32 v[26:27], v[26:27], v[30:31]
	v_pk_mul_f32 v[44:45], v[44:45], v[48:49]
	v_rcp_f32_e32 v40, v40
	v_rcp_f32_e32 v41, v41
	v_pk_mul_f32 v[26:27], v[26:27], s[14:15] op_sel_hi:[1,0]
	v_pk_mul_f32 v[28:29], v[28:29], s[14:15] op_sel_hi:[1,0]
	v_cvt_pk_bf16_f32 v42, v42, v43
	v_cvt_pk_bf16_f32 v43, v44, v45
	v_add_u32_e32 v44, 0xc000, v215
	v_pk_add_f32 v[34:35], v[34:35], 1.0 op_sel_hi:[1,0]
	v_exp_f32_e32 v26, v26
	v_exp_f32_e32 v27, v27
	v_exp_f32_e32 v28, v28
	v_exp_f32_e32 v29, v29
	v_pk_add_f32 v[20:21], v[20:21], v[24:25]
	v_pk_add_f32 v[18:19], v[18:19], v[22:23]
	ds_write2_b64 v44, v[46:47], v[42:43] offset0:192 offset1:196
	s_waitcnt vmcnt(5)
	v_lshlrev_b32_e32 v42, 16, v150
	v_and_b32_e32 v43, 0xffff0000, v150
	v_rcp_f32_e32 v34, v34
	v_rcp_f32_e32 v35, v35
	v_pk_add_f32 v[36:37], v[36:37], 1.0 op_sel_hi:[1,0]
	v_pk_mul_f32 v[18:19], v[18:19], s[14:15] op_sel_hi:[1,0]
	v_pk_mul_f32 v[20:21], v[20:21], s[14:15] op_sel_hi:[1,0]
	v_pk_mul_f32 v[38:39], v[38:39], v[42:43]
	v_lshlrev_b32_e32 v42, 16, v151
	v_and_b32_e32 v43, 0xffff0000, v151
	v_rcp_f32_e32 v36, v36
	v_rcp_f32_e32 v37, v37
	v_exp_f32_e32 v18, v18
	v_exp_f32_e32 v19, v19
	v_exp_f32_e32 v20, v20
	v_exp_f32_e32 v21, v21
	v_pk_mul_f32 v[40:41], v[40:41], v[42:43]
	v_pk_add_f32 v[12:13], v[12:13], v[16:17]
	v_pk_add_f32 v[10:11], v[10:11], v[14:15]
	v_cvt_pk_bf16_f32 v38, v38, v39
	v_cvt_pk_bf16_f32 v39, v40, v41
	s_waitcnt vmcnt(4)
	v_lshlrev_b32_e32 v40, 16, v148
	v_and_b32_e32 v41, 0xffff0000, v148
	v_pk_add_f32 v[26:27], v[26:27], 1.0 op_sel_hi:[1,0]
	v_pk_add_f32 v[28:29], v[28:29], 1.0 op_sel_hi:[1,0]
	v_pk_mul_f32 v[10:11], v[10:11], s[14:15] op_sel_hi:[1,0]
	v_pk_mul_f32 v[12:13], v[12:13], s[14:15] op_sel_hi:[1,0]
	v_pk_mul_f32 v[34:35], v[34:35], v[40:41]
	v_lshlrev_b32_e32 v40, 16, v149
	v_and_b32_e32 v41, 0xffff0000, v149
	v_rcp_f32_e32 v26, v26
	v_rcp_f32_e32 v27, v27
	v_rcp_f32_e32 v28, v28
	v_rcp_f32_e32 v29, v29
	v_exp_f32_e32 v10, v10
	v_exp_f32_e32 v11, v11
	v_exp_f32_e32 v12, v12
	v_exp_f32_e32 v13, v13
	v_pk_add_f32 v[4:5], v[4:5], v[8:9]
	v_pk_add_f32 v[2:3], v[2:3], v[6:7]
	v_pk_mul_f32 v[36:37], v[36:37], v[40:41]
	v_pk_add_f32 v[18:19], v[18:19], 1.0 op_sel_hi:[1,0]
	v_pk_add_f32 v[20:21], v[20:21], 1.0 op_sel_hi:[1,0]
	v_pk_mul_f32 v[2:3], v[2:3], s[14:15] op_sel_hi:[1,0]
	v_pk_mul_f32 v[4:5], v[4:5], s[14:15] op_sel_hi:[1,0]
	v_cvt_pk_bf16_f32 v34, v34, v35
	v_cvt_pk_bf16_f32 v35, v36, v37
	v_rcp_f32_e32 v18, v18
	v_rcp_f32_e32 v19, v19
	v_rcp_f32_e32 v20, v20
	v_rcp_f32_e32 v21, v21
	v_exp_f32_e32 v2, v2
	v_exp_f32_e32 v3, v3
	v_exp_f32_e32 v4, v4
	v_exp_f32_e32 v5, v5
	ds_write2_b64 v44, v[38:39], v[34:35] offset0:200 offset1:204
	s_waitcnt vmcnt(3)
	v_lshlrev_b32_e32 v34, 16, v144
	v_and_b32_e32 v35, 0xffff0000, v144
	v_lshlrev_b32_e32 v30, 16, v145
	v_and_b32_e32 v31, 0xffff0000, v145
	v_pk_mul_f32 v[26:27], v[26:27], v[34:35]
	v_pk_mul_f32 v[28:29], v[28:29], v[30:31]
	v_pk_add_f32 v[10:11], v[10:11], 1.0 op_sel_hi:[1,0]
	v_pk_add_f32 v[12:13], v[12:13], 1.0 op_sel_hi:[1,0]
	v_cvt_pk_bf16_f32 v26, v26, v27
	v_cvt_pk_bf16_f32 v27, v28, v29
	s_waitcnt vmcnt(2)
	v_lshlrev_b32_e32 v28, 16, v142
	v_and_b32_e32 v29, 0xffff0000, v142
	v_lshlrev_b32_e32 v22, 16, v143
	v_and_b32_e32 v23, 0xffff0000, v143
	v_rcp_f32_e32 v10, v10
	v_rcp_f32_e32 v11, v11
	v_rcp_f32_e32 v12, v12
	v_rcp_f32_e32 v13, v13
	v_pk_mul_f32 v[18:19], v[18:19], v[28:29]
	v_pk_mul_f32 v[20:21], v[20:21], v[22:23]
	v_pk_add_f32 v[2:3], v[2:3], 1.0 op_sel_hi:[1,0]
	v_pk_add_f32 v[4:5], v[4:5], 1.0 op_sel_hi:[1,0]
	v_cvt_pk_bf16_f32 v18, v18, v19
	v_cvt_pk_bf16_f32 v19, v20, v21
	v_add_u32_e32 v20, 0xe000, v215
	v_rcp_f32_e32 v2, v2
	v_rcp_f32_e32 v3, v3
	v_rcp_f32_e32 v4, v4
	v_rcp_f32_e32 v5, v5
	ds_write2_b64 v20, v[26:27], v[18:19] offset0:224 offset1:228
	s_waitcnt vmcnt(1)
	v_lshlrev_b32_e32 v18, 16, v140
	v_and_b32_e32 v19, 0xffff0000, v140
	v_lshlrev_b32_e32 v14, 16, v141
	v_and_b32_e32 v15, 0xffff0000, v141
	v_pk_mul_f32 v[10:11], v[10:11], v[18:19]
	v_pk_mul_f32 v[12:13], v[12:13], v[14:15]
	v_cvt_pk_bf16_f32 v10, v10, v11
	v_cvt_pk_bf16_f32 v11, v12, v13
	s_waitcnt vmcnt(0)
	v_lshlrev_b32_e32 v12, 16, v138
	v_and_b32_e32 v13, 0xffff0000, v138
	v_lshlrev_b32_e32 v6, 16, v139
	v_and_b32_e32 v7, 0xffff0000, v139
	v_pk_mul_f32 v[2:3], v[2:3], v[12:13]
	v_pk_mul_f32 v[4:5], v[4:5], v[6:7]
	v_cvt_pk_bf16_f32 v2, v2, v3
	v_cvt_pk_bf16_f32 v3, v4, v5
	v_lshl_or_b32 v4, s23, 5, v253
	ds_write2_b64 v20, v[10:11], v[2:3] offset0:232 offset1:236
	v_mul_lo_u32 v2, v4, s18
	s_waitcnt lgkmcnt(0)
	s_barrier
	v_add_u32_e32 v5, v211, v2
	ds_read_b128 v[14:17], v5
	s_waitcnt lgkmcnt(0)
	v_and_b32_e32 v3, 0xffff0000, v14
	v_lshlrev_b32_e32 v2, 16, v14
	v_mul_f32_e32 v3, v3, v3
	v_fmac_f32_e32 v3, v2, v2
	v_lshlrev_b32_e32 v2, 16, v15
	v_fmac_f32_e32 v3, v2, v2
	v_and_b32_e32 v2, 0xffff0000, v15
	v_fmac_f32_e32 v3, v2, v2
	v_lshlrev_b32_e32 v2, 16, v16
	v_fmac_f32_e32 v3, v2, v2
	v_and_b32_e32 v2, 0xffff0000, v16
	v_fmac_f32_e32 v3, v2, v2
	v_lshlrev_b32_e32 v2, 16, v17
	v_fmac_f32_e32 v3, v2, v2
	v_and_b32_e32 v2, 0xffff0000, v17
	v_fmac_f32_e32 v3, v2, v2
	v_and_b32_e32 v2, 64, v214
	v_add_u32_e32 v12, 64, v2
	v_xor_b32_e32 v2, 1, v214
	v_cmp_lt_i32_e64 s[0:1], v2, v12
	s_nop 1
	v_cndmask_b32_e64 v2, v214, v2, s[0:1]
	v_lshlrev_b32_e32 v6, 2, v2
	ds_bpermute_b32 v2, v6, v3
	s_waitcnt lgkmcnt(0)
	v_add_f32_e32 v2, v3, v2
	v_xor_b32_e32 v3, 2, v214
	v_cmp_lt_i32_e64 s[0:1], v3, v12
	s_nop 1
	v_cndmask_b32_e64 v3, v214, v3, s[0:1]
	v_lshlrev_b32_e32 v7, 2, v3
	ds_bpermute_b32 v3, v7, v2
	s_waitcnt lgkmcnt(0)
	v_add_f32_e32 v9, v2, v3
	v_xor_b32_e32 v2, 4, v214
	v_cmp_lt_i32_e64 s[0:1], v2, v12
	s_nop 1
	v_cndmask_b32_e64 v2, v214, v2, s[0:1]
	v_lshlrev_b32_e32 v8, 2, v2
	ds_bpermute_b32 v13, v8, v9
	v_add_u32_e32 v2, s21, v4
	v_ashrrev_i32_e32 v3, 31, v2
	v_lshlrev_b64 v[10:11], 12, v[2:3]
	v_lshl_add_u64 v[10:11], s[8:9], 0, v[10:11]
	s_waitcnt lgkmcnt(0)
	v_add_f32_e32 v13, v9, v13
	v_xor_b32_e32 v9, 8, v214
	v_cmp_lt_i32_e64 s[0:1], v9, v12
	v_lshl_add_u64 v[10:11], v[10:11], 0, s[2:3]
	v_lshl_add_u64 v[18:19], v[10:11], 0, v[146:147]
	v_cndmask_b32_e64 v9, v214, v9, s[0:1]
	v_lshlrev_b32_e32 v9, 2, v9
	ds_bpermute_b32 v20, v9, v13
	v_xor_b32_e32 v10, 16, v214
	v_cmp_lt_i32_e64 s[0:1], v10, v12
	global_store_dwordx4 v[18:19], v[14:17], off sc1
	s_nop 1
	s_waitcnt lgkmcnt(0)
	v_add_f32_e32 v11, v13, v20
	v_cndmask_b32_e64 v10, v214, v10, s[0:1]
	v_lshlrev_b32_e32 v10, 2, v10
	ds_bpermute_b32 v12, v10, v11
	s_and_saveexec_b64 s[0:1], vcc
	s_cbranch_execz .LBB0_1042
	v_lshl_add_u64 v[2:3], v[2:3], 4, s[10:11]
	s_lshl_b32 s22, s20, 2
	s_mov_b32 s23, s3
	s_waitcnt lgkmcnt(0)
	v_add_f32_e32 v11, v11, v12
	v_lshl_add_u64 v[2:3], v[2:3], 0, s[22:23]
	global_store_dword v[2:3], v11, off

.Lrot_o1:
	ds_read_b64_tr_b16 v[186:187], v154
	ds_read_b64_tr_b16 v[188:189], v154 offset:2048
	ds_read_b64_tr_b16 v[190:191], v185
	ds_read_b64_tr_b16 v[192:193], v185 offset:2048
	ds_read_b128 v[194:197], v218
	ds_read_b128 v[198:201], v218 offset:2048
	ds_read_b64_tr_b16 v[202:203], v224
	ds_read_b64_tr_b16 v[204:205], v224 offset:2048
	v_add_u32_e32 v226, s50, v153
	ds_read_b64_tr_b16 v[206:207], v226
	ds_read_b64_tr_b16 v[208:209], v226 offset:2048
	ds_read_b128 v[210:213], v218 offset:4096
	s_waitcnt lgkmcnt(6)
	v_mfma_f32_16x16x32_bf16 v[18:21], v[186:189], v[194:197], v[18:21]
	s_add_i32 s50, s48, 0
	v_add_u32_e32 v214, 0xfff40000, v152
	s_add_i32 s51, s50, s44
	v_mfma_f32_16x16x32_bf16 v[22:25], v[190:193], v[194:197], v[22:25]
	s_mov_b32 s52, m0
	s_mov_b32 m0, s51
	s_nop 0
	global_load_lds_dwordx4 v214, s[10:11]
	s_mov_b32 m0, s52
	s_waitcnt lgkmcnt(3)
	v_mfma_f32_16x16x32_bf16 v[26:29], v[202:205], v[194:197], v[26:29]
	s_waitcnt lgkmcnt(1)
	v_mfma_f32_16x16x32_bf16 v[30:33], v[206:209], v[194:197], v[30:33]
	v_mfma_f32_16x16x32_bf16 v[34:37], v[186:189], v[198:201], v[34:37]
	ds_read_b128 v[194:197], v218 offset:6144
	v_add_u32_e32 v214, 0xfff80000, v152
	s_add_i32 s51, s50, s45
	v_mfma_f32_16x16x32_bf16 v[38:41], v[190:193], v[198:201], v[38:41]
	s_mov_b32 s52, m0
	s_mov_b32 m0, s51
	s_nop 0
	global_load_lds_dwordx4 v214, s[10:11]
	s_mov_b32 m0, s52
	v_mfma_f32_16x16x32_bf16 v[42:45], v[202:205], v[198:201], v[42:45]
	v_mfma_f32_16x16x32_bf16 v[46:49], v[206:209], v[198:201], v[46:49]
	s_waitcnt lgkmcnt(1)
	v_mfma_f32_16x16x32_bf16 v[50:53], v[186:189], v[210:213], v[50:53]
	ds_read_b128 v[198:201], v218 offset:8192
	v_add_u32_e32 v214, 0xfffc0000, v152
	s_add_i32 s51, s50, s46
	v_mfma_f32_16x16x32_bf16 v[54:57], v[190:193], v[210:213], v[54:57]
	s_mov_b32 s52, m0
	s_mov_b32 m0, s51
	s_nop 0
	global_load_lds_dwordx4 v214, s[10:11]
	s_mov_b32 m0, s52
	v_mfma_f32_16x16x32_bf16 v[58:61], v[202:205], v[210:213], v[58:61]
	v_mfma_f32_16x16x32_bf16 v[62:65], v[206:209], v[210:213], v[62:65]
	s_waitcnt lgkmcnt(1)
	v_mfma_f32_16x16x32_bf16 v[66:69], v[186:189], v[194:197], v[66:69]
	ds_read_b128 v[210:213], v218 offset:10240
	s_add_i32 s50, s50, s47
	s_mov_b32 s51, m0
	s_mov_b32 m0, s50
	s_nop 0
	global_load_lds_dwordx4 v152, s[10:11]
	s_mov_b32 m0, s51
	v_mfma_f32_16x16x32_bf16 v[70:73], v[190:193], v[194:197], v[70:73]
	v_mfma_f32_16x16x32_bf16 v[74:77], v[202:205], v[194:197], v[74:77]
	v_mfma_f32_16x16x32_bf16 v[78:81], v[206:209], v[194:197], v[78:81]
	ds_read_b128 v[194:197], v218 offset:12288
	ds_read_b64_tr_b16 v[214:215], v154 offset:16384
	ds_read_b64_tr_b16 v[216:217], v154 offset:18432
	s_waitcnt lgkmcnt(4)
	v_mfma_f32_16x16x32_bf16 v[82:85], v[186:189], v[198:201], v[82:85]
	v_mfma_f32_16x16x32_bf16 v[86:89], v[190:193], v[198:201], v[86:89]
	v_mfma_f32_16x16x32_bf16 v[90:93], v[202:205], v[198:201], v[90:93]
	v_mfma_f32_16x16x32_bf16 v[94:97], v[206:209], v[198:201], v[94:97]
	ds_read_b128 v[198:201], v218 offset:14336
	ds_read_b64_tr_b16 v[218:219], v185 offset:16384
	ds_read_b64_tr_b16 v[220:221], v185 offset:18432
	s_waitcnt lgkmcnt(6)
	v_mfma_f32_16x16x32_bf16 v[98:101], v[186:189], v[210:213], v[98:101]
	v_mfma_f32_16x16x32_bf16 v[102:105], v[190:193], v[210:213], v[102:105]
	v_mfma_f32_16x16x32_bf16 v[106:109], v[202:205], v[210:213], v[106:109]
	v_mfma_f32_16x16x32_bf16 v[110:113], v[206:209], v[210:213], v[110:113]
	v_add_u32_e32 v154, s49, v162
	ds_read_b128 v[210:213], v154
	ds_read_b64_tr_b16 v[222:223], v224 offset:16384
	ds_read_b64_tr_b16 v[224:225], v224 offset:18432
	s_waitcnt lgkmcnt(8)
	v_mfma_f32_16x16x32_bf16 v[114:117], v[186:189], v[194:197], v[114:117]
	v_mfma_f32_16x16x32_bf16 v[118:121], v[190:193], v[194:197], v[118:121]
	v_mfma_f32_16x16x32_bf16 v[122:125], v[202:205], v[194:197], v[122:125]
	v_mfma_f32_16x16x32_bf16 v[126:129], v[206:209], v[194:197], v[126:129]
	s_waitcnt lgkmcnt(5)
	v_mfma_f32_16x16x32_bf16 v[130:133], v[186:189], v[198:201], v[130:133]
	ds_read_b128 v[186:189], v154 offset:2048
	s_and_b32 s49, s26, 0x8000
	v_mfma_f32_16x16x32_bf16 v[134:137], v[190:193], v[198:201], v[134:137]
	ds_read_b64_tr_b16 v[190:191], v226 offset:16384
	ds_read_b64_tr_b16 v[192:193], v226 offset:18432
	v_mfma_f32_16x16x32_bf16 v[138:141], v[202:205], v[198:201], v[138:141]
	v_mfma_f32_16x16x32_bf16 v[142:145], v[206:209], v[198:201], v[142:145]
	s_waitcnt lgkmcnt(5)
	v_mfma_f32_16x16x32_bf16 v[18:21], v[214:217], v[210:213], v[18:21]
	ds_read_b128 v[194:197], v154 offset:4096
	v_add_u32_e32 v185, s49, v163
	s_add_u32 s49, s6, s4
	v_mfma_f32_16x16x32_bf16 v[22:25], v[218:221], v[210:213], v[22:25]
	s_addc_u32 s52, s7, s5
	s_waitcnt vmcnt(7)
	s_add_u32 s50, s49, 0x80000
	s_waitcnt lgkmcnt(4)
	v_mfma_f32_16x16x32_bf16 v[26:29], v[222:225], v[210:213], v[26:29]
	ds_write_b128 v185, v[14:17]
	s_addc_u32 s51, s52, 0
	global_load_dwordx4 v[14:17], v173, s[50:51]
	s_waitcnt lgkmcnt(2)
	v_mfma_f32_16x16x32_bf16 v[30:33], v[190:193], v[210:213], v[30:33]
	v_mfma_f32_16x16x32_bf16 v[34:37], v[214:217], v[186:189], v[34:37]
	ds_read_b128 v[198:201], v154 offset:6144
	s_waitcnt vmcnt(7)
	s_add_u32 s50, s49, 0x90000
	v_mfma_f32_16x16x32_bf16 v[38:41], v[218:221], v[186:189], v[38:41]
	ds_write_b128 v185, v[10:13] offset:8192
	s_addc_u32 s51, s52, 0
	global_load_dwordx4 v[10:13], v173, s[50:51]
	v_mfma_f32_16x16x32_bf16 v[42:45], v[222:225], v[186:189], v[42:45]
	v_mfma_f32_16x16x32_bf16 v[46:49], v[190:193], v[186:189], v[46:49]
	s_waitcnt lgkmcnt(3)
	v_mfma_f32_16x16x32_bf16 v[50:53], v[214:217], v[194:197], v[50:53]
	ds_read_b128 v[186:189], v154 offset:8192
	s_waitcnt vmcnt(7)
	s_add_u32 s50, s49, 0xa0000
	v_mfma_f32_16x16x32_bf16 v[54:57], v[218:221], v[194:197], v[54:57]
	ds_write_b128 v185, v[6:9] offset:16384
	s_addc_u32 s51, s52, 0
	global_load_dwordx4 v[6:9], v173, s[50:51]
	v_mfma_f32_16x16x32_bf16 v[58:61], v[222:225], v[194:197], v[58:61]
	v_mfma_f32_16x16x32_bf16 v[62:65], v[190:193], v[194:197], v[62:65]
	s_waitcnt lgkmcnt(3)
	v_mfma_f32_16x16x32_bf16 v[66:69], v[214:217], v[198:201], v[66:69]
	ds_read_b128 v[194:197], v154 offset:10240
	s_waitcnt vmcnt(7)
	s_add_u32 s50, s49, 0xb0000
	v_mfma_f32_16x16x32_bf16 v[70:73], v[218:221], v[198:201], v[70:73]
	ds_write_b128 v185, v[2:5] offset:24576
	s_addc_u32 s51, s52, 0
	global_load_dwordx4 v[2:5], v173, s[50:51]
	v_mfma_f32_16x16x32_bf16 v[74:77], v[222:225], v[198:201], v[74:77]
	v_mfma_f32_16x16x32_bf16 v[78:81], v[190:193], v[198:201], v[78:81]
	s_waitcnt lgkmcnt(3)
	v_mfma_f32_16x16x32_bf16 v[82:85], v[214:217], v[186:189], v[82:85]
	ds_read_b128 v[198:201], v154 offset:12288
	v_mfma_f32_16x16x32_bf16 v[86:89], v[218:221], v[186:189], v[86:89]
	v_mfma_f32_16x16x32_bf16 v[90:93], v[222:225], v[186:189], v[90:93]
	v_mfma_f32_16x16x32_bf16 v[94:97], v[190:193], v[186:189], v[94:97]
	s_waitcnt lgkmcnt(2)
	v_mfma_f32_16x16x32_bf16 v[98:101], v[214:217], v[194:197], v[98:101]
	ds_read_b128 v[186:189], v154 offset:14336
	v_mfma_f32_16x16x32_bf16 v[102:105], v[218:221], v[194:197], v[102:105]
	v_mfma_f32_16x16x32_bf16 v[106:109], v[222:225], v[194:197], v[106:109]
	v_mfma_f32_16x16x32_bf16 v[110:113], v[190:193], v[194:197], v[110:113]
	s_waitcnt lgkmcnt(1)
	v_mfma_f32_16x16x32_bf16 v[114:117], v[214:217], v[198:201], v[114:117]
	v_mfma_f32_16x16x32_bf16 v[118:121], v[218:221], v[198:201], v[118:121]
	v_mfma_f32_16x16x32_bf16 v[122:125], v[222:225], v[198:201], v[122:125]
	v_mfma_f32_16x16x32_bf16 v[126:129], v[190:193], v[198:201], v[126:129]
	s_waitcnt lgkmcnt(0)
	v_mfma_f32_16x16x32_bf16 v[130:133], v[214:217], v[186:189], v[130:133]
	v_mfma_f32_16x16x32_bf16 v[134:137], v[218:221], v[186:189], v[134:137]
	v_mfma_f32_16x16x32_bf16 v[138:141], v[222:225], v[186:189], v[138:141]
	v_mfma_f32_16x16x32_bf16 v[142:145], v[190:193], v[186:189], v[142:145]
	s_add_i32 s49, s8, 0x8000
	s_cmp_lg_u32 s8, 0x10000
	s_cselect_b32 s8, s49, 0
	s_add_i32 s49, s48, 0x8000
	s_cmp_lg_u32 s48, 0x10000
	s_cselect_b32 s48, s49, 0
	s_add_u32 s4, s4, 0x40000
	s_addc_u32 s5, s5, 0
	s_add_i32 s26, s26, 0x8000
	v_add_u32_e32 v152, 0x80, v152
	s_add_i32 s50, s26, 0xffff8000
	s_and_b32 s50, s50, 0x8000
	s_add_i32 s50, s50, 0
	s_add_i32 s49, s8, 0
	s_add_i32 s50, s50, 0x18000
	v_add_u32_e32 v154, s50, v157
	v_add_u32_e32 v218, s49, v161
	v_add_u32_e32 v224, s50, v155
	v_add_u32_e32 v185, s50, v156
	s_waitcnt lgkmcnt(0)
	s_barrier
	s_cmp_eq_u32 s4, 0x400000
	s_cbranch_scc0 .Lrot_o1
	v_or_b32_e32 v152, v181, v1
	v_lshlrev_b32_e32 v185, 2, v152
	ds_bpermute_b32 v152, v185, v165
	ds_bpermute_b32 v154, v185, v165 offset:64
	ds_bpermute_b32 v186, v185, v165 offset:128
	ds_bpermute_b32 v188, v185, v184 offset:192
	ds_bpermute_b32 v190, v185, v165 offset:192
	ds_bpermute_b32 v192, v185, v184
	ds_bpermute_b32 v194, v185, v184 offset:64
	ds_bpermute_b32 v184, v185, v184 offset:128
	s_mov_b32 s8, 0
	s_waitcnt lgkmcnt(4)
	v_pk_mul_f32 v[144:145], v[144:145], v[188:189] op_sel_hi:[1,0]
	v_pk_mul_f32 v[142:143], v[142:143], v[188:189] op_sel_hi:[1,0]
	v_pk_mul_f32 v[140:141], v[140:141], v[188:189] op_sel_hi:[1,0]
	v_pk_mul_f32 v[138:139], v[138:139], v[188:189] op_sel_hi:[1,0]
	v_pk_mul_f32 v[136:137], v[136:137], v[188:189] op_sel_hi:[1,0]
	v_pk_mul_f32 v[134:135], v[134:135], v[188:189] op_sel_hi:[1,0]
	v_pk_mul_f32 v[132:133], v[132:133], v[188:189] op_sel_hi:[1,0]
	v_pk_mul_f32 v[130:131], v[130:131], v[188:189] op_sel_hi:[1,0]
	s_waitcnt lgkmcnt(0)
	v_pk_mul_f32 v[128:129], v[128:129], v[184:185] op_sel_hi:[1,0]
	v_pk_mul_f32 v[126:127], v[126:127], v[184:185] op_sel_hi:[1,0]
	v_pk_mul_f32 v[124:125], v[124:125], v[184:185] op_sel_hi:[1,0]
	v_pk_mul_f32 v[122:123], v[122:123], v[184:185] op_sel_hi:[1,0]
	v_pk_mul_f32 v[120:121], v[120:121], v[184:185] op_sel_hi:[1,0]
	v_pk_mul_f32 v[118:119], v[118:119], v[184:185] op_sel_hi:[1,0]
	v_pk_mul_f32 v[116:117], v[116:117], v[184:185] op_sel_hi:[1,0]
	v_pk_mul_f32 v[114:115], v[114:115], v[184:185] op_sel_hi:[1,0]
	v_pk_mul_f32 v[112:113], v[112:113], v[194:195] op_sel_hi:[1,0]
	v_pk_mul_f32 v[110:111], v[110:111], v[194:195] op_sel_hi:[1,0]
	v_pk_mul_f32 v[108:109], v[108:109], v[194:195] op_sel_hi:[1,0]
	v_pk_mul_f32 v[106:107], v[106:107], v[194:195] op_sel_hi:[1,0]
	v_pk_mul_f32 v[104:105], v[104:105], v[194:195] op_sel_hi:[1,0]
	v_pk_mul_f32 v[102:103], v[102:103], v[194:195] op_sel_hi:[1,0]
	v_pk_mul_f32 v[100:101], v[100:101], v[194:195] op_sel_hi:[1,0]
	v_pk_mul_f32 v[98:99], v[98:99], v[194:195] op_sel_hi:[1,0]
	v_pk_mul_f32 v[96:97], v[96:97], v[192:193] op_sel_hi:[1,0]
	v_pk_mul_f32 v[94:95], v[94:95], v[192:193] op_sel_hi:[1,0]
	v_pk_mul_f32 v[92:93], v[92:93], v[192:193] op_sel_hi:[1,0]
	v_pk_mul_f32 v[90:91], v[90:91], v[192:193] op_sel_hi:[1,0]
	v_pk_mul_f32 v[88:89], v[88:89], v[192:193] op_sel_hi:[1,0]
	v_pk_mul_f32 v[86:87], v[86:87], v[192:193] op_sel_hi:[1,0]
	v_pk_mul_f32 v[84:85], v[84:85], v[192:193] op_sel_hi:[1,0]
	v_pk_mul_f32 v[82:83], v[82:83], v[192:193] op_sel_hi:[1,0]
	v_pk_mul_f32 v[80:81], v[80:81], v[190:191] op_sel_hi:[1,0]
	v_pk_mul_f32 v[78:79], v[78:79], v[190:191] op_sel_hi:[1,0]
	v_pk_mul_f32 v[76:77], v[76:77], v[190:191] op_sel_hi:[1,0]
	v_pk_mul_f32 v[74:75], v[74:75], v[190:191] op_sel_hi:[1,0]
	v_pk_mul_f32 v[72:73], v[72:73], v[190:191] op_sel_hi:[1,0]
	v_pk_mul_f32 v[70:71], v[70:71], v[190:191] op_sel_hi:[1,0]
	v_pk_mul_f32 v[68:69], v[68:69], v[190:191] op_sel_hi:[1,0]
	v_pk_mul_f32 v[66:67], v[66:67], v[190:191] op_sel_hi:[1,0]
	v_pk_mul_f32 v[64:65], v[64:65], v[186:187] op_sel_hi:[1,0]
	v_pk_mul_f32 v[62:63], v[62:63], v[186:187] op_sel_hi:[1,0]
	v_pk_mul_f32 v[60:61], v[60:61], v[186:187] op_sel_hi:[1,0]
	v_pk_mul_f32 v[58:59], v[58:59], v[186:187] op_sel_hi:[1,0]
	v_pk_mul_f32 v[56:57], v[56:57], v[186:187] op_sel_hi:[1,0]
	v_pk_mul_f32 v[54:55], v[54:55], v[186:187] op_sel_hi:[1,0]
	v_pk_mul_f32 v[52:53], v[52:53], v[186:187] op_sel_hi:[1,0]
	v_pk_mul_f32 v[50:51], v[50:51], v[186:187] op_sel_hi:[1,0]
	v_pk_mul_f32 v[48:49], v[48:49], v[154:155] op_sel_hi:[1,0]
	v_pk_mul_f32 v[46:47], v[46:47], v[154:155] op_sel_hi:[1,0]
	v_pk_mul_f32 v[44:45], v[44:45], v[154:155] op_sel_hi:[1,0]
	v_pk_mul_f32 v[42:43], v[42:43], v[154:155] op_sel_hi:[1,0]
	v_pk_mul_f32 v[40:41], v[40:41], v[154:155] op_sel_hi:[1,0]
	v_pk_mul_f32 v[38:39], v[38:39], v[154:155] op_sel_hi:[1,0]
	v_pk_mul_f32 v[36:37], v[36:37], v[154:155] op_sel_hi:[1,0]
	v_pk_mul_f32 v[34:35], v[34:35], v[154:155] op_sel_hi:[1,0]
	v_pk_mul_f32 v[32:33], v[32:33], v[152:153] op_sel_hi:[1,0]
	v_pk_mul_f32 v[30:31], v[30:31], v[152:153] op_sel_hi:[1,0]
	v_pk_mul_f32 v[28:29], v[28:29], v[152:153] op_sel_hi:[1,0]
	v_pk_mul_f32 v[26:27], v[26:27], v[152:153] op_sel_hi:[1,0]
	v_pk_mul_f32 v[24:25], v[24:25], v[152:153] op_sel_hi:[1,0]
	v_pk_mul_f32 v[22:23], v[22:23], v[152:153] op_sel_hi:[1,0]
	v_pk_mul_f32 v[20:21], v[20:21], v[152:153] op_sel_hi:[1,0]
	v_pk_mul_f32 v[18:19], v[18:19], v[152:153] op_sel_hi:[1,0]
	v_add_u32_e32 v152, v178, v164
	s_mov_b32 s26, 0x8000
	s_mov_b64 s[4:5], 0
	s_mov_b32 s48, 0x88000

.Lrot_o2:
	ds_read_b64_tr_b16 v[184:185], v154
	ds_read_b64_tr_b16 v[186:187], v154 offset:2048
	ds_read_b64_tr_b16 v[188:189], v164
	ds_read_b64_tr_b16 v[190:191], v164 offset:2048
	ds_read_b128 v[192:195], v165
	ds_read_b128 v[196:199], v165 offset:2048
	ds_read_b64_tr_b16 v[200:201], v222
	ds_read_b64_tr_b16 v[202:203], v222 offset:2048
	v_add_u32_e32 v224, s50, v153
	ds_read_b64_tr_b16 v[204:205], v224
	ds_read_b64_tr_b16 v[206:207], v224 offset:2048
	ds_read_b128 v[208:211], v165 offset:4096
	s_waitcnt lgkmcnt(6)
	v_mfma_f32_16x16x32_bf16 v[18:21], v[184:187], v[192:195], v[18:21]
	s_add_i32 s50, s8, 0
	v_add_u32_e32 v212, 0xfff40000, v152
	s_add_i32 s51, s50, s44
	v_mfma_f32_16x16x32_bf16 v[22:25], v[188:191], v[192:195], v[22:25]
	s_mov_b32 s52, m0
	s_mov_b32 m0, s51
	s_nop 0
	global_load_lds_dwordx4 v212, s[10:11]
	s_mov_b32 m0, s52
	s_waitcnt lgkmcnt(3)
	v_mfma_f32_16x16x32_bf16 v[26:29], v[200:203], v[192:195], v[26:29]
	s_waitcnt lgkmcnt(1)
	v_mfma_f32_16x16x32_bf16 v[30:33], v[204:207], v[192:195], v[30:33]
	v_mfma_f32_16x16x32_bf16 v[34:37], v[184:187], v[196:199], v[34:37]
	ds_read_b128 v[192:195], v165 offset:6144
	v_add_u32_e32 v212, 0xfff80000, v152
	s_add_i32 s51, s50, s45
	v_mfma_f32_16x16x32_bf16 v[38:41], v[188:191], v[196:199], v[38:41]
	s_mov_b32 s52, m0
	s_mov_b32 m0, s51
	s_nop 0
	global_load_lds_dwordx4 v212, s[10:11]
	s_mov_b32 m0, s52
	v_mfma_f32_16x16x32_bf16 v[42:45], v[200:203], v[196:199], v[42:45]
	v_mfma_f32_16x16x32_bf16 v[46:49], v[204:207], v[196:199], v[46:49]
	s_waitcnt lgkmcnt(1)
	v_mfma_f32_16x16x32_bf16 v[50:53], v[184:187], v[208:211], v[50:53]
	ds_read_b128 v[196:199], v165 offset:8192
	v_add_u32_e32 v212, 0xfffc0000, v152
	s_add_i32 s51, s50, s46
	v_mfma_f32_16x16x32_bf16 v[54:57], v[188:191], v[208:211], v[54:57]
	s_mov_b32 s52, m0
	s_mov_b32 m0, s51
	s_nop 0
	global_load_lds_dwordx4 v212, s[10:11]
	s_mov_b32 m0, s52
	v_mfma_f32_16x16x32_bf16 v[58:61], v[200:203], v[208:211], v[58:61]
	v_mfma_f32_16x16x32_bf16 v[62:65], v[204:207], v[208:211], v[62:65]
	s_waitcnt lgkmcnt(1)
	v_mfma_f32_16x16x32_bf16 v[66:69], v[184:187], v[192:195], v[66:69]
	ds_read_b128 v[208:211], v165 offset:10240
	s_add_i32 s50, s50, s47
	s_mov_b32 s51, m0
	s_mov_b32 m0, s50
	s_nop 0
	global_load_lds_dwordx4 v152, s[10:11]
	s_mov_b32 m0, s51
	v_mfma_f32_16x16x32_bf16 v[70:73], v[188:191], v[192:195], v[70:73]
	v_mfma_f32_16x16x32_bf16 v[74:77], v[200:203], v[192:195], v[74:77]
	v_mfma_f32_16x16x32_bf16 v[78:81], v[204:207], v[192:195], v[78:81]
	ds_read_b128 v[192:195], v165 offset:12288
	ds_read_b64_tr_b16 v[212:213], v154 offset:16384
	ds_read_b64_tr_b16 v[214:215], v154 offset:18432
	s_waitcnt lgkmcnt(4)
	v_mfma_f32_16x16x32_bf16 v[82:85], v[184:187], v[196:199], v[82:85]
	v_mfma_f32_16x16x32_bf16 v[86:89], v[188:191], v[196:199], v[86:89]
	v_mfma_f32_16x16x32_bf16 v[90:93], v[200:203], v[196:199], v[90:93]
	v_mfma_f32_16x16x32_bf16 v[94:97], v[204:207], v[196:199], v[94:97]
	ds_read_b128 v[196:199], v165 offset:14336
	ds_read_b64_tr_b16 v[216:217], v164 offset:16384
	ds_read_b64_tr_b16 v[218:219], v164 offset:18432
	s_waitcnt lgkmcnt(6)
	v_mfma_f32_16x16x32_bf16 v[98:101], v[184:187], v[208:211], v[98:101]
	v_mfma_f32_16x16x32_bf16 v[102:105], v[188:191], v[208:211], v[102:105]
	v_mfma_f32_16x16x32_bf16 v[106:109], v[200:203], v[208:211], v[106:109]
	v_mfma_f32_16x16x32_bf16 v[110:113], v[204:207], v[208:211], v[110:113]
	v_add_u32_e32 v154, s49, v162
	ds_read_b128 v[208:211], v154
	ds_read_b64_tr_b16 v[220:221], v222 offset:16384
	ds_read_b64_tr_b16 v[222:223], v222 offset:18432
	s_waitcnt lgkmcnt(8)
	v_mfma_f32_16x16x32_bf16 v[114:117], v[184:187], v[192:195], v[114:117]
	v_mfma_f32_16x16x32_bf16 v[118:121], v[188:191], v[192:195], v[118:121]
	v_mfma_f32_16x16x32_bf16 v[122:125], v[200:203], v[192:195], v[122:125]
	v_mfma_f32_16x16x32_bf16 v[126:129], v[204:207], v[192:195], v[126:129]
	s_waitcnt lgkmcnt(5)
	v_mfma_f32_16x16x32_bf16 v[130:133], v[184:187], v[196:199], v[130:133]
	ds_read_b128 v[184:187], v154 offset:2048
	s_and_b32 s49, s48, 0x8000
	v_mfma_f32_16x16x32_bf16 v[134:137], v[188:191], v[196:199], v[134:137]
	ds_read_b64_tr_b16 v[188:189], v224 offset:16384
	ds_read_b64_tr_b16 v[190:191], v224 offset:18432
	v_mfma_f32_16x16x32_bf16 v[138:141], v[200:203], v[196:199], v[138:141]
	v_mfma_f32_16x16x32_bf16 v[142:145], v[204:207], v[196:199], v[142:145]
	s_waitcnt lgkmcnt(5)
	v_mfma_f32_16x16x32_bf16 v[18:21], v[212:215], v[208:211], v[18:21]
	ds_read_b128 v[192:195], v154 offset:4096
	v_add_u32_e32 v164, s49, v163
	s_add_u32 s49, s6, s4
	v_mfma_f32_16x16x32_bf16 v[22:25], v[216:219], v[208:211], v[22:25]
	s_addc_u32 s52, s7, s5
	s_waitcnt vmcnt(7)
	s_add_u32 s50, s49, 0x480000
	s_waitcnt lgkmcnt(4)
	v_mfma_f32_16x16x32_bf16 v[26:29], v[220:223], v[208:211], v[26:29]
	ds_write_b128 v164, v[14:17]
	s_addc_u32 s51, s52, 0
	global_load_dwordx4 v[14:17], v173, s[50:51]
	s_waitcnt lgkmcnt(2)
	v_mfma_f32_16x16x32_bf16 v[30:33], v[188:191], v[208:211], v[30:33]
	v_mfma_f32_16x16x32_bf16 v[34:37], v[212:215], v[184:187], v[34:37]
	ds_read_b128 v[196:199], v154 offset:6144
	s_waitcnt vmcnt(7)
	s_add_u32 s50, s49, 0x490000
	v_mfma_f32_16x16x32_bf16 v[38:41], v[216:219], v[184:187], v[38:41]
	ds_write_b128 v164, v[10:13] offset:8192
	s_addc_u32 s51, s52, 0
	global_load_dwordx4 v[10:13], v173, s[50:51]
	v_mfma_f32_16x16x32_bf16 v[42:45], v[220:223], v[184:187], v[42:45]
	v_mfma_f32_16x16x32_bf16 v[46:49], v[188:191], v[184:187], v[46:49]
	s_waitcnt lgkmcnt(3)
	v_mfma_f32_16x16x32_bf16 v[50:53], v[212:215], v[192:195], v[50:53]
	ds_read_b128 v[184:187], v154 offset:8192
	s_waitcnt vmcnt(7)
	s_add_u32 s50, s49, 0x4a0000
	v_mfma_f32_16x16x32_bf16 v[54:57], v[216:219], v[192:195], v[54:57]
	ds_write_b128 v164, v[6:9] offset:16384
	s_addc_u32 s51, s52, 0
	global_load_dwordx4 v[6:9], v173, s[50:51]
	v_mfma_f32_16x16x32_bf16 v[58:61], v[220:223], v[192:195], v[58:61]
	v_mfma_f32_16x16x32_bf16 v[62:65], v[188:191], v[192:195], v[62:65]
	s_waitcnt lgkmcnt(3)
	v_mfma_f32_16x16x32_bf16 v[66:69], v[212:215], v[196:199], v[66:69]
	ds_read_b128 v[192:195], v154 offset:10240
	s_waitcnt vmcnt(7)
	s_add_u32 s50, s49, 0x4b0000
	v_mfma_f32_16x16x32_bf16 v[70:73], v[216:219], v[196:199], v[70:73]
	ds_write_b128 v164, v[2:5] offset:24576
	s_addc_u32 s51, s52, 0
	global_load_dwordx4 v[2:5], v173, s[50:51]
	v_mfma_f32_16x16x32_bf16 v[74:77], v[220:223], v[196:199], v[74:77]
	v_mfma_f32_16x16x32_bf16 v[78:81], v[188:191], v[196:199], v[78:81]
	s_waitcnt lgkmcnt(3)
	v_mfma_f32_16x16x32_bf16 v[82:85], v[212:215], v[184:187], v[82:85]
	ds_read_b128 v[196:199], v154 offset:12288
	v_mfma_f32_16x16x32_bf16 v[86:89], v[216:219], v[184:187], v[86:89]
	v_mfma_f32_16x16x32_bf16 v[90:93], v[220:223], v[184:187], v[90:93]
	v_mfma_f32_16x16x32_bf16 v[94:97], v[188:191], v[184:187], v[94:97]
	s_waitcnt lgkmcnt(2)
	v_mfma_f32_16x16x32_bf16 v[98:101], v[212:215], v[192:195], v[98:101]
	ds_read_b128 v[184:187], v154 offset:14336
	v_mfma_f32_16x16x32_bf16 v[102:105], v[216:219], v[192:195], v[102:105]
	v_mfma_f32_16x16x32_bf16 v[106:109], v[220:223], v[192:195], v[106:109]
	v_mfma_f32_16x16x32_bf16 v[110:113], v[188:191], v[192:195], v[110:113]
	s_waitcnt lgkmcnt(1)
	v_mfma_f32_16x16x32_bf16 v[114:117], v[212:215], v[196:199], v[114:117]
	v_mfma_f32_16x16x32_bf16 v[118:121], v[216:219], v[196:199], v[118:121]
	v_mfma_f32_16x16x32_bf16 v[122:125], v[220:223], v[196:199], v[122:125]
	v_mfma_f32_16x16x32_bf16 v[126:129], v[188:191], v[196:199], v[126:129]
	s_waitcnt lgkmcnt(0)
	v_mfma_f32_16x16x32_bf16 v[130:133], v[212:215], v[184:187], v[130:133]
	v_mfma_f32_16x16x32_bf16 v[134:137], v[216:219], v[184:187], v[134:137]
	v_mfma_f32_16x16x32_bf16 v[138:141], v[220:223], v[184:187], v[138:141]
	v_mfma_f32_16x16x32_bf16 v[142:145], v[188:191], v[184:187], v[142:145]
	s_add_i32 s49, s26, 0x8000
	s_cmp_lg_u32 s26, 0x10000
	s_cselect_b32 s26, s49, 0
	s_add_i32 s49, s8, 0x8000
	s_cmp_lg_u32 s8, 0x10000
	s_cselect_b32 s8, s49, 0
	s_add_u32 s4, s4, 0x40000
	s_addc_u32 s5, s5, 0
	s_add_i32 s48, s48, 0x8000
	v_add_u32_e32 v152, 0x80, v152
	s_add_i32 s50, s48, 0xffff8000
	s_and_b32 s50, s50, 0x8000
	s_add_i32 s50, s50, 0
	s_add_i32 s49, s26, 0
	s_add_i32 s50, s50, 0x18000
	v_add_u32_e32 v154, s50, v157
	v_add_u32_e32 v165, s49, v161
	v_add_u32_e32 v222, s50, v155
	v_add_u32_e32 v164, s50, v156
	s_waitcnt lgkmcnt(0)
	s_barrier
	s_cmp_lg_u32 s4, 0x380000
	s_cbranch_scc1 .Lrot_o2
	s_add_i32 s4, 0, 0x18000
	v_add_u32_e32 v152, s4, v157
	v_add_u32_e32 v220, 0, v161
	v_add_u32_e32 v161, s4, v155
	v_add_u32_e32 v221, s4, v153
	ds_read_b64_tr_b16 v[184:185], v152
	ds_read_b64_tr_b16 v[186:187], v152 offset:2048
	v_add_u32_e32 v154, s4, v156
	ds_read_b128 v[188:191], v220
	ds_read_b64_tr_b16 v[192:193], v154
	ds_read_b64_tr_b16 v[194:195], v154 offset:2048
	ds_read_b128 v[196:199], v220 offset:2048
	ds_read_b64_tr_b16 v[200:201], v161
	ds_read_b64_tr_b16 v[202:203], v161 offset:2048
	ds_read_b64_tr_b16 v[204:205], v221
	ds_read_b64_tr_b16 v[206:207], v221 offset:2048
	ds_read_b128 v[208:211], v220 offset:4096
	s_waitcnt lgkmcnt(8)
	v_mfma_f32_16x16x32_bf16 v[18:21], v[184:187], v[188:191], v[18:21]
	s_waitcnt lgkmcnt(6)
	v_mfma_f32_16x16x32_bf16 v[22:25], v[192:195], v[188:191], v[22:25]
	s_waitcnt lgkmcnt(3)
	v_mfma_f32_16x16x32_bf16 v[26:29], v[200:203], v[188:191], v[26:29]
	s_waitcnt lgkmcnt(1)
	v_mfma_f32_16x16x32_bf16 v[30:33], v[204:207], v[188:191], v[30:33]
	ds_read_b128 v[188:191], v220 offset:6144
	v_mfma_f32_16x16x32_bf16 v[34:37], v[184:187], v[196:199], v[34:37]
	v_mfma_f32_16x16x32_bf16 v[38:41], v[192:195], v[196:199], v[38:41]
	v_mfma_f32_16x16x32_bf16 v[42:45], v[200:203], v[196:199], v[42:45]
	v_mfma_f32_16x16x32_bf16 v[46:49], v[204:207], v[196:199], v[46:49]
	ds_read_b128 v[196:199], v220 offset:8192
	s_waitcnt lgkmcnt(2)
	v_mfma_f32_16x16x32_bf16 v[50:53], v[184:187], v[208:211], v[50:53]
	v_mfma_f32_16x16x32_bf16 v[54:57], v[192:195], v[208:211], v[54:57]
	v_mfma_f32_16x16x32_bf16 v[58:61], v[200:203], v[208:211], v[58:61]
	v_mfma_f32_16x16x32_bf16 v[62:65], v[204:207], v[208:211], v[62:65]
	ds_read_b128 v[208:211], v220 offset:10240
	s_waitcnt lgkmcnt(2)
	v_mfma_f32_16x16x32_bf16 v[66:69], v[184:187], v[188:191], v[66:69]
	v_mfma_f32_16x16x32_bf16 v[70:73], v[192:195], v[188:191], v[70:73]
	v_mfma_f32_16x16x32_bf16 v[74:77], v[200:203], v[188:191], v[74:77]
	v_mfma_f32_16x16x32_bf16 v[78:81], v[204:207], v[188:191], v[78:81]
	ds_read_b128 v[188:191], v220 offset:12288
	ds_read_b64_tr_b16 v[212:213], v152 offset:16384
	ds_read_b64_tr_b16 v[214:215], v152 offset:18432
	s_waitcnt lgkmcnt(4)
	v_mfma_f32_16x16x32_bf16 v[82:85], v[184:187], v[196:199], v[82:85]
	v_mfma_f32_16x16x32_bf16 v[86:89], v[192:195], v[196:199], v[86:89]
	v_mfma_f32_16x16x32_bf16 v[90:93], v[200:203], v[196:199], v[90:93]
	v_mfma_f32_16x16x32_bf16 v[94:97], v[204:207], v[196:199], v[94:97]
	ds_read_b128 v[196:199], v220 offset:14336
	ds_read_b64_tr_b16 v[216:217], v154 offset:16384
	ds_read_b64_tr_b16 v[218:219], v154 offset:18432
	s_waitcnt lgkmcnt(6)
	v_mfma_f32_16x16x32_bf16 v[98:101], v[184:187], v[208:211], v[98:101]
	v_mfma_f32_16x16x32_bf16 v[102:105], v[192:195], v[208:211], v[102:105]
	v_mfma_f32_16x16x32_bf16 v[106:109], v[200:203], v[208:211], v[106:109]
	v_mfma_f32_16x16x32_bf16 v[110:113], v[204:207], v[208:211], v[110:113]
	v_add_u32_e32 v236, 0, v162
	ds_read_b128 v[162:165], v236
	ds_read_b64_tr_b16 v[208:209], v161 offset:16384
	ds_read_b64_tr_b16 v[210:211], v161 offset:18432
	s_waitcnt lgkmcnt(8)
	v_mfma_f32_16x16x32_bf16 v[114:117], v[184:187], v[188:191], v[114:117]
	v_mfma_f32_16x16x32_bf16 v[118:121], v[192:195], v[188:191], v[118:121]
	v_mfma_f32_16x16x32_bf16 v[122:125], v[200:203], v[188:191], v[122:125]
	v_mfma_f32_16x16x32_bf16 v[126:129], v[204:207], v[188:191], v[126:129]
	s_waitcnt lgkmcnt(5)
	v_mfma_f32_16x16x32_bf16 v[130:133], v[184:187], v[196:199], v[130:133]
	ds_read_b128 v[184:187], v236 offset:2048
	ds_read_b64_tr_b16 v[188:189], v221 offset:16384
	ds_read_b64_tr_b16 v[190:191], v221 offset:18432
	v_mfma_f32_16x16x32_bf16 v[134:137], v[192:195], v[196:199], v[134:137]
	v_mfma_f32_16x16x32_bf16 v[138:141], v[200:203], v[196:199], v[138:141]
	v_mfma_f32_16x16x32_bf16 v[142:145], v[204:207], v[196:199], v[142:145]
	ds_read_b128 v[192:195], v236 offset:4096
	s_waitcnt vmcnt(3)
	v_add_u32_e32 v152, s34, v160
	s_waitcnt lgkmcnt(6)
	v_mfma_f32_16x16x32_bf16 v[18:21], v[212:215], v[162:165], v[18:21]
	ds_write_b128 v152, v[14:17]
	v_mfma_f32_16x16x32_bf16 v[22:25], v[216:219], v[162:165], v[22:25]
	s_waitcnt lgkmcnt(5)
	v_mfma_f32_16x16x32_bf16 v[26:29], v[208:211], v[162:165], v[26:29]
	s_waitcnt lgkmcnt(2)
	v_mfma_f32_16x16x32_bf16 v[14:17], v[188:191], v[162:165], v[30:33]
	v_mfma_f32_16x16x32_bf16 v[30:33], v[212:215], v[184:187], v[34:37]
	v_mfma_f32_16x16x32_bf16 v[34:37], v[216:219], v[184:187], v[38:41]
	v_mfma_f32_16x16x32_bf16 v[38:41], v[208:211], v[184:187], v[42:45]
	s_nop 2
	ds_read_b128 v[42:45], v236 offset:6144
	s_waitcnt vmcnt(2)
	ds_write_b128 v152, v[10:13] offset:8192
	v_mfma_f32_16x16x32_bf16 v[10:13], v[188:191], v[184:187], v[46:49]
	s_waitcnt lgkmcnt(3)
	v_mfma_f32_16x16x32_bf16 v[46:49], v[212:215], v[192:195], v[50:53]
	v_mfma_f32_16x16x32_bf16 v[50:53], v[216:219], v[192:195], v[54:57]
	v_mfma_f32_16x16x32_bf16 v[54:57], v[208:211], v[192:195], v[58:61]
	s_nop 2
	ds_read_b128 v[58:61], v236 offset:8192
	s_waitcnt vmcnt(1)
	ds_write_b128 v152, v[6:9] offset:16384
	v_mfma_f32_16x16x32_bf16 v[6:9], v[188:191], v[192:195], v[62:65]
	s_waitcnt lgkmcnt(3)
	v_mfma_f32_16x16x32_bf16 v[62:65], v[212:215], v[42:45], v[66:69]
	v_mfma_f32_16x16x32_bf16 v[66:69], v[216:219], v[42:45], v[70:73]
	v_mfma_f32_16x16x32_bf16 v[70:73], v[208:211], v[42:45], v[74:77]
	s_nop 2
	ds_read_b128 v[74:77], v236 offset:10240
	s_waitcnt vmcnt(0)
	ds_write_b128 v152, v[2:5] offset:24576
	v_mfma_f32_16x16x32_bf16 v[2:5], v[188:191], v[42:45], v[78:81]
	s_waitcnt lgkmcnt(3)
	v_mfma_f32_16x16x32_bf16 v[78:81], v[216:219], v[58:61], v[86:89]
	s_nop 2
	ds_read_b128 v[86:89], v236 offset:12288
	v_mfma_f32_16x16x32_bf16 v[42:45], v[212:215], v[58:61], v[82:85]
	v_mfma_f32_16x16x32_bf16 v[82:85], v[208:211], v[58:61], v[90:93]
	v_mfma_f32_16x16x32_bf16 v[58:61], v[188:191], v[58:61], v[94:97]
	s_waitcnt lgkmcnt(2)
	v_mfma_f32_16x16x32_bf16 v[94:97], v[216:219], v[74:77], v[102:105]
	s_nop 2
	ds_read_b128 v[102:105], v236 offset:14336
	v_mfma_f32_16x16x32_bf16 v[90:93], v[212:215], v[74:77], v[98:101]
	v_mfma_f32_16x16x32_bf16 v[98:101], v[208:211], v[74:77], v[106:109]
	v_mfma_f32_16x16x32_bf16 v[74:77], v[188:191], v[74:77], v[110:113]
	s_waitcnt lgkmcnt(1)
	v_mfma_f32_16x16x32_bf16 v[106:109], v[212:215], v[86:89], v[114:117]
	v_mfma_f32_16x16x32_bf16 v[110:113], v[216:219], v[86:89], v[118:121]
	v_mfma_f32_16x16x32_bf16 v[114:117], v[208:211], v[86:89], v[122:125]
	v_mfma_f32_16x16x32_bf16 v[86:89], v[188:191], v[86:89], v[126:129]
	s_waitcnt lgkmcnt(0)
	v_mfma_f32_16x16x32_bf16 v[118:121], v[212:215], v[102:105], v[130:133]
	v_mfma_f32_16x16x32_bf16 v[122:125], v[216:219], v[102:105], v[134:137]
	v_mfma_f32_16x16x32_bf16 v[126:129], v[208:211], v[102:105], v[138:141]
	v_mfma_f32_16x16x32_bf16 v[102:105], v[188:191], v[102:105], v[142:145]
	s_waitcnt lgkmcnt(0)
	s_barrier
	v_add_u32_e32 v164, s34, v157
	v_add_u32_e32 v165, s34, v156
	v_add_u32_e32 v198, s34, v155
	ds_read_b64_tr_b16 v[130:131], v164
	ds_read_b64_tr_b16 v[132:133], v164 offset:2048
	ds_read_b64_tr_b16 v[134:135], v165
	ds_read_b64_tr_b16 v[136:137], v165 offset:2048
	ds_read_b128 v[138:141], v220 offset:32768
	ds_read_b64_tr_b16 v[142:143], v198
	ds_read_b128 v[154:157], v220 offset:34816
	ds_read_b128 v[160:163], v220 offset:36864
	ds_read_b64_tr_b16 v[144:145], v198 offset:2048
	v_add_u32_e32 v200, s34, v153
	ds_read_b64_tr_b16 v[184:185], v200
	ds_read_b64_tr_b16 v[186:187], v200 offset:2048
	s_waitcnt lgkmcnt(6)
	v_mfma_f32_16x16x32_bf16 v[18:21], v[130:133], v[138:141], v[18:21]
	v_mfma_f32_16x16x32_bf16 v[22:25], v[134:137], v[138:141], v[22:25]
	s_waitcnt lgkmcnt(2)
	v_mfma_f32_16x16x32_bf16 v[26:29], v[142:145], v[138:141], v[26:29]
	s_waitcnt lgkmcnt(0)
	v_mfma_f32_16x16x32_bf16 v[14:17], v[184:187], v[138:141], v[14:17]
	ds_read_b128 v[138:141], v220 offset:38912
	v_mfma_f32_16x16x32_bf16 v[30:33], v[130:133], v[154:157], v[30:33]
	v_mfma_f32_16x16x32_bf16 v[34:37], v[134:137], v[154:157], v[34:37]
	v_mfma_f32_16x16x32_bf16 v[38:41], v[142:145], v[154:157], v[38:41]
	v_mfma_f32_16x16x32_bf16 v[10:13], v[184:187], v[154:157], v[10:13]
	ds_read_b128 v[152:155], v220 offset:40960
	v_mfma_f32_16x16x32_bf16 v[46:49], v[130:133], v[160:163], v[46:49]
	v_mfma_f32_16x16x32_bf16 v[50:53], v[134:137], v[160:163], v[50:53]
	v_mfma_f32_16x16x32_bf16 v[54:57], v[142:145], v[160:163], v[54:57]
	v_mfma_f32_16x16x32_bf16 v[6:9], v[184:187], v[160:163], v[6:9]
	ds_read_b128 v[160:163], v220 offset:43008
	s_waitcnt lgkmcnt(2)
	v_mfma_f32_16x16x32_bf16 v[62:65], v[130:133], v[138:141], v[62:65]
	v_mfma_f32_16x16x32_bf16 v[66:69], v[134:137], v[138:141], v[66:69]
	v_mfma_f32_16x16x32_bf16 v[70:73], v[142:145], v[138:141], v[70:73]
	v_mfma_f32_16x16x32_bf16 v[2:5], v[184:187], v[138:141], v[2:5]
	s_waitcnt lgkmcnt(1)
	v_mfma_f32_16x16x32_bf16 v[138:141], v[134:137], v[152:155], v[78:81]
	s_nop 2
	ds_read_b128 v[78:81], v220 offset:45056
	ds_read_b64_tr_b16 v[188:189], v164 offset:16384
	ds_read_b64_tr_b16 v[190:191], v164 offset:18432
	v_mfma_f32_16x16x32_bf16 v[42:45], v[130:133], v[152:155], v[42:45]
	v_mfma_f32_16x16x32_bf16 v[82:85], v[142:145], v[152:155], v[82:85]
	v_mfma_f32_16x16x32_bf16 v[152:155], v[184:187], v[152:155], v[58:61]
	s_nop 2
	ds_read_b128 v[58:61], v220 offset:47104
	ds_read_b64_tr_b16 v[192:193], v165 offset:16384
	ds_read_b64_tr_b16 v[194:195], v165 offset:18432
	s_waitcnt lgkmcnt(6)
	v_mfma_f32_16x16x32_bf16 v[90:93], v[130:133], v[160:163], v[90:93]
	v_mfma_f32_16x16x32_bf16 v[94:97], v[134:137], v[160:163], v[94:97]
	v_mfma_f32_16x16x32_bf16 v[98:101], v[142:145], v[160:163], v[98:101]
	v_mfma_f32_16x16x32_bf16 v[160:163], v[184:187], v[160:163], v[74:77]
	s_nop 2
	ds_read_b128 v[74:77], v236 offset:32768
	ds_read_b64_tr_b16 v[196:197], v198 offset:16384
	ds_read_b64_tr_b16 v[198:199], v198 offset:18432
	s_waitcnt lgkmcnt(8)
	v_mfma_f32_16x16x32_bf16 v[106:109], v[130:133], v[78:81], v[106:109]
	v_mfma_f32_16x16x32_bf16 v[110:113], v[134:137], v[78:81], v[110:113]
	v_mfma_f32_16x16x32_bf16 v[114:117], v[142:145], v[78:81], v[114:117]
	v_mfma_f32_16x16x32_bf16 v[86:89], v[184:187], v[78:81], v[86:89]
	s_waitcnt lgkmcnt(5)
	v_mfma_f32_16x16x32_bf16 v[118:121], v[130:133], v[58:61], v[118:121]
	ds_read_b128 v[78:81], v236 offset:34816
	ds_read_b64_tr_b16 v[130:131], v200 offset:16384
	ds_read_b64_tr_b16 v[132:133], v200 offset:18432
	v_mfma_f32_16x16x32_bf16 v[122:125], v[134:137], v[58:61], v[122:125]
	v_mfma_f32_16x16x32_bf16 v[126:129], v[142:145], v[58:61], v[126:129]
	v_mfma_f32_16x16x32_bf16 v[102:105], v[184:187], v[58:61], v[102:105]
	s_waitcnt lgkmcnt(5)
	v_mfma_f32_16x16x32_bf16 v[134:137], v[188:191], v[74:77], v[18:21]
	s_nop 2
	ds_read_b128 v[18:21], v236 offset:36864
	v_mfma_f32_16x16x32_bf16 v[142:145], v[192:195], v[74:77], v[22:25]
	s_waitcnt lgkmcnt(4)
	v_mfma_f32_16x16x32_bf16 v[184:187], v[196:199], v[74:77], v[26:29]
	s_waitcnt lgkmcnt(1)
	v_mfma_f32_16x16x32_bf16 v[14:17], v[130:133], v[74:77], v[14:17]
	ds_read_b128 v[22:25], v236 offset:38912
	v_mfma_f32_16x16x32_bf16 v[200:203], v[188:191], v[78:81], v[30:33]
	v_mfma_f32_16x16x32_bf16 v[204:207], v[192:195], v[78:81], v[34:37]
	v_mfma_f32_16x16x32_bf16 v[208:211], v[196:199], v[78:81], v[38:41]
	v_mfma_f32_16x16x32_bf16 v[10:13], v[130:133], v[78:81], v[10:13]
	ds_read_b128 v[26:29], v236 offset:40960
	s_waitcnt lgkmcnt(2)
	v_mfma_f32_16x16x32_bf16 v[212:215], v[188:191], v[18:21], v[46:49]
	v_mfma_f32_16x16x32_bf16 v[216:219], v[192:195], v[18:21], v[50:53]
	v_mfma_f32_16x16x32_bf16 v[220:223], v[196:199], v[18:21], v[54:57]
	v_mfma_f32_16x16x32_bf16 v[6:9], v[130:133], v[18:21], v[6:9]
	ds_read_b128 v[18:21], v236 offset:43008
	s_waitcnt lgkmcnt(2)
	v_mfma_f32_16x16x32_bf16 v[224:227], v[188:191], v[22:25], v[62:65]
	v_mfma_f32_16x16x32_bf16 v[228:231], v[192:195], v[22:25], v[66:69]
	v_mfma_f32_16x16x32_bf16 v[232:235], v[196:199], v[22:25], v[70:73]
	v_mfma_f32_16x16x32_bf16 v[2:5], v[130:133], v[22:25], v[2:5]
	ds_read_b128 v[22:25], v236 offset:45056
	s_waitcnt lgkmcnt(2)
	v_mfma_f32_16x16x32_bf16 v[78:81], v[188:191], v[26:29], v[42:45]
	v_mfma_f32_16x16x32_bf16 v[74:77], v[192:195], v[26:29], v[138:141]
	v_mfma_f32_16x16x32_bf16 v[58:61], v[196:199], v[26:29], v[82:85]
	v_mfma_f32_16x16x32_bf16 v[62:65], v[130:133], v[26:29], v[152:155]
	s_nop 1
	ds_read_b128 v[82:85], v236 offset:47104
	s_waitcnt lgkmcnt(2)
	v_mfma_f32_16x16x32_bf16 v[70:73], v[188:191], v[18:21], v[90:93]
	v_mfma_f32_16x16x32_bf16 v[66:69], v[192:195], v[18:21], v[94:97]
	v_mfma_f32_16x16x32_bf16 v[50:53], v[196:199], v[18:21], v[98:101]
	v_mfma_f32_16x16x32_bf16 v[54:57], v[130:133], v[18:21], v[160:163]
	s_waitcnt lgkmcnt(1)
	v_mfma_f32_16x16x32_bf16 v[46:49], v[188:191], v[22:25], v[106:109]
	v_mfma_f32_16x16x32_bf16 v[42:45], v[192:195], v[22:25], v[110:113]
	v_mfma_f32_16x16x32_bf16 v[38:41], v[196:199], v[22:25], v[114:117]
	v_mfma_f32_16x16x32_bf16 v[30:33], v[130:133], v[22:25], v[86:89]
	s_waitcnt lgkmcnt(0)
	v_mfma_f32_16x16x32_bf16 v[34:37], v[188:191], v[82:85], v[118:121]
	v_mfma_f32_16x16x32_bf16 v[26:29], v[192:195], v[82:85], v[122:125]
	v_mfma_f32_16x16x32_bf16 v[22:25], v[196:199], v[82:85], v[126:129]
	v_mfma_f32_16x16x32_bf16 v[18:21], v[130:133], v[82:85], v[102:105]
	v_mov_b32_e32 v236, v1
	v_mov_b32_e32 v237, v166
	s_waitcnt lgkmcnt(0)
	s_barrier
	s_lshl_b32 s4, s42, 6
	v_and_or_b32 v82, v236, 63, v181
	v_lshlrev_b32_e32 v122, 2, v82
	ds_bpermute_b32 v82, v122, v183
	v_xor_b32_e32 v239, 0x80, v122
	s_or_b32 s4, s4, s24
	v_lshlrev_b32_e32 v240, 3, v237
	s_waitcnt lgkmcnt(0)
	v_pk_mul_f32 v[162:163], v[136:137], v[82:83] op_sel_hi:[1,0]
	v_pk_mul_f32 v[164:165], v[134:135], v[82:83] op_sel_hi:[1,0]
	v_pk_mul_f32 v[152:153], v[144:145], v[82:83] op_sel_hi:[1,0]
	v_pk_mul_f32 v[154:155], v[142:143], v[82:83] op_sel_hi:[1,0]
	v_add_u32_e32 v83, 16, v236
	v_and_or_b32 v83, v83, 63, v181
	v_lshlrev_b32_e32 v238, 2, v83
	ds_bpermute_b32 v84, v238, v183
	v_pk_mul_f32 v[138:139], v[14:15], v[82:83] op_sel_hi:[1,0]
	ds_bpermute_b32 v14, v239, v183
	v_add_u32_e32 v144, s43, v236
	v_ashrrev_i32_e32 v145, 31, v144
	s_waitcnt lgkmcnt(1)
	v_pk_mul_f32 v[116:117], v[10:11], v[84:85] op_sel_hi:[1,0]
	v_add_u32_e32 v10, 48, v236
	v_and_or_b32 v10, v10, 63, v181
	s_waitcnt lgkmcnt(0)
	v_pk_mul_f32 v[112:113], v[212:213], v[14:15] op_sel_hi:[1,0]
	v_lshlrev_b32_e32 v213, 2, v10
	ds_bpermute_b32 v10, v213, v183
	v_pk_mul_f32 v[98:99], v[8:9], v[14:15] op_sel_hi:[1,0]
	v_lshlrev_b64 v[8:9], 13, v[144:145]
	v_pk_mul_f32 v[118:119], v[208:209], v[84:85] op_sel_hi:[1,0]
	v_pk_mul_f32 v[100:101], v[6:7], v[14:15] op_sel_hi:[1,0]
	s_waitcnt lgkmcnt(0)
	v_pk_mul_f32 v[86:87], v[2:3], v[10:11] op_sel_hi:[1,0]
	v_lshl_add_u32 v2, v237, 2, s4
	s_mul_i32 s4, s41, 0x3000
	s_ashr_i32 s5, s4, 31
	s_lshl_b64 s[4:5], s[4:5], 2
	s_add_u32 s4, s70, s4
	s_addc_u32 s5, s71, s5
	s_add_u32 s4, s4, 0xc000
	v_ashrrev_i32_e32 v3, 31, v2
	ds_bpermute_b32 v208, v122, v182
	s_addc_u32 s5, s5, 0
	v_lshlrev_b64 v[122:123], 2, v[2:3]
	v_add_u32_e32 v6, 16, v2
	v_lshl_add_u64 v[8:9], s[12:13], 0, v[8:9]
	v_pk_mul_f32 v[128:129], v[202:203], v[84:85] op_sel_hi:[1,0]
	v_pk_mul_f32 v[130:131], v[200:201], v[84:85] op_sel_hi:[1,0]
	v_pk_mul_f32 v[124:125], v[206:207], v[84:85] op_sel_hi:[1,0]
	v_pk_mul_f32 v[126:127], v[204:205], v[84:85] op_sel_hi:[1,0]
	v_pk_mul_f32 v[120:121], v[210:211], v[84:85] op_sel_hi:[1,0]
	v_pk_mul_f32 v[114:115], v[12:13], v[84:85] op_sel_hi:[1,0]
	v_pk_mul_f32 v[84:85], v[4:5], v[10:11] op_sel_hi:[1,0]
	v_lshl_add_u64 v[4:5], s[4:5], 0, v[122:123]
	v_ashrrev_i32_e32 v7, 31, v6
	v_lshl_add_u64 v[132:133], v[8:9], 0, v[122:123]
	v_pk_mul_f32 v[156:157], v[186:187], v[82:83] op_sel_hi:[1,0]
	v_pk_mul_f32 v[160:161], v[184:185], v[82:83] op_sel_hi:[1,0]
	v_pk_mul_f32 v[136:137], v[16:17], v[82:83] op_sel_hi:[1,0]
	v_pk_mul_f32 v[110:111], v[214:215], v[14:15] op_sel_hi:[1,0]
	v_pk_mul_f32 v[106:107], v[218:219], v[14:15] op_sel_hi:[1,0]
	v_pk_mul_f32 v[108:109], v[216:217], v[14:15] op_sel_hi:[1,0]
	v_pk_mul_f32 v[102:103], v[222:223], v[14:15] op_sel_hi:[1,0]
	v_pk_mul_f32 v[104:105], v[220:221], v[14:15] op_sel_hi:[1,0]
	v_pk_mul_f32 v[94:95], v[226:227], v[10:11] op_sel_hi:[1,0]
	v_pk_mul_f32 v[96:97], v[224:225], v[10:11] op_sel_hi:[1,0]
	v_pk_mul_f32 v[90:91], v[230:231], v[10:11] op_sel_hi:[1,0]
	v_pk_mul_f32 v[92:93], v[228:229], v[10:11] op_sel_hi:[1,0]
	v_pk_mul_f32 v[88:89], v[234:235], v[10:11] op_sel_hi:[1,0]
	v_pk_mul_f32 v[82:83], v[232:233], v[10:11] op_sel_hi:[1,0]
	v_lshl_add_u64 v[6:7], v[6:7], 2, s[4:5]
	global_load_dwordx4 v[184:187], v[132:133], off nt
	global_load_dwordx4 v[14:17], v[4:5], off
	global_load_dwordx4 v[10:13], v[6:7], off
	v_add_u32_e32 v4, 32, v2
	v_add_u32_e32 v2, 48, v2
	v_ashrrev_i32_e32 v5, 31, v4
	v_ashrrev_i32_e32 v3, 31, v2
	v_lshl_add_u64 v[4:5], v[4:5], 2, s[4:5]
	v_lshl_add_u64 v[2:3], v[2:3], 2, s[4:5]
	global_load_dwordx4 v[188:191], v[132:133], off offset:64 nt
	global_load_dwordx4 v[192:195], v[132:133], off offset:128 nt
	global_load_dwordx4 v[6:9], v[4:5], off
	s_nop 0
	global_load_dwordx4 v[2:5], v[2:3], off
	s_nop 0
	global_load_dwordx4 v[196:199], v[132:133], off offset:192 nt
	v_add_u32_e32 v132, 16, v144
	ds_bpermute_b32 v212, v238, v182
	ds_bpermute_b32 v216, v239, v182
	v_ashrrev_i32_e32 v133, 31, v132
	v_lshlrev_b64 v[132:133], 13, v[132:133]
	v_lshl_add_u64 v[132:133], s[12:13], 0, v[132:133]
	v_lshl_add_u64 v[210:211], v[132:133], 0, v[122:123]
	global_load_dwordx4 v[200:203], v[210:211], off nt
	global_load_dwordx4 v[204:207], v[210:211], off offset:64 nt
	s_waitcnt lgkmcnt(2)
	v_pk_mul_f32 v[142:143], v[78:79], v[208:209] op_sel_hi:[1,0]
	v_pk_mul_f32 v[78:79], v[60:61], v[208:209] op_sel_hi:[1,0]
	s_waitcnt lgkmcnt(1)
	v_pk_mul_f32 v[60:61], v[50:51], v[212:213] op_sel_hi:[1,0]
	s_waitcnt lgkmcnt(0)
	v_pk_mul_f32 v[50:51], v[48:49], v[216:217] op_sel_hi:[1,0]
	v_pk_mul_f32 v[48:49], v[42:43], v[216:217] op_sel_hi:[1,0]
	v_add_u32_e32 v42, 32, v144
	ds_bpermute_b32 v182, v213, v182
	v_ashrrev_i32_e32 v43, 31, v42
	v_pk_mul_f32 v[132:133], v[76:77], v[208:209] op_sel_hi:[1,0]
	v_pk_mul_f32 v[134:135], v[74:75], v[208:209] op_sel_hi:[1,0]
	v_pk_mul_f32 v[74:75], v[64:65], v[208:209] op_sel_hi:[1,0]
	v_pk_mul_f32 v[76:77], v[62:63], v[208:209] op_sel_hi:[1,0]
	v_pk_mul_f32 v[62:63], v[68:69], v[212:213] op_sel_hi:[1,0]
	v_pk_mul_f32 v[64:65], v[66:67], v[212:213] op_sel_hi:[1,0]
	global_load_dwordx4 v[66:69], v[210:211], off offset:128 nt
	v_lshlrev_b64 v[42:43], 13, v[42:43]
	v_lshl_add_u64 v[42:43], s[12:13], 0, v[42:43]
	v_lshl_add_u64 v[220:221], v[42:43], 0, v[122:123]
	v_pk_mul_f32 v[140:141], v[80:81], v[208:209] op_sel_hi:[1,0]
	v_pk_mul_f32 v[80:81], v[58:59], v[208:209] op_sel_hi:[1,0]
	v_pk_mul_f32 v[72:73], v[72:73], v[212:213] op_sel_hi:[1,0]
	v_pk_mul_f32 v[70:71], v[70:71], v[212:213] op_sel_hi:[1,0]
	v_pk_mul_f32 v[58:59], v[52:53], v[212:213] op_sel_hi:[1,0]
	v_pk_mul_f32 v[56:57], v[56:57], v[212:213] op_sel_hi:[1,0]
	v_pk_mul_f32 v[54:55], v[54:55], v[212:213] op_sel_hi:[1,0]
	global_load_dwordx4 v[212:215], v[220:221], off nt
	v_pk_mul_f32 v[52:53], v[46:47], v[216:217] op_sel_hi:[1,0]
	global_load_dwordx4 v[208:211], v[210:211], off offset:192 nt
	v_pk_mul_f32 v[46:47], v[44:45], v[216:217] op_sel_hi:[1,0]
	v_pk_mul_f32 v[42:43], v[32:33], v[216:217] op_sel_hi:[1,0]
	v_pk_mul_f32 v[44:45], v[30:31], v[216:217] op_sel_hi:[1,0]
	s_waitcnt lgkmcnt(0)
	v_pk_mul_f32 v[30:31], v[36:37], v[182:183] op_sel_hi:[1,0]
	v_pk_mul_f32 v[32:33], v[34:35], v[182:183] op_sel_hi:[1,0]
	global_load_dwordx4 v[34:37], v[220:221], off offset:64 nt
	v_pk_mul_f32 v[40:41], v[40:41], v[216:217] op_sel_hi:[1,0]
	v_pk_mul_f32 v[38:39], v[38:39], v[216:217] op_sel_hi:[1,0]
	global_load_dwordx4 v[216:219], v[220:221], off offset:128 nt
	s_nop 0
	global_load_dwordx4 v[220:223], v[220:221], off offset:192 nt
	v_pk_mul_f32 v[28:29], v[28:29], v[182:183] op_sel_hi:[1,0]
	v_pk_mul_f32 v[26:27], v[26:27], v[182:183] op_sel_hi:[1,0]
	v_pk_mul_f32 v[24:25], v[24:25], v[182:183] op_sel_hi:[1,0]
	v_pk_mul_f32 v[22:23], v[22:23], v[182:183] op_sel_hi:[1,0]
	v_pk_mul_f32 v[20:21], v[20:21], v[182:183] op_sel_hi:[1,0]
	v_pk_mul_f32 v[18:19], v[18:19], v[182:183] op_sel_hi:[1,0]
	v_add_u32_e32 v182, 48, v144
	v_ashrrev_i32_e32 v183, 31, v182
	v_lshlrev_b64 v[182:183], 13, v[182:183]
	v_lshl_add_u64 v[182:183], s[12:13], 0, v[182:183]
	v_lshl_add_u64 v[182:183], v[182:183], 0, v[122:123]
	v_add_u32_e32 v145, s39, v236
	global_load_dwordx4 v[224:227], v[182:183], off nt
	global_load_dwordx4 v[228:231], v[182:183], off offset:64 nt
	global_load_dwordx4 v[232:235], v[182:183], off offset:128 nt
	global_load_dwordx4 v[236:239], v[182:183], off offset:192 nt
	s_add_i32 s40, s40, 0
	v_mul_lo_u32 v145, v145, s35
	v_add3_u32 v240, s40, v240, v145
	v_add_u32_e32 v145, 0x2000, v240
	s_andn2_b64 vcc, exec, s[76:77]
	s_waitcnt vmcnt(18)
	v_pk_fma_f32 v[162:163], v[162:163], v[16:17], v[186:187]
	v_pk_fma_f32 v[164:165], v[164:165], v[14:15], v[184:185]
	s_waitcnt vmcnt(16)
	v_pk_fma_f32 v[152:153], v[152:153], v[12:13], v[190:191]
	v_pk_fma_f32 v[154:155], v[154:155], v[10:11], v[188:189]
	v_cvt_pk_bf16_f32 v164, v164, v165
	v_cvt_pk_bf16_f32 v165, v162, v163
	v_cvt_pk_bf16_f32 v154, v154, v155
	v_cvt_pk_bf16_f32 v155, v152, v153
	ds_write2_b64 v240, v[164:165], v[154:155] offset1:4
	s_waitcnt vmcnt(14)
	v_pk_fma_f32 v[152:153], v[156:157], v[8:9], v[194:195]
	v_pk_fma_f32 v[154:155], v[160:161], v[6:7], v[192:193]
	s_waitcnt vmcnt(12)
	v_pk_fma_f32 v[136:137], v[136:137], v[4:5], v[198:199]
	v_pk_fma_f32 v[138:139], v[138:139], v[2:3], v[196:197]
	s_waitcnt vmcnt(11)
	v_pk_fma_f32 v[128:129], v[128:129], v[16:17], v[202:203]
	v_pk_fma_f32 v[130:131], v[130:131], v[14:15], v[200:201]
	s_waitcnt vmcnt(10)
	v_pk_fma_f32 v[124:125], v[124:125], v[12:13], v[206:207]
	v_cvt_pk_bf16_f32 v130, v130, v131
	v_cvt_pk_bf16_f32 v131, v128, v129
	v_cvt_pk_bf16_f32 v129, v124, v125
	v_add_u32_e32 v124, 64, v144
	v_ashrrev_i32_e32 v125, 31, v124
	v_lshlrev_b64 v[124:125], 13, v[124:125]
	v_pk_fma_f32 v[126:127], v[126:127], v[10:11], v[204:205]
	v_lshl_add_u64 v[124:125], s[12:13], 0, v[124:125]
	v_cvt_pk_bf16_f32 v154, v154, v155
	v_cvt_pk_bf16_f32 v155, v152, v153
	v_cvt_pk_bf16_f32 v138, v138, v139
	v_cvt_pk_bf16_f32 v139, v136, v137
	v_cvt_pk_bf16_f32 v128, v126, v127
	s_waitcnt vmcnt(9)
	v_pk_fma_f32 v[66:67], v[118:119], v[6:7], v[66:67]
	v_add_u32_e32 v118, 0x50, v144
	v_ashrrev_i32_e32 v119, 31, v118
	v_lshlrev_b64 v[118:119], 13, v[118:119]
	v_lshl_add_u64 v[136:137], v[124:125], 0, v[122:123]
	v_pk_fma_f32 v[68:69], v[120:121], v[8:9], v[68:69]
	v_lshl_add_u64 v[118:119], s[12:13], 0, v[118:119]
	ds_write2_b64 v240, v[154:155], v[138:139] offset0:8 offset1:12
	global_load_dwordx4 v[124:127], v[136:137], off nt
	ds_write2_b64 v145, v[130:131], v[128:129] offset0:32 offset1:36
	global_load_dwordx4 v[128:131], v[136:137], off offset:64 nt
	v_cvt_pk_bf16_f32 v138, v66, v67
	v_cvt_pk_bf16_f32 v139, v68, v69
	s_waitcnt vmcnt(9)
	v_pk_fma_f32 v[114:115], v[114:115], v[4:5], v[210:211]
	v_pk_fma_f32 v[116:117], v[116:117], v[2:3], v[208:209]
	global_load_dwordx4 v[66:69], v[136:137], off offset:128 nt
	v_cvt_pk_bf16_f32 v152, v116, v117
	v_cvt_pk_bf16_f32 v153, v114, v115
	global_load_dwordx4 v[114:117], v[136:137], off offset:192 nt
	v_lshl_add_u64 v[136:137], v[118:119], 0, v[122:123]
	s_waitcnt vmcnt(10)
	v_pk_fma_f32 v[106:107], v[106:107], v[12:13], v[36:37]
	v_pk_fma_f32 v[34:35], v[108:109], v[10:11], v[34:35]
	global_load_dwordx4 v[118:121], v[136:137], off nt
	ds_write2_b64 v145, v[138:139], v[152:153] offset0:40 offset1:44
	v_pk_fma_f32 v[138:139], v[110:111], v[16:17], v[214:215]
	v_pk_fma_f32 v[152:153], v[112:113], v[14:15], v[212:213]
	global_load_dwordx4 v[110:113], v[136:137], off offset:64 nt
	v_cvt_pk_bf16_f32 v154, v34, v35
	global_load_dwordx4 v[34:37], v[136:137], off offset:128 nt
	v_cvt_pk_bf16_f32 v155, v106, v107
	global_load_dwordx4 v[106:109], v[136:137], off offset:192 nt
	v_add_u32_e32 v136, 0x60, v144
	v_cvt_pk_bf16_f32 v152, v152, v153
	v_cvt_pk_bf16_f32 v153, v138, v139
	v_add_u32_e32 v145, 0x4000, v240
	v_ashrrev_i32_e32 v137, 31, v136
	v_lshlrev_b64 v[136:137], 13, v[136:137]
	ds_write2_b64 v145, v[152:153], v[154:155] offset0:64 offset1:68
	s_waitcnt vmcnt(13)
	v_pk_fma_f32 v[152:153], v[102:103], v[8:9], v[218:219]
	v_pk_fma_f32 v[154:155], v[104:105], v[6:7], v[216:217]
	v_lshl_add_u64 v[136:137], s[12:13], 0, v[136:137]
	v_cvt_pk_bf16_f32 v154, v154, v155
	v_cvt_pk_bf16_f32 v155, v152, v153
	s_waitcnt vmcnt(12)
	v_pk_fma_f32 v[152:153], v[98:99], v[4:5], v[222:223]
	v_pk_fma_f32 v[98:99], v[100:101], v[2:3], v[220:221]
	v_lshl_add_u64 v[156:157], v[136:137], 0, v[122:123]
	v_cvt_pk_bf16_f32 v160, v98, v99
	v_cvt_pk_bf16_f32 v161, v152, v153
	v_add_u32_e32 v144, 0x70, v144
	global_load_dwordx4 v[136:139], v[156:157], off nt
	global_load_dwordx4 v[102:105], v[156:157], off offset:64 nt
	ds_write2_b64 v145, v[154:155], v[160:161] offset0:72 offset1:76
	v_ashrrev_i32_e32 v145, 31, v144
	v_lshlrev_b64 v[144:145], 13, v[144:145]
	v_lshl_add_u64 v[144:145], s[12:13], 0, v[144:145]
	global_load_dwordx4 v[98:101], v[156:157], off offset:128 nt
	global_load_dwordx4 v[152:155], v[156:157], off offset:192 nt
	v_lshl_add_u64 v[122:123], v[144:145], 0, v[122:123]
	s_waitcnt vmcnt(15)
	v_pk_fma_f32 v[144:145], v[94:95], v[16:17], v[226:227]
	v_pk_fma_f32 v[94:95], v[96:97], v[14:15], v[224:225]
	s_waitcnt vmcnt(14)
	v_pk_fma_f32 v[90:91], v[90:91], v[12:13], v[230:231]
	v_pk_fma_f32 v[92:93], v[92:93], v[10:11], v[228:229]
	global_load_dwordx4 v[160:163], v[122:123], off nt
	v_cvt_pk_bf16_f32 v156, v94, v95
	global_load_dwordx4 v[94:97], v[122:123], off offset:64 nt
	v_cvt_pk_bf16_f32 v157, v144, v145
	v_cvt_pk_bf16_f32 v144, v92, v93
	v_cvt_pk_bf16_f32 v145, v90, v91
	global_load_dwordx4 v[90:93], v[122:123], off offset:128 nt
	global_load_dwordx4 v[182:185], v[122:123], off offset:192 nt
	s_waitcnt vmcnt(17)
	v_pk_fma_f32 v[88:89], v[88:89], v[8:9], v[234:235]
	v_pk_fma_f32 v[82:83], v[82:83], v[6:7], v[232:233]
	s_waitcnt vmcnt(16)
	v_pk_fma_f32 v[84:85], v[84:85], v[4:5], v[238:239]
	v_pk_fma_f32 v[86:87], v[86:87], v[2:3], v[236:237]
	v_add_u32_e32 v164, 0x6000, v240
	v_cvt_pk_bf16_f32 v82, v82, v83
	v_cvt_pk_bf16_f32 v83, v88, v89
	v_cvt_pk_bf16_f32 v86, v86, v87
	v_cvt_pk_bf16_f32 v87, v84, v85
	ds_write2_b64 v164, v[82:83], v[86:87] offset0:104 offset1:108
	ds_write2_b64 v164, v[156:157], v[144:145] offset0:96 offset1:100
	s_waitcnt vmcnt(15)
	v_pk_fma_f32 v[82:83], v[140:141], v[16:17], v[126:127]
	v_pk_fma_f32 v[84:85], v[142:143], v[14:15], v[124:125]
	s_waitcnt vmcnt(14)
	v_pk_fma_f32 v[86:87], v[134:135], v[10:11], v[128:129]
	v_cvt_pk_bf16_f32 v84, v84, v85
	v_cvt_pk_bf16_f32 v85, v82, v83
	v_pk_fma_f32 v[82:83], v[132:133], v[12:13], v[130:131]
	v_cvt_pk_bf16_f32 v86, v86, v87
	s_waitcnt vmcnt(13)
	v_pk_fma_f32 v[68:69], v[78:79], v[8:9], v[68:69]
	v_pk_fma_f32 v[66:67], v[80:81], v[6:7], v[66:67]
	v_cvt_pk_bf16_f32 v87, v82, v83
	v_cvt_pk_bf16_f32 v66, v66, v67
	v_cvt_pk_bf16_f32 v67, v68, v69
	s_waitcnt vmcnt(12)
	v_pk_fma_f32 v[68:69], v[74:75], v[4:5], v[116:117]
	v_pk_fma_f32 v[74:75], v[76:77], v[2:3], v[114:115]
	v_add_u32_e32 v82, 0x8000, v240
	v_cvt_pk_bf16_f32 v74, v74, v75
	v_cvt_pk_bf16_f32 v75, v68, v69
	ds_write2_b64 v82, v[66:67], v[74:75] offset0:136 offset1:140
	s_waitcnt vmcnt(10)
	v_pk_fma_f32 v[62:63], v[62:63], v[12:13], v[112:113]
	v_pk_fma_f32 v[64:65], v[64:65], v[10:11], v[110:111]
	s_waitcnt vmcnt(9)
	v_pk_fma_f32 v[36:37], v[58:59], v[8:9], v[36:37]
	v_pk_fma_f32 v[34:35], v[60:61], v[6:7], v[34:35]
	s_waitcnt vmcnt(8)
	v_pk_fma_f32 v[54:55], v[54:55], v[2:3], v[106:107]
	v_cvt_pk_bf16_f32 v34, v34, v35
	v_cvt_pk_bf16_f32 v35, v36, v37
	v_pk_fma_f32 v[36:37], v[56:57], v[4:5], v[108:109]
	v_cvt_pk_bf16_f32 v64, v64, v65
	v_cvt_pk_bf16_f32 v65, v62, v63
	v_add_u32_e32 v62, 0xa000, v240
	v_cvt_pk_bf16_f32 v54, v54, v55
	v_cvt_pk_bf16_f32 v55, v36, v37
	ds_write2_b64 v62, v[34:35], v[54:55] offset0:168 offset1:172
	v_pk_fma_f32 v[66:67], v[16:17], v[72:73], v[120:121]
	v_pk_fma_f32 v[68:69], v[14:15], v[70:71], v[118:119]
	ds_write2_b64 v82, v[84:85], v[86:87] offset0:128 offset1:132
	v_cvt_pk_bf16_f32 v68, v68, v69
	v_cvt_pk_bf16_f32 v69, v66, v67
	ds_write2_b64 v62, v[68:69], v[64:65] offset0:160 offset1:164
	s_waitcnt vmcnt(7)
	v_pk_fma_f32 v[34:35], v[16:17], v[50:51], v[138:139]
	v_pk_fma_f32 v[36:37], v[14:15], v[52:53], v[136:137]
	s_waitcnt vmcnt(3)
	v_pk_fma_f32 v[16:17], v[16:17], v[30:31], v[162:163]
	v_cvt_pk_bf16_f32 v36, v36, v37
	v_cvt_pk_bf16_f32 v37, v34, v35
	v_pk_fma_f32 v[34:35], v[12:13], v[46:47], v[104:105]
	v_pk_fma_f32 v[46:47], v[10:11], v[48:49], v[102:103]
	v_add_u32_e32 v48, 0xc000, v240
	v_cvt_pk_bf16_f32 v46, v46, v47
	v_cvt_pk_bf16_f32 v47, v34, v35
	ds_write2_b64 v48, v[36:37], v[46:47] offset0:192 offset1:196
	v_pk_fma_f32 v[34:35], v[40:41], v[8:9], v[100:101]
	v_pk_fma_f32 v[36:37], v[38:39], v[6:7], v[98:99]
	v_pk_fma_f32 v[38:39], v[44:45], v[2:3], v[152:153]
	v_cvt_pk_bf16_f32 v36, v36, v37
	v_cvt_pk_bf16_f32 v37, v34, v35
	v_pk_fma_f32 v[34:35], v[42:43], v[4:5], v[154:155]
	s_waitcnt vmcnt(2)
	v_pk_fma_f32 v[12:13], v[12:13], v[28:29], v[96:97]
	v_pk_fma_f32 v[10:11], v[10:11], v[26:27], v[94:95]
	s_waitcnt vmcnt(1)
	v_pk_fma_f32 v[8:9], v[8:9], v[24:25], v[92:93]
	v_pk_fma_f32 v[6:7], v[6:7], v[22:23], v[90:91]
	s_waitcnt vmcnt(0)
	v_pk_fma_f32 v[4:5], v[20:21], v[4:5], v[184:185]
	v_pk_fma_f32 v[2:3], v[18:19], v[2:3], v[182:183]
	v_cvt_pk_bf16_f32 v10, v10, v11
	v_cvt_pk_bf16_f32 v11, v12, v13
	v_add_u32_e32 v12, 0xe000, v240
	v_cvt_pk_bf16_f32 v6, v6, v7
	v_cvt_pk_bf16_f32 v7, v8, v9
	v_cvt_pk_bf16_f32 v2, v2, v3
	v_cvt_pk_bf16_f32 v3, v4, v5
	v_lshl_or_b32 v8, s38, 5, v167
	v_pk_fma_f32 v[14:15], v[14:15], v[32:33], v[160:161]
	ds_write2_b64 v12, v[6:7], v[2:3] offset0:232 offset1:236
	v_mad_u64_u32 v[6:7], s[4:5], v8, s35, v[148:149]
	v_add_u32_e32 v8, s25, v8
	v_cvt_pk_bf16_f32 v14, v14, v15
	v_cvt_pk_bf16_f32 v15, v16, v17
	v_ashrrev_i32_e32 v9, 31, v8
	ds_write2_b64 v12, v[14:15], v[10:11] offset0:224 offset1:228
	v_lshlrev_b64 v[10:11], 12, v[8:9]
	v_cvt_pk_bf16_f32 v38, v38, v39
	v_cvt_pk_bf16_f32 v39, v34, v35
	v_lshl_add_u64 v[10:11], s[18:19], 0, v[10:11]
	ds_write2_b64 v48, v[36:37], v[38:39] offset0:200 offset1:204
	v_lshl_add_u64 v[10:11], v[10:11], 0, s[22:23]
	s_waitcnt lgkmcnt(0)
	s_barrier
	v_lshl_add_u64 v[10:11], v[10:11], 0, v[146:147]
	ds_read_b128 v[2:5], v6
	s_waitcnt lgkmcnt(0)
	global_store_dwordx4 v[10:11], v[2:5], off sc1
	s_nop 1
	v_add_u32_e32 v10, 2, v8
	v_ashrrev_i32_e32 v11, 31, v10
	v_lshlrev_b64 v[10:11], 12, v[10:11]
	v_lshl_add_u64 v[10:11], s[18:19], 0, v[10:11]
	v_lshl_add_u64 v[10:11], v[10:11], 0, s[22:23]
	v_lshl_add_u64 v[10:11], v[10:11], 0, v[146:147]
	ds_read_b128 v[2:5], v6 offset:1056
	s_waitcnt lgkmcnt(0)
	global_store_dwordx4 v[10:11], v[2:5], off sc1
	s_nop 1
	v_add_u32_e32 v10, 4, v8
	v_ashrrev_i32_e32 v11, 31, v10
	v_lshlrev_b64 v[10:11], 12, v[10:11]
	v_lshl_add_u64 v[10:11], s[18:19], 0, v[10:11]
	v_lshl_add_u64 v[10:11], v[10:11], 0, s[22:23]
	v_lshl_add_u64 v[10:11], v[10:11], 0, v[146:147]
	ds_read_b128 v[2:5], v6 offset:2112
	s_waitcnt lgkmcnt(0)
	global_store_dwordx4 v[10:11], v[2:5], off sc1
	s_nop 1
	v_add_u32_e32 v10, 6, v8
	v_ashrrev_i32_e32 v11, 31, v10
	v_lshlrev_b64 v[10:11], 12, v[10:11]
	v_lshl_add_u64 v[10:11], s[18:19], 0, v[10:11]
	v_lshl_add_u64 v[10:11], v[10:11], 0, s[22:23]
	v_lshl_add_u64 v[10:11], v[10:11], 0, v[146:147]
	ds_read_b128 v[2:5], v6 offset:3168
	s_waitcnt lgkmcnt(0)
	global_store_dwordx4 v[10:11], v[2:5], off sc1
	s_nop 1
	v_add_u32_e32 v10, 8, v8
	v_ashrrev_i32_e32 v11, 31, v10
	v_lshlrev_b64 v[10:11], 12, v[10:11]
	v_lshl_add_u64 v[10:11], s[18:19], 0, v[10:11]
	v_lshl_add_u64 v[10:11], v[10:11], 0, s[22:23]
	v_lshl_add_u64 v[10:11], v[10:11], 0, v[146:147]
	ds_read_b128 v[2:5], v6 offset:4224
	s_waitcnt lgkmcnt(0)
	global_store_dwordx4 v[10:11], v[2:5], off sc1
	s_nop 1
	v_add_u32_e32 v10, 10, v8
	v_ashrrev_i32_e32 v11, 31, v10
	v_lshlrev_b64 v[10:11], 12, v[10:11]
	v_lshl_add_u64 v[10:11], s[18:19], 0, v[10:11]
	v_lshl_add_u64 v[10:11], v[10:11], 0, s[22:23]
	v_lshl_add_u64 v[10:11], v[10:11], 0, v[146:147]
	ds_read_b128 v[2:5], v6 offset:5280
	s_waitcnt lgkmcnt(0)
	global_store_dwordx4 v[10:11], v[2:5], off sc1
	s_nop 1
	v_add_u32_e32 v10, 12, v8
	v_ashrrev_i32_e32 v11, 31, v10
	v_lshlrev_b64 v[10:11], 12, v[10:11]
	v_lshl_add_u64 v[10:11], s[18:19], 0, v[10:11]
	v_lshl_add_u64 v[10:11], v[10:11], 0, s[22:23]
	v_lshl_add_u64 v[10:11], v[10:11], 0, v[146:147]
	ds_read_b128 v[2:5], v6 offset:6336
	s_waitcnt lgkmcnt(0)
	global_store_dwordx4 v[10:11], v[2:5], off sc1
	s_nop 1
	v_add_u32_e32 v10, 14, v8
	v_ashrrev_i32_e32 v11, 31, v10
	v_lshlrev_b64 v[10:11], 12, v[10:11]
	v_lshl_add_u64 v[10:11], s[18:19], 0, v[10:11]
	v_lshl_add_u64 v[10:11], v[10:11], 0, s[22:23]
	v_lshl_add_u64 v[10:11], v[10:11], 0, v[146:147]
	ds_read_b128 v[2:5], v6 offset:7392
	s_waitcnt lgkmcnt(0)
	global_store_dwordx4 v[10:11], v[2:5], off sc1
	s_nop 1
	v_add_u32_e32 v10, 16, v8
	v_ashrrev_i32_e32 v11, 31, v10
	v_lshlrev_b64 v[10:11], 12, v[10:11]
	v_lshl_add_u64 v[10:11], s[18:19], 0, v[10:11]
	v_lshl_add_u64 v[10:11], v[10:11], 0, s[22:23]
	v_lshl_add_u64 v[10:11], v[10:11], 0, v[146:147]
	ds_read_b128 v[2:5], v6 offset:8448
	s_waitcnt lgkmcnt(0)
	global_store_dwordx4 v[10:11], v[2:5], off sc1
	s_nop 1
	v_add_u32_e32 v10, 18, v8
	v_ashrrev_i32_e32 v11, 31, v10
	v_lshlrev_b64 v[10:11], 12, v[10:11]
	v_lshl_add_u64 v[10:11], s[18:19], 0, v[10:11]
	v_lshl_add_u64 v[10:11], v[10:11], 0, s[22:23]
	v_lshl_add_u64 v[10:11], v[10:11], 0, v[146:147]
	ds_read_b128 v[2:5], v6 offset:9504
	s_waitcnt lgkmcnt(0)
	global_store_dwordx4 v[10:11], v[2:5], off sc1
	s_nop 1
	v_add_u32_e32 v10, 20, v8
	v_ashrrev_i32_e32 v11, 31, v10
	v_lshlrev_b64 v[10:11], 12, v[10:11]
	v_lshl_add_u64 v[10:11], s[18:19], 0, v[10:11]
	v_lshl_add_u64 v[10:11], v[10:11], 0, s[22:23]
	v_lshl_add_u64 v[10:11], v[10:11], 0, v[146:147]
	ds_read_b128 v[2:5], v6 offset:10560
	s_waitcnt lgkmcnt(0)
	global_store_dwordx4 v[10:11], v[2:5], off sc1
	s_nop 1
	v_add_u32_e32 v10, 22, v8
	v_ashrrev_i32_e32 v11, 31, v10
	v_lshlrev_b64 v[10:11], 12, v[10:11]
	v_lshl_add_u64 v[10:11], s[18:19], 0, v[10:11]
	v_lshl_add_u64 v[10:11], v[10:11], 0, s[22:23]
	v_lshl_add_u64 v[10:11], v[10:11], 0, v[146:147]
	ds_read_b128 v[2:5], v6 offset:11616
	s_waitcnt lgkmcnt(0)
	global_store_dwordx4 v[10:11], v[2:5], off sc1
	s_nop 1
	v_add_u32_e32 v10, 24, v8
	v_ashrrev_i32_e32 v11, 31, v10
	v_lshlrev_b64 v[10:11], 12, v[10:11]
	v_lshl_add_u64 v[10:11], s[18:19], 0, v[10:11]
	v_lshl_add_u64 v[10:11], v[10:11], 0, s[22:23]
	v_lshl_add_u64 v[10:11], v[10:11], 0, v[146:147]
	ds_read_b128 v[2:5], v6 offset:12672
	s_waitcnt lgkmcnt(0)
	global_store_dwordx4 v[10:11], v[2:5], off sc1
	s_nop 1
	v_add_u32_e32 v10, 26, v8
	v_ashrrev_i32_e32 v11, 31, v10
	v_lshlrev_b64 v[10:11], 12, v[10:11]
	v_lshl_add_u64 v[10:11], s[18:19], 0, v[10:11]
	v_lshl_add_u64 v[10:11], v[10:11], 0, s[22:23]
	v_lshl_add_u64 v[10:11], v[10:11], 0, v[146:147]
	ds_read_b128 v[2:5], v6 offset:13728
	s_waitcnt lgkmcnt(0)
	global_store_dwordx4 v[10:11], v[2:5], off sc1
	s_nop 1
	v_add_u32_e32 v10, 28, v8
	v_ashrrev_i32_e32 v11, 31, v10
	v_lshlrev_b64 v[10:11], 12, v[10:11]
	v_lshl_add_u64 v[10:11], s[18:19], 0, v[10:11]
	v_lshl_add_u64 v[10:11], v[10:11], 0, s[22:23]
	ds_read_b128 v[2:5], v6 offset:14784
	v_lshl_add_u64 v[10:11], v[10:11], 0, v[146:147]
	s_waitcnt lgkmcnt(0)
	global_store_dwordx4 v[10:11], v[2:5], off sc1
	s_nop 1
	ds_read_b128 v[2:5], v6 offset:15840
	v_add_u32_e32 v6, 30, v8
	v_ashrrev_i32_e32 v7, 31, v6
	v_lshlrev_b64 v[6:7], 12, v[6:7]
	v_lshl_add_u64 v[6:7], s[18:19], 0, v[6:7]
	v_lshl_add_u64 v[6:7], v[6:7], 0, s[22:23]
	v_lshl_add_u64 v[6:7], v[6:7], 0, v[146:147]
	s_waitcnt lgkmcnt(0)
	global_store_dwordx4 v[6:7], v[2:5], off sc1
	s_nop 1
	s_waitcnt lgkmcnt(0)
	s_barrier
	s_cbranch_vccnz .LBB0_1127
	s_waitcnt vmcnt(0)
	s_barrier
	s_and_saveexec_b64 s[4:5], s[0:1]
	s_cbranch_execz .LBB0_1126
	s_mov_b64 s[6:7], exec
	v_mbcnt_lo_u32_b32 v2, s6, 0
	v_mbcnt_hi_u32_b32 v2, s7, v2
	v_cmp_eq_u32_e32 vcc, 0, v2
	s_and_b64 s[22:23], exec, vcc
	s_mov_b64 exec, s[22:23]
	s_cbranch_execz .LBB0_1126
	s_lshl_b32 s22, s37, 4
	s_ashr_i32 s23, s22, 31
	s_lshl_b64 s[22:23], s[22:23], 2
	s_add_u32 s22, s29, s22
	s_addc_u32 s23, s30, s23
	s_bcnt1_i32_b64 s6, s[6:7]
	v_mov_b32_e32 v2, s6
	global_atomic_add v147, v2, s[22:23]
	s_branch .LBB0_1126

.Lrot_mo:
	ds_read_b64_tr_b16 v[216:217], v240
	ds_read_b64_tr_b16 v[218:219], v240 offset:2048
	ds_read_b64_tr_b16 v[220:221], v244
	ds_read_b64_tr_b16 v[222:223], v244 offset:2048
	ds_read_b128 v[162:165], v241
	ds_read_b128 v[166:169], v241 offset:2048
	ds_read_b64_tr_b16 v[224:225], v246
	ds_read_b64_tr_b16 v[226:227], v246 offset:2048
	ds_read_b64_tr_b16 v[228:229], v248
	ds_read_b64_tr_b16 v[230:231], v248 offset:2048
	s_waitcnt lgkmcnt(5)
	v_mfma_f32_16x16x32_bf16 v[62:65], v[216:219], v[162:165], v[62:65]
	ds_read_b128 v[232:235], v241 offset:4096
	s_and_b32 s87, s37, 0x8000
	s_add_i32 s88, s36, s84
	v_mfma_f32_16x16x32_bf16 v[58:61], v[220:223], v[162:165], v[58:61]
	s_mov_b32 s89, m0
	s_mov_b32 m0, s88
	s_nop 0
	global_load_lds_dwordx4 v215, s[18:19]
	s_mov_b32 m0, s89
	s_waitcnt lgkmcnt(3)
	v_mfma_f32_16x16x32_bf16 v[54:57], v[224:227], v[162:165], v[54:57]
	s_waitcnt lgkmcnt(1)
	v_mfma_f32_16x16x32_bf16 v[42:45], v[228:231], v[162:165], v[42:45]
	v_mfma_f32_16x16x32_bf16 v[50:53], v[216:219], v[166:169], v[50:53]
	ds_read_b128 v[162:165], v241 offset:6144
	s_add_i32 s89, s88, 0x2000
	s_mov_b32 s90, m0
	s_mov_b32 m0, s89
	s_nop 0
	global_load_lds_dwordx4 v214, s[18:19]
	s_mov_b32 m0, s90
	v_mfma_f32_16x16x32_bf16 v[46:49], v[220:223], v[166:169], v[46:49]
	v_mfma_f32_16x16x32_bf16 v[38:41], v[224:227], v[166:169], v[38:41]
	v_mfma_f32_16x16x32_bf16 v[34:37], v[228:231], v[166:169], v[34:37]
	s_waitcnt lgkmcnt(1)
	v_mfma_f32_16x16x32_bf16 v[66:69], v[216:219], v[232:235], v[66:69]
	ds_read_b128 v[166:169], v241 offset:8192
	s_add_i32 s89, s88, 0x4000
	s_mov_b32 s90, m0
	s_mov_b32 m0, s89
	s_nop 0
	global_load_lds_dwordx4 v213, s[18:19]
	s_mov_b32 m0, s90
	v_mfma_f32_16x16x32_bf16 v[70:73], v[220:223], v[232:235], v[70:73]
	v_mfma_f32_16x16x32_bf16 v[74:77], v[224:227], v[232:235], v[74:77]
	v_mfma_f32_16x16x32_bf16 v[78:81], v[228:231], v[232:235], v[78:81]
	s_waitcnt lgkmcnt(1)
	v_mfma_f32_16x16x32_bf16 v[82:85], v[216:219], v[162:165], v[82:85]
	ds_read_b128 v[232:235], v241 offset:10240
	s_addk_i32 s88, 0x6000
	s_mov_b32 s89, m0
	s_mov_b32 m0, s88
	s_nop 0
	global_load_lds_dwordx4 v212, s[18:19]
	s_mov_b32 m0, s89
	v_mfma_f32_16x16x32_bf16 v[86:89], v[220:223], v[162:165], v[86:89]
	v_mfma_f32_16x16x32_bf16 v[90:93], v[224:227], v[162:165], v[90:93]
	v_mfma_f32_16x16x32_bf16 v[94:97], v[228:231], v[162:165], v[94:97]
	ds_read_b128 v[236:239], v241 offset:12288
	ds_read_b64_tr_b16 v[162:163], v240 offset:16384
	ds_read_b64_tr_b16 v[164:165], v240 offset:18432
	s_waitcnt lgkmcnt(4)
	v_mfma_f32_16x16x32_bf16 v[98:101], v[216:219], v[166:169], v[98:101]
	v_mfma_f32_16x16x32_bf16 v[102:105], v[220:223], v[166:169], v[102:105]
	v_mfma_f32_16x16x32_bf16 v[106:109], v[224:227], v[166:169], v[106:109]
	v_mfma_f32_16x16x32_bf16 v[110:113], v[228:231], v[166:169], v[110:113]
	ds_read_b128 v[240:243], v241 offset:14336
	ds_read_b64_tr_b16 v[166:167], v244 offset:16384
	ds_read_b64_tr_b16 v[168:169], v244 offset:18432
	s_waitcnt lgkmcnt(6)
	v_mfma_f32_16x16x32_bf16 v[114:117], v[216:219], v[232:235], v[114:117]
	v_mfma_f32_16x16x32_bf16 v[118:121], v[220:223], v[232:235], v[118:121]
	v_mfma_f32_16x16x32_bf16 v[122:125], v[224:227], v[232:235], v[122:125]
	v_mfma_f32_16x16x32_bf16 v[126:129], v[228:231], v[232:235], v[126:129]
	v_add_u32_e32 v249, s86, v187
	ds_read_b128 v[232:235], v249
	ds_read_b64_tr_b16 v[244:245], v246 offset:16384
	ds_read_b64_tr_b16 v[246:247], v246 offset:18432
	s_waitcnt lgkmcnt(8)
	v_mfma_f32_16x16x32_bf16 v[130:133], v[216:219], v[236:239], v[130:133]
	v_mfma_f32_16x16x32_bf16 v[134:137], v[220:223], v[236:239], v[134:137]
	v_mfma_f32_16x16x32_bf16 v[138:141], v[224:227], v[236:239], v[138:141]
	v_mfma_f32_16x16x32_bf16 v[142:145], v[228:231], v[236:239], v[142:145]
	s_waitcnt lgkmcnt(5)
	v_mfma_f32_16x16x32_bf16 v[146:149], v[216:219], v[240:243], v[146:149]
	v_mfma_f32_16x16x32_bf16 v[150:153], v[220:223], v[240:243], v[150:153]
	ds_read_b128 v[216:219], v249 offset:2048
	ds_read_b64_tr_b16 v[220:221], v248 offset:16384
	ds_read_b64_tr_b16 v[222:223], v248 offset:18432
	v_mfma_f32_16x16x32_bf16 v[154:157], v[224:227], v[240:243], v[154:157]
	v_mfma_f32_16x16x32_bf16 v[158:161], v[228:231], v[240:243], v[158:161]
	ds_read_b128 v[224:227], v249 offset:4096
	s_waitcnt lgkmcnt(6)
	v_mfma_f32_16x16x32_bf16 v[62:65], v[162:165], v[232:235], v[62:65]
	s_add_u32 s88, s40, s2
	s_waitcnt vmcnt(11)
	s_addc_u32 s89, s41, s3
	v_mfma_f32_16x16x32_bf16 v[58:61], v[166:169], v[232:235], v[58:61]
	v_cvt_pk_bf16_f32 v30, v30, v31
	v_cvt_pk_bf16_f32 v31, v32, v33
	v_add_u32_e32 v236, s87, v189
	s_waitcnt lgkmcnt(4)
	v_mfma_f32_16x16x32_bf16 v[54:57], v[244:247], v[232:235], v[54:57]
	s_add_u32 s86, s88, 0x160000
	ds_write_b64 v236, v[30:31]
	s_addc_u32 s87, s89, 0
	s_waitcnt lgkmcnt(2)
	v_mfma_f32_16x16x32_bf16 v[42:45], v[220:223], v[232:235], v[42:45]
	global_load_dwordx4 v[30:33], v199, s[86:87]
	v_mfma_f32_16x16x32_bf16 v[50:53], v[162:165], v[216:219], v[50:53]
	ds_read_b128 v[228:231], v249 offset:6144
	s_waitcnt vmcnt(11)
	s_add_u32 s86, s88, 0x18c000
	v_mfma_f32_16x16x32_bf16 v[46:49], v[166:169], v[216:219], v[46:49]
	v_cvt_pk_bf16_f32 v26, v26, v27
	v_cvt_pk_bf16_f32 v27, v28, v29
	ds_write_b64 v236, v[26:27] offset:8192
	v_mfma_f32_16x16x32_bf16 v[38:41], v[244:247], v[216:219], v[38:41]
	s_addc_u32 s87, s89, 0
	global_load_dwordx4 v[26:29], v199, s[86:87]
	v_mfma_f32_16x16x32_bf16 v[34:37], v[220:223], v[216:219], v[34:37]
	s_waitcnt lgkmcnt(3)
	v_mfma_f32_16x16x32_bf16 v[66:69], v[162:165], v[224:227], v[66:69]
	ds_read_b128 v[216:219], v249 offset:8192
	s_waitcnt vmcnt(11)
	s_add_u32 s86, s88, 0x1b8000
	v_mfma_f32_16x16x32_bf16 v[70:73], v[166:169], v[224:227], v[70:73]
	v_cvt_pk_bf16_f32 v22, v22, v23
	v_cvt_pk_bf16_f32 v23, v24, v25
	ds_write_b64 v236, v[22:23] offset:16384
	v_mfma_f32_16x16x32_bf16 v[74:77], v[244:247], v[224:227], v[74:77]
	s_addc_u32 s87, s89, 0
	global_load_dwordx4 v[22:25], v199, s[86:87]
	v_mfma_f32_16x16x32_bf16 v[78:81], v[220:223], v[224:227], v[78:81]
	s_waitcnt lgkmcnt(3)
	v_mfma_f32_16x16x32_bf16 v[82:85], v[162:165], v[228:231], v[82:85]
	ds_read_b128 v[224:227], v249 offset:10240
	s_waitcnt vmcnt(11)
	s_add_u32 s86, s88, 0x1e4000
	v_mfma_f32_16x16x32_bf16 v[86:89], v[166:169], v[228:231], v[86:89]
	v_cvt_pk_bf16_f32 v18, v18, v19
	v_cvt_pk_bf16_f32 v19, v20, v21
	ds_write_b64 v236, v[18:19] offset:24576
	v_mfma_f32_16x16x32_bf16 v[90:93], v[244:247], v[228:231], v[90:93]
	s_addc_u32 s87, s89, 0
	global_load_dwordx4 v[18:21], v199, s[86:87]
	v_mfma_f32_16x16x32_bf16 v[94:97], v[220:223], v[228:231], v[94:97]
	ds_read_b128 v[228:231], v249 offset:12288
	s_waitcnt lgkmcnt(4)
	v_mfma_f32_16x16x32_bf16 v[98:101], v[162:165], v[216:219], v[98:101]
	s_add_u32 s88, s38, s2
	s_waitcnt vmcnt(11)
	s_addc_u32 s89, s39, s3
	v_mfma_f32_16x16x32_bf16 v[102:105], v[166:169], v[216:219], v[102:105]
	v_cvt_pk_bf16_f32 v14, v14, v15
	v_cvt_pk_bf16_f32 v15, v16, v17
	s_add_u32 s86, s88, 0x160000
	v_mfma_f32_16x16x32_bf16 v[106:109], v[244:247], v[216:219], v[106:109]
	ds_write_b64 v236, v[14:15] offset:256
	s_addc_u32 s87, s89, 0
	global_load_dwordx4 v[14:17], v199, s[86:87]
	v_mfma_f32_16x16x32_bf16 v[110:113], v[220:223], v[216:219], v[110:113]
	s_waitcnt lgkmcnt(3)
	v_mfma_f32_16x16x32_bf16 v[114:117], v[162:165], v[224:227], v[114:117]
	ds_read_b128 v[216:219], v249 offset:14336
	s_waitcnt vmcnt(11)
	s_add_u32 s86, s88, 0x18c000
	v_mfma_f32_16x16x32_bf16 v[118:121], v[166:169], v[224:227], v[118:121]
	v_cvt_pk_bf16_f32 v10, v10, v11
	v_cvt_pk_bf16_f32 v11, v12, v13
	ds_write_b64 v236, v[10:11] offset:8448
	v_mfma_f32_16x16x32_bf16 v[122:125], v[244:247], v[224:227], v[122:125]
	s_addc_u32 s87, s89, 0
	global_load_dwordx4 v[10:13], v199, s[86:87]
	v_mfma_f32_16x16x32_bf16 v[126:129], v[220:223], v[224:227], v[126:129]
	s_waitcnt lgkmcnt(3)
	v_mfma_f32_16x16x32_bf16 v[130:133], v[162:165], v[228:231], v[130:133]
	s_waitcnt vmcnt(11)
	s_add_u32 s86, s88, 0x1b8000
	v_cvt_pk_bf16_f32 v6, v6, v7
	v_mfma_f32_16x16x32_bf16 v[134:137], v[166:169], v[228:231], v[134:137]
	v_cvt_pk_bf16_f32 v7, v8, v9
	ds_write_b64 v236, v[6:7] offset:16640
	s_addc_u32 s87, s89, 0
	v_mfma_f32_16x16x32_bf16 v[138:141], v[244:247], v[228:231], v[138:141]
	global_load_dwordx4 v[6:9], v199, s[86:87]
	v_mfma_f32_16x16x32_bf16 v[142:145], v[220:223], v[228:231], v[142:145]
	s_waitcnt lgkmcnt(2)
	v_mfma_f32_16x16x32_bf16 v[146:149], v[162:165], v[216:219], v[146:149]
	s_waitcnt vmcnt(11)
	s_add_u32 s86, s88, 0x1e4000
	v_cvt_pk_bf16_f32 v2, v2, v3
	v_mfma_f32_16x16x32_bf16 v[150:153], v[166:169], v[216:219], v[150:153]
	v_cvt_pk_bf16_f32 v3, v4, v5
	ds_write_b64 v236, v[2:3] offset:24832
	s_addc_u32 s87, s89, 0
	v_mfma_f32_16x16x32_bf16 v[154:157], v[244:247], v[216:219], v[154:157]
	global_load_dwordx4 v[2:5], v199, s[86:87]
	v_mfma_f32_16x16x32_bf16 v[158:161], v[220:223], v[216:219], v[158:161]
	s_add_i32 s86, s85, 0x8000
	s_cmp_lg_u32 s85, 0x10000
	s_cselect_b32 s85, s86, 0
	s_add_i32 s86, s84, 0x8000
	s_cmp_lg_u32 s84, 0x10000
	s_cselect_b32 s84, s86, 0
	s_add_u32 s2, s2, 0xb0000
	s_addc_u32 s3, s3, 0
	s_add_i32 s37, s37, 0x8000
	v_add_u32_e32 v212, 0x80, v212
	v_add_u32_e32 v213, 0x80, v213
	v_add_u32_e32 v214, 0x80, v214
	v_add_u32_e32 v215, 0x80, v215
	s_add_i32 s87, s37, 0xffff8000
	s_and_b32 s87, s87, 0x8000
	s_add_i32 s87, s87, 0
	s_add_i32 s86, s85, 0
	s_add_i32 s87, s87, 0x18000
	v_add_u32_e32 v240, s87, v185
	v_add_u32_e32 v241, s86, v183
	v_add_u32_e32 v246, s87, v181
	v_add_u32_e32 v248, s87, v172
	v_add_u32_e32 v244, s87, v184
	s_waitcnt lgkmcnt(0)
	s_barrier
	s_cmp_lg_u32 s2, 0xb00000
	s_cbranch_scc1 .Lrot_mo
	v_add_u32_e32 v189, s52, v185
	v_add_u32_e32 v236, 0, v183
	v_add_u32_e32 v242, s52, v181
	v_add_u32_e32 v244, s52, v172
	v_add_u32_e32 v238, s52, v184
	ds_read_b64_tr_b16 v[162:163], v189
	ds_read_b64_tr_b16 v[164:165], v189 offset:2048
	ds_read_b64_tr_b16 v[166:167], v238
	ds_read_b64_tr_b16 v[168:169], v238 offset:2048
	ds_read_b128 v[212:215], v236 offset:32768
	ds_read_b128 v[216:219], v236 offset:34816
	ds_read_b64_tr_b16 v[220:221], v242
	ds_read_b64_tr_b16 v[222:223], v242 offset:2048
	ds_read_b64_tr_b16 v[224:225], v244
	ds_read_b64_tr_b16 v[226:227], v244 offset:2048
	s_waitcnt lgkmcnt(5)
	v_mfma_f32_16x16x32_bf16 v[62:65], v[162:165], v[212:215], v[62:65]
	ds_read_b128 v[228:231], v236 offset:36864
	v_mfma_f32_16x16x32_bf16 v[58:61], v[166:169], v[212:215], v[58:61]
	s_waitcnt lgkmcnt(3)
	v_mfma_f32_16x16x32_bf16 v[54:57], v[220:223], v[212:215], v[54:57]
	s_waitcnt lgkmcnt(1)
	v_mfma_f32_16x16x32_bf16 v[42:45], v[224:227], v[212:215], v[42:45]
	v_mfma_f32_16x16x32_bf16 v[50:53], v[162:165], v[216:219], v[50:53]
	ds_read_b128 v[212:215], v236 offset:38912
	v_mfma_f32_16x16x32_bf16 v[46:49], v[166:169], v[216:219], v[46:49]
	v_mfma_f32_16x16x32_bf16 v[38:41], v[220:223], v[216:219], v[38:41]
	v_mfma_f32_16x16x32_bf16 v[34:37], v[224:227], v[216:219], v[34:37]
	s_waitcnt lgkmcnt(1)
	v_mfma_f32_16x16x32_bf16 v[66:69], v[162:165], v[228:231], v[66:69]
	ds_read_b128 v[216:219], v236 offset:40960
	v_mfma_f32_16x16x32_bf16 v[70:73], v[166:169], v[228:231], v[70:73]
	v_mfma_f32_16x16x32_bf16 v[74:77], v[220:223], v[228:231], v[74:77]
	v_mfma_f32_16x16x32_bf16 v[78:81], v[224:227], v[228:231], v[78:81]
	s_waitcnt lgkmcnt(1)
	v_mfma_f32_16x16x32_bf16 v[82:85], v[162:165], v[212:215], v[82:85]
	ds_read_b128 v[228:231], v236 offset:43008
	v_mfma_f32_16x16x32_bf16 v[86:89], v[166:169], v[212:215], v[86:89]
	v_mfma_f32_16x16x32_bf16 v[90:93], v[220:223], v[212:215], v[90:93]
	v_mfma_f32_16x16x32_bf16 v[94:97], v[224:227], v[212:215], v[94:97]
	ds_read_b128 v[212:215], v236 offset:45056
	ds_read_b64_tr_b16 v[232:233], v189 offset:16384
	ds_read_b64_tr_b16 v[234:235], v189 offset:18432
	s_waitcnt lgkmcnt(4)
	v_mfma_f32_16x16x32_bf16 v[98:101], v[162:165], v[216:219], v[98:101]
	v_mfma_f32_16x16x32_bf16 v[102:105], v[166:169], v[216:219], v[102:105]
	v_mfma_f32_16x16x32_bf16 v[106:109], v[220:223], v[216:219], v[106:109]
	v_mfma_f32_16x16x32_bf16 v[110:113], v[224:227], v[216:219], v[110:113]
	ds_read_b128 v[216:219], v236 offset:47104
	ds_read_b64_tr_b16 v[236:237], v238 offset:16384
	ds_read_b64_tr_b16 v[238:239], v238 offset:18432
	s_waitcnt lgkmcnt(6)
	v_mfma_f32_16x16x32_bf16 v[114:117], v[162:165], v[228:231], v[114:117]
	v_mfma_f32_16x16x32_bf16 v[118:121], v[166:169], v[228:231], v[118:121]
	v_mfma_f32_16x16x32_bf16 v[122:125], v[220:223], v[228:231], v[122:125]
	v_mfma_f32_16x16x32_bf16 v[126:129], v[224:227], v[228:231], v[126:129]
	v_add_u32_e32 v189, 0, v187
	ds_read_b128 v[228:231], v189 offset:32768
	ds_read_b64_tr_b16 v[240:241], v242 offset:16384
	ds_read_b64_tr_b16 v[242:243], v242 offset:18432
	s_waitcnt lgkmcnt(8)
	v_mfma_f32_16x16x32_bf16 v[130:133], v[162:165], v[212:215], v[130:133]
	v_mfma_f32_16x16x32_bf16 v[134:137], v[166:169], v[212:215], v[134:137]
	v_mfma_f32_16x16x32_bf16 v[138:141], v[220:223], v[212:215], v[138:141]
	v_mfma_f32_16x16x32_bf16 v[142:145], v[224:227], v[212:215], v[142:145]
	s_waitcnt lgkmcnt(5)
	v_mfma_f32_16x16x32_bf16 v[146:149], v[162:165], v[216:219], v[146:149]
	v_mfma_f32_16x16x32_bf16 v[150:153], v[166:169], v[216:219], v[150:153]
	ds_read_b128 v[162:165], v189 offset:34816
	ds_read_b64_tr_b16 v[166:167], v244 offset:16384
	ds_read_b64_tr_b16 v[168:169], v244 offset:18432
	v_mfma_f32_16x16x32_bf16 v[154:157], v[220:223], v[216:219], v[154:157]
	v_mfma_f32_16x16x32_bf16 v[158:161], v[224:227], v[216:219], v[158:161]
	ds_read_b128 v[212:215], v189 offset:36864
	s_waitcnt vmcnt(7)
	v_add_u32_e32 v188, s56, v188
	v_cvt_pk_bf16_f32 v30, v30, v31
	v_cvt_pk_bf16_f32 v31, v32, v33
	s_waitcnt lgkmcnt(6)
	v_mfma_f32_16x16x32_bf16 v[62:65], v[232:235], v[228:231], v[62:65]
	ds_write_b64 v188, v[30:31]
	v_mfma_f32_16x16x32_bf16 v[58:61], v[236:239], v[228:231], v[58:61]
	s_waitcnt lgkmcnt(5)
	v_mfma_f32_16x16x32_bf16 v[54:57], v[240:243], v[228:231], v[54:57]
	s_waitcnt lgkmcnt(2)
	v_mfma_f32_16x16x32_bf16 v[30:33], v[166:169], v[228:231], v[42:45]
	v_mfma_f32_16x16x32_bf16 v[42:45], v[232:235], v[162:165], v[50:53]
	s_nop 2
	ds_read_b128 v[50:53], v189 offset:38912
	s_waitcnt vmcnt(6)
	v_mfma_f32_16x16x32_bf16 v[46:49], v[236:239], v[162:165], v[46:49]
	v_cvt_pk_bf16_f32 v26, v26, v27
	v_cvt_pk_bf16_f32 v27, v28, v29
	ds_write_b64 v188, v[26:27] offset:8192
	v_mfma_f32_16x16x32_bf16 v[38:41], v[240:243], v[162:165], v[38:41]
	v_mfma_f32_16x16x32_bf16 v[26:29], v[166:169], v[162:165], v[34:37]
	s_waitcnt lgkmcnt(3)
	v_mfma_f32_16x16x32_bf16 v[34:37], v[232:235], v[212:215], v[66:69]
	v_mfma_f32_16x16x32_bf16 v[66:69], v[236:239], v[212:215], v[70:73]
	s_nop 2
	ds_read_b128 v[70:73], v189 offset:40960
	s_waitcnt vmcnt(5)
	v_mfma_f32_16x16x32_bf16 v[74:77], v[240:243], v[212:215], v[74:77]
	v_cvt_pk_bf16_f32 v22, v22, v23
	v_cvt_pk_bf16_f32 v23, v24, v25
	ds_write_b64 v188, v[22:23] offset:16384
	v_mfma_f32_16x16x32_bf16 v[22:25], v[166:169], v[212:215], v[78:81]
	s_waitcnt lgkmcnt(3)
	v_mfma_f32_16x16x32_bf16 v[78:81], v[232:235], v[50:53], v[82:85]
	v_mfma_f32_16x16x32_bf16 v[82:85], v[236:239], v[50:53], v[86:89]
	s_nop 2
	ds_read_b128 v[86:89], v189 offset:43008
	s_waitcnt vmcnt(4)
	v_mfma_f32_16x16x32_bf16 v[90:93], v[240:243], v[50:53], v[90:93]
	v_cvt_pk_bf16_f32 v18, v18, v19
	v_cvt_pk_bf16_f32 v19, v20, v21
	ds_write_b64 v188, v[18:19] offset:24576
	v_mfma_f32_16x16x32_bf16 v[18:21], v[166:169], v[50:53], v[94:97]
	s_waitcnt lgkmcnt(3)
	v_mfma_f32_16x16x32_bf16 v[50:53], v[232:235], v[70:73], v[98:101]
	v_add_u32_e32 v162, s56, v186
	s_nop 1
	ds_read_b128 v[98:101], v189 offset:45056
	s_waitcnt vmcnt(3)
	v_mfma_f32_16x16x32_bf16 v[94:97], v[236:239], v[70:73], v[102:105]
	v_cvt_pk_bf16_f32 v14, v14, v15
	v_cvt_pk_bf16_f32 v15, v16, v17
	ds_write_b64 v162, v[14:15]
	v_mfma_f32_16x16x32_bf16 v[102:105], v[240:243], v[70:73], v[106:109]
	v_mfma_f32_16x16x32_bf16 v[14:17], v[166:169], v[70:73], v[110:113]
	s_nop 2
	ds_read_b128 v[110:113], v189 offset:47104
	s_waitcnt vmcnt(2)
	s_waitcnt lgkmcnt(4)
	v_mfma_f32_16x16x32_bf16 v[70:73], v[232:235], v[86:89], v[114:117]
	v_cvt_pk_bf16_f32 v10, v10, v11
	v_cvt_pk_bf16_f32 v11, v12, v13
	ds_write_b64 v162, v[10:11] offset:8192
	v_mfma_f32_16x16x32_bf16 v[106:109], v[236:239], v[86:89], v[118:121]
	v_mfma_f32_16x16x32_bf16 v[114:117], v[240:243], v[86:89], v[122:125]
	v_mfma_f32_16x16x32_bf16 v[10:13], v[166:169], v[86:89], v[126:129]
	s_waitcnt vmcnt(1)
	s_waitcnt lgkmcnt(3)
	v_mfma_f32_16x16x32_bf16 v[86:89], v[232:235], v[98:101], v[130:133]
	v_cvt_pk_bf16_f32 v6, v6, v7
	v_cvt_pk_bf16_f32 v7, v8, v9
	ds_write_b64 v162, v[6:7] offset:16384
	v_mfma_f32_16x16x32_bf16 v[118:121], v[236:239], v[98:101], v[134:137]
	v_mfma_f32_16x16x32_bf16 v[122:125], v[240:243], v[98:101], v[138:141]
	v_mfma_f32_16x16x32_bf16 v[6:9], v[166:169], v[98:101], v[142:145]
	s_waitcnt vmcnt(0)
	s_waitcnt lgkmcnt(2)
	v_mfma_f32_16x16x32_bf16 v[98:101], v[232:235], v[110:113], v[146:149]
	v_cvt_pk_bf16_f32 v2, v2, v3
	v_cvt_pk_bf16_f32 v3, v4, v5
	ds_write_b64 v162, v[2:3] offset:24576
	v_mfma_f32_16x16x32_bf16 v[126:129], v[236:239], v[110:113], v[150:153]
	v_mfma_f32_16x16x32_bf16 v[2:5], v[166:169], v[110:113], v[158:161]
	v_mfma_f32_16x16x32_bf16 v[130:133], v[240:243], v[110:113], v[154:157]
	s_add_i32 s2, 0, 0x10000
	s_waitcnt lgkmcnt(0)
	s_barrier
	v_add_u32_e32 v168, s56, v185
	v_add_u32_e32 v183, s2, v183
	v_add_u32_e32 v181, s56, v181
	v_add_u32_e32 v172, s56, v172
	v_add_u32_e32 v184, s56, v184
	ds_read_b64_tr_b16 v[110:111], v168
	ds_read_b64_tr_b16 v[112:113], v168 offset:2048
	ds_read_b64_tr_b16 v[134:135], v184
	ds_read_b64_tr_b16 v[136:137], v184 offset:2048
	ds_read_b128 v[138:141], v183
	ds_read_b128 v[142:145], v183 offset:2048
	ds_read_b64_tr_b16 v[146:147], v181
	ds_read_b64_tr_b16 v[148:149], v181 offset:2048
	ds_read_b64_tr_b16 v[150:151], v172
	ds_read_b64_tr_b16 v[152:153], v172 offset:2048
	s_waitcnt lgkmcnt(5)
	v_mfma_f32_16x16x32_bf16 v[62:65], v[110:113], v[138:141], v[62:65]
	ds_read_b128 v[154:157], v183 offset:4096
	v_mfma_f32_16x16x32_bf16 v[58:61], v[134:137], v[138:141], v[58:61]
	s_waitcnt lgkmcnt(3)
	v_mfma_f32_16x16x32_bf16 v[54:57], v[146:149], v[138:141], v[54:57]
	s_waitcnt lgkmcnt(1)
	v_mfma_f32_16x16x32_bf16 v[30:33], v[150:153], v[138:141], v[30:33]
	v_mfma_f32_16x16x32_bf16 v[42:45], v[110:113], v[142:145], v[42:45]
	ds_read_b128 v[138:141], v183 offset:6144
	v_mfma_f32_16x16x32_bf16 v[46:49], v[134:137], v[142:145], v[46:49]
	v_mfma_f32_16x16x32_bf16 v[38:41], v[146:149], v[142:145], v[38:41]
	v_mfma_f32_16x16x32_bf16 v[26:29], v[150:153], v[142:145], v[26:29]
	s_waitcnt lgkmcnt(1)
	v_mfma_f32_16x16x32_bf16 v[34:37], v[110:113], v[154:157], v[34:37]
	ds_read_b128 v[142:145], v183 offset:8192
	v_mfma_f32_16x16x32_bf16 v[66:69], v[134:137], v[154:157], v[66:69]
	v_mfma_f32_16x16x32_bf16 v[74:77], v[146:149], v[154:157], v[74:77]
	v_mfma_f32_16x16x32_bf16 v[22:25], v[150:153], v[154:157], v[22:25]
	s_waitcnt lgkmcnt(1)
	v_mfma_f32_16x16x32_bf16 v[154:157], v[134:137], v[138:141], v[82:85]
	s_nop 2
	ds_read_b128 v[82:85], v183 offset:10240
	v_mfma_f32_16x16x32_bf16 v[78:81], v[110:113], v[138:141], v[78:81]
	v_mfma_f32_16x16x32_bf16 v[18:21], v[150:153], v[138:141], v[18:21]
	v_mfma_f32_16x16x32_bf16 v[158:161], v[146:149], v[138:141], v[90:93]
	s_nop 2
	ds_read_b128 v[90:93], v183 offset:12288
	ds_read_b64_tr_b16 v[166:167], v168 offset:16384
	ds_read_b64_tr_b16 v[168:169], v168 offset:18432
	s_waitcnt lgkmcnt(4)
	v_mfma_f32_16x16x32_bf16 v[50:53], v[110:113], v[142:145], v[50:53]
	v_mfma_f32_16x16x32_bf16 v[14:17], v[150:153], v[142:145], v[14:17]
	v_mfma_f32_16x16x32_bf16 v[138:141], v[134:137], v[142:145], v[94:97]
	v_mfma_f32_16x16x32_bf16 v[162:165], v[146:149], v[142:145], v[102:105]
	s_waitcnt lgkmcnt(3)
	v_mfma_f32_16x16x32_bf16 v[142:145], v[110:113], v[82:85], v[70:73]
	s_nop 2
	ds_read_b128 v[70:73], v183 offset:14336
	ds_read_b64_tr_b16 v[220:221], v184 offset:16384
	ds_read_b64_tr_b16 v[222:223], v184 offset:18432
	v_mfma_f32_16x16x32_bf16 v[10:13], v[150:153], v[82:85], v[10:13]
	v_mfma_f32_16x16x32_bf16 v[212:215], v[134:137], v[82:85], v[106:109]
	v_mfma_f32_16x16x32_bf16 v[216:219], v[146:149], v[82:85], v[114:117]
	v_add_u32_e32 v183, s2, v187
	ds_read_b128 v[82:85], v183
	ds_read_b64_tr_b16 v[232:233], v181 offset:16384
	ds_read_b64_tr_b16 v[234:235], v181 offset:18432
	s_waitcnt lgkmcnt(8)
	v_mfma_f32_16x16x32_bf16 v[6:9], v[150:153], v[90:93], v[6:9]
	v_mfma_f32_16x16x32_bf16 v[224:227], v[110:113], v[90:93], v[86:89]
	v_mfma_f32_16x16x32_bf16 v[228:231], v[134:137], v[90:93], v[118:121]
	v_mfma_f32_16x16x32_bf16 v[184:187], v[146:149], v[90:93], v[122:125]
	s_waitcnt lgkmcnt(5)
	v_mfma_f32_16x16x32_bf16 v[130:133], v[146:149], v[70:73], v[130:133]
	ds_read_b128 v[86:89], v183 offset:2048
	ds_read_b64_tr_b16 v[146:147], v172 offset:16384
	ds_read_b64_tr_b16 v[148:149], v172 offset:18432
	v_mfma_f32_16x16x32_bf16 v[2:5], v[150:153], v[70:73], v[2:5]
	v_mfma_f32_16x16x32_bf16 v[236:239], v[110:113], v[70:73], v[98:101]
	v_mfma_f32_16x16x32_bf16 v[134:137], v[134:137], v[70:73], v[126:129]
	s_waitcnt lgkmcnt(3)
	v_mfma_f32_16x16x32_bf16 v[122:125], v[232:235], v[82:85], v[54:57]
	s_nop 2
	ds_read_b128 v[54:57], v183 offset:4096
	v_mfma_f32_16x16x32_bf16 v[126:129], v[166:169], v[82:85], v[62:65]
	v_mfma_f32_16x16x32_bf16 v[118:121], v[220:223], v[82:85], v[58:61]
	s_waitcnt lgkmcnt(1)
	v_mfma_f32_16x16x32_bf16 v[114:117], v[146:149], v[82:85], v[30:33]
	s_nop 2
	ds_read_b128 v[30:33], v183 offset:6144
	v_mfma_f32_16x16x32_bf16 v[110:113], v[166:169], v[86:89], v[42:45]
	v_mfma_f32_16x16x32_bf16 v[102:105], v[220:223], v[86:89], v[46:49]
	v_mfma_f32_16x16x32_bf16 v[106:109], v[232:235], v[86:89], v[38:41]
	v_mfma_f32_16x16x32_bf16 v[98:101], v[146:149], v[86:89], v[26:29]
	s_nop 2
	ds_read_b128 v[26:29], v183 offset:8192
	s_waitcnt lgkmcnt(2)
	v_mfma_f32_16x16x32_bf16 v[94:97], v[166:169], v[54:57], v[34:37]
	v_mfma_f32_16x16x32_bf16 v[86:89], v[220:223], v[54:57], v[66:69]
	v_mfma_f32_16x16x32_bf16 v[90:93], v[232:235], v[54:57], v[74:77]
	v_mfma_f32_16x16x32_bf16 v[82:85], v[146:149], v[54:57], v[22:25]
	s_nop 2
	ds_read_b128 v[22:25], v183 offset:10240
	s_waitcnt lgkmcnt(2)
	v_mfma_f32_16x16x32_bf16 v[78:81], v[166:169], v[30:33], v[78:81]
	v_mfma_f32_16x16x32_bf16 v[70:73], v[220:223], v[30:33], v[154:157]
	v_mfma_f32_16x16x32_bf16 v[74:77], v[232:235], v[30:33], v[158:161]
	v_mfma_f32_16x16x32_bf16 v[66:69], v[146:149], v[30:33], v[18:21]
	s_nop 2
	ds_read_b128 v[18:21], v183 offset:12288
	s_waitcnt lgkmcnt(2)
	v_mfma_f32_16x16x32_bf16 v[62:65], v[166:169], v[26:29], v[50:53]
	v_mfma_f32_16x16x32_bf16 v[54:57], v[220:223], v[26:29], v[138:141]
	v_mfma_f32_16x16x32_bf16 v[58:61], v[232:235], v[26:29], v[162:165]
	v_mfma_f32_16x16x32_bf16 v[50:53], v[146:149], v[26:29], v[14:17]
	s_waitcnt lgkmcnt(1)
	v_mfma_f32_16x16x32_bf16 v[46:49], v[166:169], v[22:25], v[142:145]
	ds_read_b128 v[138:141], v183 offset:14336
	v_mfma_f32_16x16x32_bf16 v[38:41], v[220:223], v[22:25], v[212:215]
	v_mfma_f32_16x16x32_bf16 v[42:45], v[232:235], v[22:25], v[216:219]
	v_mfma_f32_16x16x32_bf16 v[34:37], v[146:149], v[22:25], v[10:13]
	s_waitcnt lgkmcnt(1)
	v_mfma_f32_16x16x32_bf16 v[30:33], v[166:169], v[18:21], v[224:227]
	v_mfma_f32_16x16x32_bf16 v[22:25], v[220:223], v[18:21], v[228:231]
	v_mfma_f32_16x16x32_bf16 v[26:29], v[232:235], v[18:21], v[184:187]
	v_mfma_f32_16x16x32_bf16 v[18:21], v[146:149], v[18:21], v[6:9]
	s_waitcnt lgkmcnt(0)
	v_mfma_f32_16x16x32_bf16 v[14:17], v[166:169], v[138:141], v[236:239]
	v_mfma_f32_16x16x32_bf16 v[6:9], v[220:223], v[138:141], v[134:137]
	v_mfma_f32_16x16x32_bf16 v[10:13], v[232:235], v[138:141], v[130:133]
	v_mfma_f32_16x16x32_bf16 v[2:5], v[146:149], v[138:141], v[2:5]
	s_waitcnt lgkmcnt(0)
	s_barrier
	s_and_saveexec_b64 s[2:3], s[0:1]
	s_cbranch_execz .LBB0_1467
	global_load_dword v130, v173, s[6:7] sc1
	s_waitcnt vmcnt(0)
	v_cmp_ne_u32_e32 vcc, 0, v130
	s_cbranch_vccnz .LBB0_1466
	s_mov_b32 s84, 1
	s_branch .LBB0_1451

.Lrot_mh:
	ds_read_b64_tr_b16 v[212:213], v236
	ds_read_b64_tr_b16 v[214:215], v236 offset:2048
	ds_read_b64_tr_b16 v[216:217], v240
	ds_read_b64_tr_b16 v[218:219], v240 offset:2048
	ds_read_b128 v[162:165], v237
	ds_read_b128 v[166:169], v237 offset:2048
	ds_read_b64_tr_b16 v[220:221], v242
	ds_read_b64_tr_b16 v[222:223], v242 offset:2048
	ds_read_b64_tr_b16 v[224:225], v244
	ds_read_b64_tr_b16 v[226:227], v244 offset:2048
	s_waitcnt lgkmcnt(5)
	v_mfma_f32_16x16x32_bf16 v[62:65], v[212:215], v[162:165], v[62:65]
	ds_read_b128 v[228:231], v237 offset:4096
	s_and_b32 s59, s34, 0x8000
	s_add_i32 s73, s33, s39
	v_mfma_f32_16x16x32_bf16 v[58:61], v[216:219], v[162:165], v[58:61]
	s_mov_b32 s74, m0
	s_mov_b32 m0, s73
	s_nop 0
	global_load_lds_dwordx4 v208, s[18:19]
	s_mov_b32 m0, s74
	s_waitcnt lgkmcnt(3)
	v_mfma_f32_16x16x32_bf16 v[54:57], v[220:223], v[162:165], v[54:57]
	s_waitcnt lgkmcnt(1)
	v_mfma_f32_16x16x32_bf16 v[42:45], v[224:227], v[162:165], v[42:45]
	v_mfma_f32_16x16x32_bf16 v[50:53], v[212:215], v[166:169], v[50:53]
	ds_read_b128 v[162:165], v237 offset:6144
	s_add_i32 s74, s73, 0x2000
	s_mov_b32 s75, m0
	s_mov_b32 m0, s74
	s_nop 0
	global_load_lds_dwordx4 v209, s[18:19]
	s_mov_b32 m0, s75
	v_mfma_f32_16x16x32_bf16 v[46:49], v[216:219], v[166:169], v[46:49]
	v_mfma_f32_16x16x32_bf16 v[38:41], v[220:223], v[166:169], v[38:41]
	v_mfma_f32_16x16x32_bf16 v[34:37], v[224:227], v[166:169], v[34:37]
	s_waitcnt lgkmcnt(1)
	v_mfma_f32_16x16x32_bf16 v[66:69], v[212:215], v[228:231], v[66:69]
	ds_read_b128 v[166:169], v237 offset:8192
	s_add_i32 s74, s73, 0x4000
	s_mov_b32 s75, m0
	s_mov_b32 m0, s74
	s_nop 0
	global_load_lds_dwordx4 v210, s[18:19]
	s_mov_b32 m0, s75
	v_mfma_f32_16x16x32_bf16 v[70:73], v[216:219], v[228:231], v[70:73]
	v_mfma_f32_16x16x32_bf16 v[74:77], v[220:223], v[228:231], v[74:77]
	v_mfma_f32_16x16x32_bf16 v[78:81], v[224:227], v[228:231], v[78:81]
	s_waitcnt lgkmcnt(1)
	v_mfma_f32_16x16x32_bf16 v[82:85], v[212:215], v[162:165], v[82:85]
	ds_read_b128 v[228:231], v237 offset:10240
	s_addk_i32 s73, 0x6000
	s_mov_b32 s74, m0
	s_mov_b32 m0, s73
	s_nop 0
	global_load_lds_dwordx4 v211, s[18:19]
	s_mov_b32 m0, s74
	v_mfma_f32_16x16x32_bf16 v[86:89], v[216:219], v[162:165], v[86:89]
	v_mfma_f32_16x16x32_bf16 v[90:93], v[220:223], v[162:165], v[90:93]
	v_mfma_f32_16x16x32_bf16 v[94:97], v[224:227], v[162:165], v[94:97]
	ds_read_b128 v[232:235], v237 offset:12288
	ds_read_b64_tr_b16 v[162:163], v236 offset:16384
	ds_read_b64_tr_b16 v[164:165], v236 offset:18432
	s_waitcnt lgkmcnt(4)
	v_mfma_f32_16x16x32_bf16 v[98:101], v[212:215], v[166:169], v[98:101]
	v_mfma_f32_16x16x32_bf16 v[102:105], v[216:219], v[166:169], v[102:105]
	v_mfma_f32_16x16x32_bf16 v[106:109], v[220:223], v[166:169], v[106:109]
	v_mfma_f32_16x16x32_bf16 v[110:113], v[224:227], v[166:169], v[110:113]
	ds_read_b128 v[236:239], v237 offset:14336
	ds_read_b64_tr_b16 v[166:167], v240 offset:16384
	ds_read_b64_tr_b16 v[168:169], v240 offset:18432
	s_waitcnt lgkmcnt(6)
	v_mfma_f32_16x16x32_bf16 v[114:117], v[212:215], v[228:231], v[114:117]
	v_mfma_f32_16x16x32_bf16 v[118:121], v[216:219], v[228:231], v[118:121]
	v_mfma_f32_16x16x32_bf16 v[122:125], v[220:223], v[228:231], v[122:125]
	v_mfma_f32_16x16x32_bf16 v[126:129], v[224:227], v[228:231], v[126:129]
	v_add_u32_e32 v245, s41, v188
	ds_read_b128 v[228:231], v245
	ds_read_b64_tr_b16 v[240:241], v242 offset:16384
	ds_read_b64_tr_b16 v[242:243], v242 offset:18432
	s_waitcnt lgkmcnt(8)
	v_mfma_f32_16x16x32_bf16 v[130:133], v[212:215], v[232:235], v[130:133]
	v_mfma_f32_16x16x32_bf16 v[134:137], v[216:219], v[232:235], v[134:137]
	v_mfma_f32_16x16x32_bf16 v[138:141], v[220:223], v[232:235], v[138:141]
	v_mfma_f32_16x16x32_bf16 v[142:145], v[224:227], v[232:235], v[142:145]
	s_waitcnt lgkmcnt(5)
	v_mfma_f32_16x16x32_bf16 v[146:149], v[212:215], v[236:239], v[146:149]
	v_mfma_f32_16x16x32_bf16 v[150:153], v[216:219], v[236:239], v[150:153]
	ds_read_b128 v[212:215], v245 offset:2048
	ds_read_b64_tr_b16 v[216:217], v244 offset:16384
	ds_read_b64_tr_b16 v[218:219], v244 offset:18432
	v_mfma_f32_16x16x32_bf16 v[154:157], v[220:223], v[236:239], v[154:157]
	v_mfma_f32_16x16x32_bf16 v[158:161], v[224:227], v[236:239], v[158:161]
	ds_read_b128 v[220:223], v245 offset:4096
	s_waitcnt lgkmcnt(6)
	v_mfma_f32_16x16x32_bf16 v[62:65], v[162:165], v[228:231], v[62:65]
	s_add_u32 s41, s37, s2
	s_waitcnt vmcnt(11)
	v_add_u32_e32 v232, s59, v189
	v_mfma_f32_16x16x32_bf16 v[58:61], v[166:169], v[228:231], v[58:61]
	s_addc_u32 s59, s38, s3
	v_cvt_pk_bf16_f32 v30, v30, v31
	v_cvt_pk_bf16_f32 v31, v32, v33
	s_waitcnt lgkmcnt(4)
	v_mfma_f32_16x16x32_bf16 v[54:57], v[240:243], v[228:231], v[54:57]
	s_add_u32 s74, s41, 0x160000
	ds_write_b64 v232, v[30:31]
	s_addc_u32 s75, s59, 0
	s_waitcnt lgkmcnt(2)
	v_mfma_f32_16x16x32_bf16 v[42:45], v[216:219], v[228:231], v[42:45]
	global_load_dwordx4 v[30:33], v199, s[74:75]
	v_mfma_f32_16x16x32_bf16 v[50:53], v[162:165], v[212:215], v[50:53]
	ds_read_b128 v[224:227], v245 offset:6144
	s_waitcnt vmcnt(11)
	s_add_u32 s74, s41, 0x18c000
	v_mfma_f32_16x16x32_bf16 v[46:49], v[166:169], v[212:215], v[46:49]
	v_cvt_pk_bf16_f32 v26, v26, v27
	v_cvt_pk_bf16_f32 v27, v28, v29
	ds_write_b64 v232, v[26:27] offset:8192
	v_mfma_f32_16x16x32_bf16 v[38:41], v[240:243], v[212:215], v[38:41]
	s_addc_u32 s75, s59, 0
	global_load_dwordx4 v[26:29], v199, s[74:75]
	v_mfma_f32_16x16x32_bf16 v[34:37], v[216:219], v[212:215], v[34:37]
	s_waitcnt lgkmcnt(3)
	v_mfma_f32_16x16x32_bf16 v[66:69], v[162:165], v[220:223], v[66:69]
	ds_read_b128 v[212:215], v245 offset:8192
	s_waitcnt vmcnt(11)
	s_add_u32 s74, s41, 0x1b8000
	v_mfma_f32_16x16x32_bf16 v[70:73], v[166:169], v[220:223], v[70:73]
	v_cvt_pk_bf16_f32 v22, v22, v23
	v_cvt_pk_bf16_f32 v23, v24, v25
	ds_write_b64 v232, v[22:23] offset:16384
	v_mfma_f32_16x16x32_bf16 v[74:77], v[240:243], v[220:223], v[74:77]
	s_addc_u32 s75, s59, 0
	global_load_dwordx4 v[22:25], v199, s[74:75]
	v_mfma_f32_16x16x32_bf16 v[78:81], v[216:219], v[220:223], v[78:81]
	s_waitcnt lgkmcnt(3)
	v_mfma_f32_16x16x32_bf16 v[82:85], v[162:165], v[224:227], v[82:85]
	ds_read_b128 v[220:223], v245 offset:10240
	s_waitcnt vmcnt(11)
	s_add_u32 s74, s41, 0x1e4000
	v_mfma_f32_16x16x32_bf16 v[86:89], v[166:169], v[224:227], v[86:89]
	v_cvt_pk_bf16_f32 v18, v18, v19
	v_cvt_pk_bf16_f32 v19, v20, v21
	ds_write_b64 v232, v[18:19] offset:24576
	v_mfma_f32_16x16x32_bf16 v[90:93], v[240:243], v[224:227], v[90:93]
	s_addc_u32 s75, s59, 0
	global_load_dwordx4 v[18:21], v199, s[74:75]
	v_mfma_f32_16x16x32_bf16 v[94:97], v[216:219], v[224:227], v[94:97]
	ds_read_b128 v[224:227], v245 offset:12288
	s_waitcnt lgkmcnt(4)
	v_mfma_f32_16x16x32_bf16 v[98:101], v[162:165], v[212:215], v[98:101]
	s_add_u32 s41, s35, s2
	s_waitcnt vmcnt(11)
	s_addc_u32 s59, s36, s3
	v_mfma_f32_16x16x32_bf16 v[102:105], v[166:169], v[212:215], v[102:105]
	v_cvt_pk_bf16_f32 v14, v14, v15
	v_cvt_pk_bf16_f32 v15, v16, v17
	s_add_u32 s74, s41, 0x160000
	v_mfma_f32_16x16x32_bf16 v[106:109], v[240:243], v[212:215], v[106:109]
	ds_write_b64 v232, v[14:15] offset:256
	s_addc_u32 s75, s59, 0
	global_load_dwordx4 v[14:17], v199, s[74:75]
	v_mfma_f32_16x16x32_bf16 v[110:113], v[216:219], v[212:215], v[110:113]
	s_waitcnt lgkmcnt(3)
	v_mfma_f32_16x16x32_bf16 v[114:117], v[162:165], v[220:223], v[114:117]
	ds_read_b128 v[212:215], v245 offset:14336
	s_waitcnt vmcnt(11)
	s_add_u32 s74, s41, 0x18c000
	v_mfma_f32_16x16x32_bf16 v[118:121], v[166:169], v[220:223], v[118:121]
	v_cvt_pk_bf16_f32 v10, v10, v11
	v_cvt_pk_bf16_f32 v11, v12, v13
	ds_write_b64 v232, v[10:11] offset:8448
	v_mfma_f32_16x16x32_bf16 v[122:125], v[240:243], v[220:223], v[122:125]
	s_addc_u32 s75, s59, 0
	global_load_dwordx4 v[10:13], v199, s[74:75]
	v_mfma_f32_16x16x32_bf16 v[126:129], v[216:219], v[220:223], v[126:129]
	s_waitcnt lgkmcnt(3)
	v_mfma_f32_16x16x32_bf16 v[130:133], v[162:165], v[224:227], v[130:133]
	s_waitcnt vmcnt(11)
	s_add_u32 s74, s41, 0x1b8000
	v_cvt_pk_bf16_f32 v6, v6, v7
	v_mfma_f32_16x16x32_bf16 v[134:137], v[166:169], v[224:227], v[134:137]
	v_cvt_pk_bf16_f32 v7, v8, v9
	ds_write_b64 v232, v[6:7] offset:16640
	s_addc_u32 s75, s59, 0
	v_mfma_f32_16x16x32_bf16 v[138:141], v[240:243], v[224:227], v[138:141]
	global_load_dwordx4 v[6:9], v199, s[74:75]
	v_mfma_f32_16x16x32_bf16 v[142:145], v[216:219], v[224:227], v[142:145]
	s_waitcnt lgkmcnt(2)
	v_mfma_f32_16x16x32_bf16 v[146:149], v[162:165], v[212:215], v[146:149]
	s_waitcnt vmcnt(11)
	s_add_u32 s74, s41, 0x1e4000
	v_cvt_pk_bf16_f32 v2, v2, v3
	v_mfma_f32_16x16x32_bf16 v[150:153], v[166:169], v[212:215], v[150:153]
	v_cvt_pk_bf16_f32 v3, v4, v5
	ds_write_b64 v232, v[2:3] offset:24832
	s_addc_u32 s75, s59, 0
	v_mfma_f32_16x16x32_bf16 v[154:157], v[240:243], v[212:215], v[154:157]
	global_load_dwordx4 v[2:5], v199, s[74:75]
	v_mfma_f32_16x16x32_bf16 v[158:161], v[216:219], v[212:215], v[158:161]
	s_add_i32 s41, s40, 0x8000
	s_cmp_lg_u32 s40, 0x10000
	s_cselect_b32 s40, s41, 0
	s_add_i32 s41, s39, 0x8000
	s_cmp_lg_u32 s39, 0x10000
	s_cselect_b32 s39, s41, 0
	s_add_u32 s2, s2, 0xb0000
	s_addc_u32 s3, s3, 0
	s_add_i32 s34, s34, 0x8000
	v_add_u32_e32 v211, 0x80, v211
	v_add_u32_e32 v210, 0x80, v210
	v_add_u32_e32 v209, 0x80, v209
	v_add_u32_e32 v208, 0x80, v208
	s_add_i32 s59, s34, 0xffff8000
	s_and_b32 s59, s59, 0x8000
	s_add_i32 s59, s59, 0
	s_add_i32 s41, s40, 0
	s_add_i32 s59, s59, 0x18000
	v_add_u32_e32 v236, s59, v184
	v_add_u32_e32 v237, s41, v187
	v_add_u32_e32 v242, s59, v181
	v_add_u32_e32 v244, s59, v172
	v_add_u32_e32 v240, s59, v183
	s_waitcnt lgkmcnt(0)
	s_barrier
	s_cmp_lg_u32 s2, 0x840000
	s_cbranch_scc1 .Lrot_mh
	v_add_u32_e32 v189, s52, v184
	v_add_u32_e32 v187, 0, v187
	v_add_u32_e32 v238, s52, v181
	v_add_u32_e32 v240, s52, v172
	v_add_u32_e32 v234, s52, v183
	ds_read_b64_tr_b16 v[162:163], v189
	ds_read_b64_tr_b16 v[164:165], v189 offset:2048
	ds_read_b64_tr_b16 v[166:167], v234
	ds_read_b64_tr_b16 v[168:169], v234 offset:2048
	ds_read_b128 v[208:211], v187
	ds_read_b128 v[212:215], v187 offset:2048
	ds_read_b64_tr_b16 v[216:217], v238
	ds_read_b64_tr_b16 v[218:219], v238 offset:2048
	ds_read_b64_tr_b16 v[220:221], v240
	ds_read_b64_tr_b16 v[222:223], v240 offset:2048
	ds_read_b128 v[224:227], v187 offset:4096
	s_waitcnt lgkmcnt(6)
	v_mfma_f32_16x16x32_bf16 v[62:65], v[162:165], v[208:211], v[62:65]
	v_mfma_f32_16x16x32_bf16 v[58:61], v[166:169], v[208:211], v[58:61]
	s_waitcnt lgkmcnt(3)
	v_mfma_f32_16x16x32_bf16 v[54:57], v[216:219], v[208:211], v[54:57]
	s_waitcnt lgkmcnt(1)
	v_mfma_f32_16x16x32_bf16 v[42:45], v[220:223], v[208:211], v[42:45]
	ds_read_b128 v[208:211], v187 offset:6144
	v_mfma_f32_16x16x32_bf16 v[50:53], v[162:165], v[212:215], v[50:53]
	v_mfma_f32_16x16x32_bf16 v[46:49], v[166:169], v[212:215], v[46:49]
	v_mfma_f32_16x16x32_bf16 v[38:41], v[216:219], v[212:215], v[38:41]
	v_mfma_f32_16x16x32_bf16 v[34:37], v[220:223], v[212:215], v[34:37]
	ds_read_b128 v[212:215], v187 offset:8192
	s_waitcnt lgkmcnt(2)
	v_mfma_f32_16x16x32_bf16 v[66:69], v[162:165], v[224:227], v[66:69]
	v_mfma_f32_16x16x32_bf16 v[70:73], v[166:169], v[224:227], v[70:73]
	v_mfma_f32_16x16x32_bf16 v[74:77], v[216:219], v[224:227], v[74:77]
	v_mfma_f32_16x16x32_bf16 v[78:81], v[220:223], v[224:227], v[78:81]
	ds_read_b128 v[224:227], v187 offset:10240
	s_waitcnt lgkmcnt(2)
	v_mfma_f32_16x16x32_bf16 v[82:85], v[162:165], v[208:211], v[82:85]
	v_mfma_f32_16x16x32_bf16 v[86:89], v[166:169], v[208:211], v[86:89]
	v_mfma_f32_16x16x32_bf16 v[90:93], v[216:219], v[208:211], v[90:93]
	v_mfma_f32_16x16x32_bf16 v[94:97], v[220:223], v[208:211], v[94:97]
	ds_read_b128 v[208:211], v187 offset:12288
	ds_read_b64_tr_b16 v[228:229], v189 offset:16384
	ds_read_b64_tr_b16 v[230:231], v189 offset:18432
	s_waitcnt lgkmcnt(4)
	v_mfma_f32_16x16x32_bf16 v[98:101], v[162:165], v[212:215], v[98:101]
	v_mfma_f32_16x16x32_bf16 v[102:105], v[166:169], v[212:215], v[102:105]
	v_mfma_f32_16x16x32_bf16 v[106:109], v[216:219], v[212:215], v[106:109]
	v_mfma_f32_16x16x32_bf16 v[110:113], v[220:223], v[212:215], v[110:113]
	ds_read_b128 v[212:215], v187 offset:14336
	ds_read_b64_tr_b16 v[232:233], v234 offset:16384
	ds_read_b64_tr_b16 v[234:235], v234 offset:18432
	s_waitcnt lgkmcnt(6)
	v_mfma_f32_16x16x32_bf16 v[114:117], v[162:165], v[224:227], v[114:117]
	v_mfma_f32_16x16x32_bf16 v[118:121], v[166:169], v[224:227], v[118:121]
	v_mfma_f32_16x16x32_bf16 v[122:125], v[216:219], v[224:227], v[122:125]
	v_mfma_f32_16x16x32_bf16 v[126:129], v[220:223], v[224:227], v[126:129]
	v_add_u32_e32 v188, 0, v188
	ds_read_b128 v[224:227], v188
	ds_read_b64_tr_b16 v[236:237], v238 offset:16384
	ds_read_b64_tr_b16 v[238:239], v238 offset:18432
	s_waitcnt lgkmcnt(8)
	v_mfma_f32_16x16x32_bf16 v[130:133], v[162:165], v[208:211], v[130:133]
	v_mfma_f32_16x16x32_bf16 v[134:137], v[166:169], v[208:211], v[134:137]
	v_mfma_f32_16x16x32_bf16 v[138:141], v[216:219], v[208:211], v[138:141]
	v_mfma_f32_16x16x32_bf16 v[142:145], v[220:223], v[208:211], v[142:145]
	s_waitcnt lgkmcnt(5)
	v_mfma_f32_16x16x32_bf16 v[146:149], v[162:165], v[212:215], v[146:149]
	v_mfma_f32_16x16x32_bf16 v[150:153], v[166:169], v[212:215], v[150:153]
	ds_read_b128 v[162:165], v188 offset:2048
	ds_read_b64_tr_b16 v[166:167], v240 offset:16384
	ds_read_b64_tr_b16 v[168:169], v240 offset:18432
	v_mfma_f32_16x16x32_bf16 v[154:157], v[216:219], v[212:215], v[154:157]
	v_mfma_f32_16x16x32_bf16 v[158:161], v[220:223], v[212:215], v[158:161]
	ds_read_b128 v[208:211], v188 offset:4096
	s_waitcnt vmcnt(7)
	v_add_u32_e32 v186, s56, v186
	v_cvt_pk_bf16_f32 v30, v30, v31
	v_cvt_pk_bf16_f32 v31, v32, v33
	s_waitcnt lgkmcnt(6)
	v_mfma_f32_16x16x32_bf16 v[62:65], v[228:231], v[224:227], v[62:65]
	ds_write_b64 v186, v[30:31]
	v_mfma_f32_16x16x32_bf16 v[58:61], v[232:235], v[224:227], v[58:61]
	s_waitcnt lgkmcnt(5)
	v_mfma_f32_16x16x32_bf16 v[54:57], v[236:239], v[224:227], v[54:57]
	s_waitcnt lgkmcnt(2)
	v_mfma_f32_16x16x32_bf16 v[30:33], v[166:169], v[224:227], v[42:45]
	v_mfma_f32_16x16x32_bf16 v[42:45], v[228:231], v[162:165], v[50:53]
	s_nop 2
	ds_read_b128 v[50:53], v188 offset:6144
	s_waitcnt vmcnt(6)
	v_mfma_f32_16x16x32_bf16 v[46:49], v[232:235], v[162:165], v[46:49]
	v_cvt_pk_bf16_f32 v26, v26, v27
	v_cvt_pk_bf16_f32 v27, v28, v29
	ds_write_b64 v186, v[26:27] offset:8192
	v_mfma_f32_16x16x32_bf16 v[38:41], v[236:239], v[162:165], v[38:41]
	v_mfma_f32_16x16x32_bf16 v[26:29], v[166:169], v[162:165], v[34:37]
	s_waitcnt lgkmcnt(3)
	v_mfma_f32_16x16x32_bf16 v[34:37], v[228:231], v[208:211], v[66:69]
	v_mfma_f32_16x16x32_bf16 v[66:69], v[232:235], v[208:211], v[70:73]
	s_nop 2
	ds_read_b128 v[70:73], v188 offset:8192
	s_waitcnt vmcnt(5)
	v_mfma_f32_16x16x32_bf16 v[74:77], v[236:239], v[208:211], v[74:77]
	v_cvt_pk_bf16_f32 v22, v22, v23
	v_cvt_pk_bf16_f32 v23, v24, v25
	ds_write_b64 v186, v[22:23] offset:16384
	v_mfma_f32_16x16x32_bf16 v[22:25], v[166:169], v[208:211], v[78:81]
	s_waitcnt lgkmcnt(3)
	v_mfma_f32_16x16x32_bf16 v[78:81], v[228:231], v[50:53], v[82:85]
	v_mfma_f32_16x16x32_bf16 v[82:85], v[232:235], v[50:53], v[86:89]
	s_nop 2
	ds_read_b128 v[86:89], v188 offset:10240
	s_waitcnt vmcnt(4)
	v_mfma_f32_16x16x32_bf16 v[90:93], v[236:239], v[50:53], v[90:93]
	v_cvt_pk_bf16_f32 v18, v18, v19
	v_cvt_pk_bf16_f32 v19, v20, v21
	ds_write_b64 v186, v[18:19] offset:24576
	v_mfma_f32_16x16x32_bf16 v[18:21], v[166:169], v[50:53], v[94:97]
	s_waitcnt lgkmcnt(3)
	v_mfma_f32_16x16x32_bf16 v[50:53], v[228:231], v[70:73], v[98:101]
	v_add_u32_e32 v162, s56, v185
	s_nop 1
	ds_read_b128 v[98:101], v188 offset:12288
	s_waitcnt vmcnt(3)
	v_mfma_f32_16x16x32_bf16 v[94:97], v[232:235], v[70:73], v[102:105]
	v_cvt_pk_bf16_f32 v14, v14, v15
	v_cvt_pk_bf16_f32 v15, v16, v17
	ds_write_b64 v162, v[14:15]
	v_mfma_f32_16x16x32_bf16 v[102:105], v[236:239], v[70:73], v[106:109]
	v_mfma_f32_16x16x32_bf16 v[14:17], v[166:169], v[70:73], v[110:113]
	s_nop 2
	ds_read_b128 v[110:113], v188 offset:14336
	s_waitcnt vmcnt(2)
	s_waitcnt lgkmcnt(4)
	v_mfma_f32_16x16x32_bf16 v[70:73], v[228:231], v[86:89], v[114:117]
	v_cvt_pk_bf16_f32 v10, v10, v11
	v_cvt_pk_bf16_f32 v11, v12, v13
	ds_write_b64 v162, v[10:11] offset:8192
	v_mfma_f32_16x16x32_bf16 v[106:109], v[232:235], v[86:89], v[118:121]
	v_mfma_f32_16x16x32_bf16 v[114:117], v[236:239], v[86:89], v[122:125]
	v_mfma_f32_16x16x32_bf16 v[10:13], v[166:169], v[86:89], v[126:129]
	s_waitcnt vmcnt(1)
	s_waitcnt lgkmcnt(3)
	v_mfma_f32_16x16x32_bf16 v[86:89], v[228:231], v[98:101], v[130:133]
	v_cvt_pk_bf16_f32 v6, v6, v7
	v_cvt_pk_bf16_f32 v7, v8, v9
	ds_write_b64 v162, v[6:7] offset:16384
	v_mfma_f32_16x16x32_bf16 v[118:121], v[232:235], v[98:101], v[134:137]
	v_mfma_f32_16x16x32_bf16 v[122:125], v[236:239], v[98:101], v[138:141]
	v_mfma_f32_16x16x32_bf16 v[6:9], v[166:169], v[98:101], v[142:145]
	s_waitcnt vmcnt(0)
	s_waitcnt lgkmcnt(2)
	v_mfma_f32_16x16x32_bf16 v[98:101], v[228:231], v[110:113], v[146:149]
	v_cvt_pk_bf16_f32 v2, v2, v3
	v_cvt_pk_bf16_f32 v3, v4, v5
	ds_write_b64 v162, v[2:3] offset:24576
	v_mfma_f32_16x16x32_bf16 v[126:129], v[232:235], v[110:113], v[150:153]
	v_mfma_f32_16x16x32_bf16 v[130:133], v[236:239], v[110:113], v[154:157]
	v_mfma_f32_16x16x32_bf16 v[2:5], v[166:169], v[110:113], v[158:161]
	s_waitcnt lgkmcnt(0)
	s_barrier
	s_nop 1
	v_add_u32_e32 v160, s56, v184
	v_add_u32_e32 v164, s56, v183
	v_add_u32_e32 v168, s56, v181
	ds_read_b64_tr_b16 v[110:111], v160
	ds_read_b64_tr_b16 v[112:113], v160 offset:2048
	ds_read_b64_tr_b16 v[134:135], v164
	ds_read_b64_tr_b16 v[136:137], v164 offset:2048
	ds_read_b128 v[138:141], v187 offset:32768
	ds_read_b64_tr_b16 v[142:143], v168
	ds_read_b128 v[146:149], v187 offset:34816
	ds_read_b128 v[150:153], v187 offset:36864
	ds_read_b64_tr_b16 v[144:145], v168 offset:2048
	v_add_u32_e32 v172, s56, v172
	ds_read_b64_tr_b16 v[154:155], v172
	ds_read_b64_tr_b16 v[156:157], v172 offset:2048
	s_waitcnt lgkmcnt(6)
	v_mfma_f32_16x16x32_bf16 v[62:65], v[110:113], v[138:141], v[62:65]
	v_mfma_f32_16x16x32_bf16 v[58:61], v[134:137], v[138:141], v[58:61]
	s_waitcnt lgkmcnt(2)
	v_mfma_f32_16x16x32_bf16 v[54:57], v[142:145], v[138:141], v[54:57]
	s_waitcnt lgkmcnt(0)
	v_mfma_f32_16x16x32_bf16 v[30:33], v[154:157], v[138:141], v[30:33]
	ds_read_b128 v[138:141], v187 offset:38912
	v_mfma_f32_16x16x32_bf16 v[42:45], v[110:113], v[146:149], v[42:45]
	v_mfma_f32_16x16x32_bf16 v[46:49], v[134:137], v[146:149], v[46:49]
	v_mfma_f32_16x16x32_bf16 v[38:41], v[142:145], v[146:149], v[38:41]
	v_mfma_f32_16x16x32_bf16 v[26:29], v[154:157], v[146:149], v[26:29]
	ds_read_b128 v[146:149], v187 offset:40960
	v_mfma_f32_16x16x32_bf16 v[34:37], v[110:113], v[150:153], v[34:37]
	v_mfma_f32_16x16x32_bf16 v[66:69], v[134:137], v[150:153], v[66:69]
	v_mfma_f32_16x16x32_bf16 v[74:77], v[142:145], v[150:153], v[74:77]
	v_mfma_f32_16x16x32_bf16 v[22:25], v[154:157], v[150:153], v[22:25]
	ds_read_b128 v[150:153], v187 offset:43008
	s_waitcnt lgkmcnt(2)
	v_mfma_f32_16x16x32_bf16 v[78:81], v[110:113], v[138:141], v[78:81]
	v_mfma_f32_16x16x32_bf16 v[82:85], v[134:137], v[138:141], v[82:85]
	v_mfma_f32_16x16x32_bf16 v[90:93], v[142:145], v[138:141], v[90:93]
	v_mfma_f32_16x16x32_bf16 v[18:21], v[154:157], v[138:141], v[18:21]
	ds_read_b128 v[138:141], v187 offset:45056
	ds_read_b64_tr_b16 v[158:159], v160 offset:16384
	ds_read_b64_tr_b16 v[160:161], v160 offset:18432
	s_waitcnt lgkmcnt(4)
	v_mfma_f32_16x16x32_bf16 v[50:53], v[110:113], v[146:149], v[50:53]
	v_mfma_f32_16x16x32_bf16 v[94:97], v[134:137], v[146:149], v[94:97]
	v_mfma_f32_16x16x32_bf16 v[102:105], v[142:145], v[146:149], v[102:105]
	v_mfma_f32_16x16x32_bf16 v[14:17], v[154:157], v[146:149], v[14:17]
	ds_read_b128 v[146:149], v187 offset:47104
	ds_read_b64_tr_b16 v[162:163], v164 offset:16384
	ds_read_b64_tr_b16 v[164:165], v164 offset:18432
	s_waitcnt lgkmcnt(6)
	v_mfma_f32_16x16x32_bf16 v[70:73], v[110:113], v[150:153], v[70:73]
	v_mfma_f32_16x16x32_bf16 v[106:109], v[134:137], v[150:153], v[106:109]
	v_mfma_f32_16x16x32_bf16 v[114:117], v[142:145], v[150:153], v[114:117]
	v_mfma_f32_16x16x32_bf16 v[10:13], v[154:157], v[150:153], v[10:13]
	ds_read_b128 v[150:153], v188 offset:32768
	ds_read_b64_tr_b16 v[166:167], v168 offset:16384
	ds_read_b64_tr_b16 v[168:169], v168 offset:18432
	s_waitcnt lgkmcnt(8)
	v_mfma_f32_16x16x32_bf16 v[86:89], v[110:113], v[138:141], v[86:89]
	v_mfma_f32_16x16x32_bf16 v[118:121], v[134:137], v[138:141], v[118:121]
	v_mfma_f32_16x16x32_bf16 v[122:125], v[142:145], v[138:141], v[122:125]
	v_mfma_f32_16x16x32_bf16 v[6:9], v[154:157], v[138:141], v[6:9]
	s_waitcnt lgkmcnt(5)
	v_mfma_f32_16x16x32_bf16 v[98:101], v[110:113], v[146:149], v[98:101]
	v_mfma_f32_16x16x32_bf16 v[110:113], v[134:137], v[146:149], v[126:129]
	v_mfma_f32_16x16x32_bf16 v[126:129], v[142:145], v[146:149], v[130:133]
	s_nop 2
	ds_read_b128 v[130:133], v188 offset:34816
	ds_read_b64_tr_b16 v[134:135], v172 offset:16384
	ds_read_b64_tr_b16 v[136:137], v172 offset:18432
	v_mfma_f32_16x16x32_bf16 v[2:5], v[154:157], v[146:149], v[2:5]
	ds_read_b128 v[138:141], v188 offset:36864
	s_waitcnt lgkmcnt(6)
	v_mfma_f32_16x16x32_bf16 v[62:65], v[158:161], v[150:153], v[62:65]
	v_mfma_f32_16x16x32_bf16 v[58:61], v[162:165], v[150:153], v[58:61]
	s_waitcnt lgkmcnt(4)
	v_mfma_f32_16x16x32_bf16 v[54:57], v[166:169], v[150:153], v[54:57]
	s_waitcnt lgkmcnt(1)
	v_mfma_f32_16x16x32_bf16 v[30:33], v[134:137], v[150:153], v[30:33]
	ds_read_b128 v[142:145], v188 offset:38912
	v_mfma_f32_16x16x32_bf16 v[42:45], v[158:161], v[130:133], v[42:45]
	v_mfma_f32_16x16x32_bf16 v[46:49], v[162:165], v[130:133], v[46:49]
	v_mfma_f32_16x16x32_bf16 v[38:41], v[166:169], v[130:133], v[38:41]
	v_mfma_f32_16x16x32_bf16 v[26:29], v[134:137], v[130:133], v[26:29]
	ds_read_b128 v[130:133], v188 offset:40960
	s_waitcnt lgkmcnt(2)
	v_mfma_f32_16x16x32_bf16 v[34:37], v[158:161], v[138:141], v[34:37]
	v_mfma_f32_16x16x32_bf16 v[66:69], v[162:165], v[138:141], v[66:69]
	v_mfma_f32_16x16x32_bf16 v[74:77], v[166:169], v[138:141], v[74:77]
	v_mfma_f32_16x16x32_bf16 v[22:25], v[134:137], v[138:141], v[22:25]
	ds_read_b128 v[138:141], v188 offset:43008
	s_waitcnt lgkmcnt(2)
	v_mfma_f32_16x16x32_bf16 v[78:81], v[158:161], v[142:145], v[78:81]
	v_mfma_f32_16x16x32_bf16 v[82:85], v[162:165], v[142:145], v[82:85]
	v_mfma_f32_16x16x32_bf16 v[90:93], v[166:169], v[142:145], v[90:93]
	v_mfma_f32_16x16x32_bf16 v[18:21], v[134:137], v[142:145], v[18:21]
	ds_read_b128 v[142:145], v188 offset:45056
	s_waitcnt lgkmcnt(2)
	v_mfma_f32_16x16x32_bf16 v[50:53], v[158:161], v[130:133], v[50:53]
	v_mfma_f32_16x16x32_bf16 v[94:97], v[162:165], v[130:133], v[94:97]
	v_mfma_f32_16x16x32_bf16 v[102:105], v[166:169], v[130:133], v[102:105]
	v_mfma_f32_16x16x32_bf16 v[14:17], v[134:137], v[130:133], v[14:17]
	ds_read_b128 v[130:133], v188 offset:47104
	s_waitcnt lgkmcnt(2)
	v_mfma_f32_16x16x32_bf16 v[70:73], v[158:161], v[138:141], v[70:73]
	v_mfma_f32_16x16x32_bf16 v[106:109], v[162:165], v[138:141], v[106:109]
	v_mfma_f32_16x16x32_bf16 v[114:117], v[166:169], v[138:141], v[114:117]
	v_mfma_f32_16x16x32_bf16 v[10:13], v[134:137], v[138:141], v[10:13]
	s_waitcnt lgkmcnt(1)
	v_mfma_f32_16x16x32_bf16 v[86:89], v[158:161], v[142:145], v[86:89]
	v_mfma_f32_16x16x32_bf16 v[118:121], v[162:165], v[142:145], v[118:121]
	v_mfma_f32_16x16x32_bf16 v[122:125], v[166:169], v[142:145], v[122:125]
	v_mfma_f32_16x16x32_bf16 v[138:141], v[134:137], v[142:145], v[6:9]
	s_waitcnt lgkmcnt(0)
	v_mfma_f32_16x16x32_bf16 v[98:101], v[158:161], v[130:133], v[98:101]
	v_mfma_f32_16x16x32_bf16 v[6:9], v[162:165], v[130:133], v[110:113]
	v_mfma_f32_16x16x32_bf16 v[110:113], v[166:169], v[130:133], v[126:129]
	v_mfma_f32_16x16x32_bf16 v[2:5], v[134:137], v[130:133], v[2:5]
	s_nop 1
	v_mov_b32_e32 v126, v192
	v_mov_b32_e32 v127, v1
	s_waitcnt lgkmcnt(0)
	s_barrier
	s_add_i32 s5, s5, s29
	s_lshl_b32 s2, s4, 5
	v_add_u32_e32 v127, s5, v127
	s_or_b32 s2, s2, s28
	v_lshl_add_u32 v132, v126, 2, s2
	v_lshlrev_b32_e32 v126, 8, v127
	v_and_b32_e32 v172, 0xff00, v126
	v_and_b32_e32 v128, 0x7c, v132
	v_lshlrev_b32_e32 v133, 7, v127
	v_lshl_add_u64 v[126:127], s[30:31], 0, v[172:173]
	v_lshlrev_b32_e32 v172, 1, v128
	v_lshl_add_u64 v[128:129], v[126:127], 0, v[172:173]
	v_cvt_pk_bf16_f32 v62, v62, v63
	v_cvt_pk_bf16_f32 v63, v64, v65
	v_cvt_pk_bf16_f32 v54, v54, v55
	global_store_dwordx2 v[128:129], v[62:63], off sc1
	s_nop 1
	v_lshl_add_u64 v[130:131], v[128:129], 0, s[22:23]
	v_cvt_pk_bf16_f32 v55, v56, v57
	global_store_dwordx2 v[130:131], v[54:55], off sc1
	s_nop 1
	v_add_u32_e32 v54, 16, v132
	v_and_b32_e32 v54, 0x7c, v54
	v_lshlrev_b32_e32 v54, 1, v54
	v_mov_b32_e32 v55, v173
	v_lshl_add_u64 v[56:57], v[126:127], 0, v[54:55]
	v_cvt_pk_bf16_f32 v58, v58, v59
	v_cvt_pk_bf16_f32 v59, v60, v61
	v_cvt_pk_bf16_f32 v30, v30, v31
	global_store_dwordx2 v[56:57], v[58:59], off sc1
	s_nop 1
	v_lshl_add_u64 v[62:63], v[56:57], 0, s[22:23]
	v_cvt_pk_bf16_f32 v31, v32, v33
	global_store_dwordx2 v[62:63], v[30:31], off sc1
	s_nop 1
	v_add_u32_e32 v30, 0x800, v133
	v_and_b32_e32 v30, 0x7f80, v30
	v_lshlrev_b32_e32 v30, 1, v30
	v_mov_b32_e32 v31, v173
	v_lshl_add_u64 v[30:31], s[30:31], 0, v[30:31]
	v_lshl_add_u64 v[32:33], v[30:31], 0, v[172:173]
	v_cvt_pk_bf16_f32 v42, v42, v43
	v_cvt_pk_bf16_f32 v43, v44, v45
	global_store_dwordx2 v[32:33], v[42:43], off sc1
	s_nop 1
	v_lshl_add_u64 v[56:57], v[32:33], 0, s[22:23]
	v_cvt_pk_bf16_f32 v38, v38, v39
	v_cvt_pk_bf16_f32 v39, v40, v41
	global_store_dwordx2 v[56:57], v[38:39], off sc1
	s_nop 1
	v_lshl_add_u64 v[30:31], v[30:31], 0, v[54:55]
	v_cvt_pk_bf16_f32 v38, v46, v47
	v_cvt_pk_bf16_f32 v39, v48, v49
	v_cvt_pk_bf16_f32 v26, v26, v27
	global_store_dwordx2 v[30:31], v[38:39], off sc1
	s_nop 1
	v_lshl_add_u64 v[32:33], v[30:31], 0, s[22:23]
	v_cvt_pk_bf16_f32 v27, v28, v29
	global_store_dwordx2 v[32:33], v[26:27], off sc1
	s_nop 1
	v_add_u32_e32 v26, 0x1000, v133
	v_and_b32_e32 v26, 0x7f80, v26
	v_lshlrev_b32_e32 v26, 1, v26
	v_mov_b32_e32 v27, v173
	v_lshl_add_u64 v[26:27], s[30:31], 0, v[26:27]
	v_lshl_add_u64 v[28:29], v[26:27], 0, v[172:173]
	v_cvt_pk_bf16_f32 v32, v34, v35
	v_cvt_pk_bf16_f32 v33, v36, v37
	global_store_dwordx2 v[28:29], v[32:33], off sc1
	s_nop 1
	v_lshl_add_u64 v[30:31], v[28:29], 0, s[22:23]
	v_cvt_pk_bf16_f32 v34, v74, v75
	v_cvt_pk_bf16_f32 v35, v76, v77
	global_store_dwordx2 v[30:31], v[34:35], off sc1
	s_nop 1
	v_lshl_add_u64 v[26:27], v[26:27], 0, v[54:55]
	v_cvt_pk_bf16_f32 v30, v66, v67
	v_cvt_pk_bf16_f32 v31, v68, v69
	v_cvt_pk_bf16_f32 v22, v22, v23
	global_store_dwordx2 v[26:27], v[30:31], off sc1
	s_nop 1
	v_lshl_add_u64 v[28:29], v[26:27], 0, s[22:23]
	v_cvt_pk_bf16_f32 v23, v24, v25
	global_store_dwordx2 v[28:29], v[22:23], off sc1
	s_nop 1
	v_add_u32_e32 v22, 0x1800, v133
	v_and_b32_e32 v22, 0x7f80, v22
	v_lshlrev_b32_e32 v22, 1, v22
	v_mov_b32_e32 v23, v173
	v_lshl_add_u64 v[22:23], s[30:31], 0, v[22:23]
	v_lshl_add_u64 v[24:25], v[22:23], 0, v[172:173]
	v_cvt_pk_bf16_f32 v28, v78, v79
	v_cvt_pk_bf16_f32 v29, v80, v81
	global_store_dwordx2 v[24:25], v[28:29], off sc1
	s_nop 1
	v_lshl_add_u64 v[26:27], v[24:25], 0, s[22:23]
	v_cvt_pk_bf16_f32 v30, v90, v91
	v_cvt_pk_bf16_f32 v31, v92, v93
	global_store_dwordx2 v[26:27], v[30:31], off sc1
	s_nop 1
	v_lshl_add_u64 v[22:23], v[22:23], 0, v[54:55]
	v_cvt_pk_bf16_f32 v26, v82, v83
	v_cvt_pk_bf16_f32 v27, v84, v85
	v_cvt_pk_bf16_f32 v18, v18, v19
	global_store_dwordx2 v[22:23], v[26:27], off sc1
	s_nop 1
	v_lshl_add_u64 v[24:25], v[22:23], 0, s[22:23]
	v_cvt_pk_bf16_f32 v19, v20, v21
	global_store_dwordx2 v[24:25], v[18:19], off sc1
	s_nop 1
	v_add_u32_e32 v18, 0x2000, v133
	v_and_b32_e32 v18, 0x7f80, v18
	v_lshlrev_b32_e32 v18, 1, v18
	v_mov_b32_e32 v19, v173
	v_lshl_add_u64 v[18:19], s[30:31], 0, v[18:19]
	v_lshl_add_u64 v[20:21], v[18:19], 0, v[172:173]
	v_cvt_pk_bf16_f32 v24, v50, v51
	v_cvt_pk_bf16_f32 v25, v52, v53
	global_store_dwordx2 v[20:21], v[24:25], off sc1
	s_nop 1
	v_lshl_add_u64 v[22:23], v[20:21], 0, s[22:23]
	v_cvt_pk_bf16_f32 v26, v102, v103
	v_cvt_pk_bf16_f32 v27, v104, v105
	global_store_dwordx2 v[22:23], v[26:27], off sc1
	s_nop 1
	v_lshl_add_u64 v[18:19], v[18:19], 0, v[54:55]
	v_cvt_pk_bf16_f32 v22, v94, v95
	v_cvt_pk_bf16_f32 v23, v96, v97
	v_cvt_pk_bf16_f32 v14, v14, v15
	global_store_dwordx2 v[18:19], v[22:23], off sc1
	s_nop 1
	v_lshl_add_u64 v[20:21], v[18:19], 0, s[22:23]
	v_cvt_pk_bf16_f32 v15, v16, v17
	global_store_dwordx2 v[20:21], v[14:15], off sc1
	s_nop 1
	v_add_u32_e32 v14, 0x2800, v133
	v_and_b32_e32 v14, 0x7f80, v14
	v_lshlrev_b32_e32 v14, 1, v14
	v_mov_b32_e32 v15, v173
	v_lshl_add_u64 v[14:15], s[30:31], 0, v[14:15]
	v_lshl_add_u64 v[16:17], v[14:15], 0, v[172:173]
	v_cvt_pk_bf16_f32 v20, v70, v71
	v_cvt_pk_bf16_f32 v21, v72, v73
	global_store_dwordx2 v[16:17], v[20:21], off sc1
	s_nop 1
	v_lshl_add_u64 v[18:19], v[16:17], 0, s[22:23]
	v_cvt_pk_bf16_f32 v22, v114, v115
	v_cvt_pk_bf16_f32 v23, v116, v117
	global_store_dwordx2 v[18:19], v[22:23], off sc1
	s_nop 1
	v_lshl_add_u64 v[14:15], v[14:15], 0, v[54:55]
	v_cvt_pk_bf16_f32 v18, v106, v107
	v_cvt_pk_bf16_f32 v19, v108, v109
	v_cvt_pk_bf16_f32 v10, v10, v11
	global_store_dwordx2 v[14:15], v[18:19], off sc1
	s_nop 1
	v_lshl_add_u64 v[16:17], v[14:15], 0, s[22:23]
	v_cvt_pk_bf16_f32 v11, v12, v13
	global_store_dwordx2 v[16:17], v[10:11], off sc1
	s_nop 1
	v_add_u32_e32 v10, 0x3000, v133
	v_and_b32_e32 v10, 0x7f80, v10
	v_lshlrev_b32_e32 v10, 1, v10
	v_mov_b32_e32 v11, v173
	v_lshl_add_u64 v[10:11], s[30:31], 0, v[10:11]
	v_lshl_add_u64 v[12:13], v[10:11], 0, v[172:173]
	v_cvt_pk_bf16_f32 v16, v86, v87
	v_cvt_pk_bf16_f32 v17, v88, v89
	global_store_dwordx2 v[12:13], v[16:17], off sc1
	s_nop 1
	v_lshl_add_u64 v[14:15], v[12:13], 0, s[22:23]
	v_cvt_pk_bf16_f32 v18, v122, v123
	v_cvt_pk_bf16_f32 v19, v124, v125
	global_store_dwordx2 v[14:15], v[18:19], off sc1
	s_nop 1
	v_lshl_add_u64 v[10:11], v[10:11], 0, v[54:55]
	v_lshl_add_u64 v[12:13], v[10:11], 0, s[22:23]
	v_cvt_pk_bf16_f32 v14, v118, v119
	v_cvt_pk_bf16_f32 v15, v120, v121
	global_store_dwordx2 v[10:11], v[14:15], off sc1
	s_nop 1
	v_add_u32_e32 v10, 0x3800, v133
	v_and_b32_e32 v10, 0x7f80, v10
	v_lshlrev_b32_e32 v10, 1, v10
	v_mov_b32_e32 v11, v173
	v_cvt_pk_bf16_f32 v16, v138, v139
	v_cvt_pk_bf16_f32 v17, v140, v141
	global_store_dwordx2 v[12:13], v[16:17], off sc1
	s_nop 1
	v_lshl_add_u64 v[10:11], s[30:31], 0, v[10:11]
	v_lshl_add_u64 v[12:13], v[10:11], 0, v[172:173]
	v_cvt_pk_bf16_f32 v16, v98, v99
	v_cvt_pk_bf16_f32 v17, v100, v101
	global_store_dwordx2 v[12:13], v[16:17], off sc1
	s_nop 1
	v_lshl_add_u64 v[14:15], v[12:13], 0, s[22:23]
	v_cvt_pk_bf16_f32 v18, v110, v111
	v_cvt_pk_bf16_f32 v19, v112, v113
	global_store_dwordx2 v[14:15], v[18:19], off sc1
	s_nop 1
	v_lshl_add_u64 v[10:11], v[10:11], 0, v[54:55]
	v_cvt_pk_bf16_f32 v6, v6, v7
	v_cvt_pk_bf16_f32 v7, v8, v9
	global_store_dwordx2 v[10:11], v[6:7], off sc1
	s_nop 1
	v_lshl_add_u64 v[12:13], v[10:11], 0, s[22:23]
	v_cvt_pk_bf16_f32 v2, v2, v3
	v_cvt_pk_bf16_f32 v3, v4, v5
	global_store_dwordx2 v[12:13], v[2:3], off sc1
	s_nop 1
	s_waitcnt vmcnt(0)
	s_barrier
	s_and_saveexec_b64 s[2:3], s[0:1]
	s_cbranch_execz .LBB0_1419
	v_mov_b32_e32 v2, 1
	global_store_dword v173, v2, s[6:7] sc1
	s_branch .LBB0_1419
